# added s_waitcnt vmcnt(8) at the end of each K-loop load segment so LDS-DMA tiles staged by the lagging wave half are counted-complete before the leading half reads them (removes a timing dependence)
# speedup vs baseline: 1.0039x; 1.0039x over previous
; #define G_STAGE(bufoff, gbase, voff) do { _Pragma("unroll") for (int _i = 0; _i < 2; ++_i) \
;         __builtin_amdgcn_global_load_lds((const unsigned*)((const char*)(gbase) + (voff)[_i]), (LAS unsigned*)(lds + (bufoff) + ldsw + _i * 8192), 16, 0, 0); } while (0)
; #define G_LDA(dst, b, h) do { _Pragma("unroll") for (int m = 0; m < 4; ++m) G_LD8(dst[m], lds + G_SA(b, h) + aoff + m * 2048); } while (0)
; #define G_LDB(dst, b, h) do { _Pragma("unroll") for (int n = 0; n < 2; ++n) G_LD8(dst[n], lds + G_SB(b, h) + boff + n * 2048); } while (0)
; #define G_WAIT_V(n) asm volatile("s_waitcnt vmcnt(" #n ")" ::: "memory")
; #define G_WAIT_L(n) asm volatile("s_waitcnt lgkmcnt(" #n ")" ::: "memory")
; #define G_BAR __builtin_amdgcn_s_barrier()
; #define G_SCHED __builtin_amdgcn_sched_barrier(0)
;     __device__ __forceinline__ unsigned row_off(const Unit& u, int r, LAS unsigned char* lds) const { return (unsigned)((const LAS int*)(lds + LDS_STAGE + u.q * 4096))[r] * (unsigned)rowbytes; }
;     ...
;             const char* a11 = cur.a1 + (size_t)(t + 1) * kstep;
;             const char* a02 = last ? nxt.a0 : cur.a0 + (size_t)(t + 2) * kstep; const char* a12 = last ? nxt.a1 : cur.a1 + (size_t)(t + 2) * kstep;
;             const char* b02 = last ? nxt.b0 : cur.b0 + (size_t)(t + 2) * kstep; const char* b12 = last ? nxt.b1 : cur.b1 + (size_t)(t + 2) * kstep;
;             G_LDB(B0, 0, 0); G_LDB(B1, 0, 1); G_SCHED; G_LDA(At, 0, 0); G_STAGE(G_SA(1, 1), a11, vA1);
;             if constexpr (GATHER) { if (last) { int tz = tid; asm volatile("" : "+v"(tz));
; #pragma unroll
;                 for (int i = 0; i < 2; ++i) { int R, C; stage_rc(tz * 16 + i * 8192, R, C); gc0[i] = S.row_off(nxt, R, lds) + (unsigned)C * 2u; gc1[i] = S.row_off(nxt, 128 + R, lds) + (unsigned)C * 2u; } } }
;             G_WAIT_L(0); G_BAR; G_MMA(0, 0, At, B0); G_MMA(0, 1, At, B1); G_WAIT_V(8); G_BAR; G_SCHED;
;             G_LDA(At, 0, 1); G_STAGE(G_SB(0, 0), b02, voffB); G_STAGE(G_SB(0, 1), b12, voffB); G_STAGE(G_SA(0, 0), a02, vA0);
;             G_WAIT_L(0); G_BAR; G_MMA(1, 0, At, B0); G_MMA(1, 1, At, B1); G_WAIT_V(8); G_BAR; G_SCHED;
.LBB0_179:
	v_add_u32_e32 v144, s91, v163
	v_add_u32_e32 v170, s3, v163
	ds_read_b128 v[34:37], v144
	ds_read_b128 v[38:41], v144 offset:1024
	ds_read_b128 v[42:45], v144 offset:2048
	ds_read_b128 v[144:147], v144 offset:3072
	ds_read_b128 v[150:153], v170
	ds_read_b128 v[154:157], v170 offset:1024
	ds_read_b128 v[166:169], v170 offset:2048
	ds_read_b128 v[170:173], v170 offset:3072
	s_add_i32 s63, s59, 2
	s_add_u32 s73, s74, 0x80
	s_addc_u32 s76, s75, 0
	s_add_i32 s83, s91, s97
	s_add_i32 m0, s22, 0xc000
	s_add_i32 s82, s22, 0xe000
	s_add_i32 s89, s83, 0x2000
	s_cmp_eq_u32 s20, s59
	s_cselect_b32 s79, s65, s33
	s_cselect_b32 s78, s64, s19
	s_cselect_b32 s81, s69, s2
	s_cselect_b32 s80, s68, s0
	s_cselect_b32 s77, s67, s76
	s_cselect_b32 s76, s66, s73
	ds_read_b128 v[174:177], v164
	ds_read_b128 v[178:181], v164 offset:1024
	ds_read_b128 v[182:185], v164 offset:2048
	ds_read_b128 v[186:189], v164 offset:3072
	ds_read_b128 v[190:193], v164 offset:4096
	ds_read_b128 v[194:197], v164 offset:5120
	ds_read_b128 v[198:201], v164 offset:6144
	ds_read_b128 v[202:205], v164 offset:7168
	global_load_lds_dwordx4 v240, s[74:75]
	s_mov_b32 m0, s82
	s_nop 0
	global_load_lds_dwordx4 v242, s[74:75]
	s_waitcnt lgkmcnt(0)
	v_mov_b32_e32 v33, v149
	s_waitcnt vmcnt(8)
	s_barrier
	s_setprio 1
	s_waitcnt lgkmcnt(0)
	v_mfma_i32_16x16x64_i8 v[140:143], v[34:37], v[174:177], v[140:143]
	v_mfma_i32_16x16x64_i8 v[132:135], v[42:45], v[174:177], v[132:135]
	v_mfma_i32_16x16x64_i8 v[124:127], v[34:37], v[182:185], v[124:127]
	v_mfma_i32_16x16x64_i8 v[116:119], v[42:45], v[182:185], v[116:119]
	v_mfma_i32_16x16x64_i8 v[108:111], v[34:37], v[190:193], v[108:111]
	v_mfma_i32_16x16x64_i8 v[100:103], v[42:45], v[190:193], v[100:103]
	v_mfma_i32_16x16x64_i8 v[92:95], v[34:37], v[198:201], v[92:95]
	v_mfma_i32_16x16x64_i8 v[84:87], v[42:45], v[198:201], v[84:87]
	v_mfma_i32_16x16x64_i8 v[140:143], v[38:41], v[178:181], v[140:143]
	v_mfma_i32_16x16x64_i8 v[132:135], v[144:147], v[178:181], v[132:135]
	v_mfma_i32_16x16x64_i8 v[124:127], v[38:41], v[186:189], v[124:127]
	v_mfma_i32_16x16x64_i8 v[116:119], v[144:147], v[186:189], v[116:119]
	v_mfma_i32_16x16x64_i8 v[108:111], v[38:41], v[194:197], v[108:111]
	v_mfma_i32_16x16x64_i8 v[100:103], v[144:147], v[194:197], v[100:103]
	v_mfma_i32_16x16x64_i8 v[92:95], v[38:41], v[202:205], v[92:95]
	v_mfma_i32_16x16x64_i8 v[84:87], v[144:147], v[202:205], v[84:87]
	v_mfma_i32_16x16x64_i8 v[136:139], v[150:153], v[174:177], v[136:139]
	v_mfma_i32_16x16x64_i8 v[128:131], v[166:169], v[174:177], v[128:131]
	v_mfma_i32_16x16x64_i8 v[120:123], v[150:153], v[182:185], v[120:123]
	v_mfma_i32_16x16x64_i8 v[112:115], v[166:169], v[182:185], v[112:115]
	v_mfma_i32_16x16x64_i8 v[104:107], v[150:153], v[190:193], v[104:107]
	v_mfma_i32_16x16x64_i8 v[96:99], v[166:169], v[190:193], v[96:99]
	v_mfma_i32_16x16x64_i8 v[88:91], v[150:153], v[198:201], v[88:91]
	v_mfma_i32_16x16x64_i8 v[80:83], v[166:169], v[198:201], v[80:83]
	v_mfma_i32_16x16x64_i8 v[136:139], v[154:157], v[178:181], v[136:139]
	v_mfma_i32_16x16x64_i8 v[128:131], v[170:173], v[178:181], v[128:131]
	v_mfma_i32_16x16x64_i8 v[120:123], v[154:157], v[186:189], v[120:123]
	v_mfma_i32_16x16x64_i8 v[112:115], v[170:173], v[186:189], v[112:115]
	v_mfma_i32_16x16x64_i8 v[104:107], v[154:157], v[194:197], v[104:107]
	v_mfma_i32_16x16x64_i8 v[96:99], v[170:173], v[194:197], v[96:99]
	v_mfma_i32_16x16x64_i8 v[88:91], v[154:157], v[202:205], v[88:91]
	v_mfma_i32_16x16x64_i8 v[80:83], v[170:173], v[202:205], v[80:83]
	s_setprio 0
	s_waitcnt vmcnt(8)
	s_barrier
	s_mov_b32 m0, s83
	ds_read_b128 v[174:177], v164 offset:16384
	ds_read_b128 v[178:181], v164 offset:17408
	ds_read_b128 v[182:185], v164 offset:18432
	ds_read_b128 v[186:189], v164 offset:19456
	ds_read_b128 v[190:193], v164 offset:20480
	ds_read_b128 v[194:197], v164 offset:21504
	ds_read_b128 v[198:201], v164 offset:22528
	ds_read_b128 v[202:205], v164 offset:23552
	v_mov_b32_e32 v47, v149
	global_load_lds_dwordx4 v244, s[80:81]
	v_mov_b32_e32 v159, v149
	s_mov_b32 m0, s89
	v_lshl_add_u64 v[206:207], s[80:81], 0, v[244:245]
	v_lshl_add_u64 v[208:209], s[80:81], 0, v[246:247]
	global_load_lds_dwordx4 v246, s[80:81]
	s_cselect_b32 s81, s71, s6
	s_cselect_b32 s80, s70, s5
	s_add_i32 s59, s3, s97
	s_mov_b32 m0, s59
	v_lshl_add_u64 v[210:211], s[80:81], 0, v[244:245]
	global_load_lds_dwordx4 v244, s[80:81]
	s_add_i32 m0, s59, 0x2000
	v_lshl_add_u64 v[212:213], s[80:81], 0, v[246:247]
	global_load_lds_dwordx4 v246, s[80:81]
	s_mov_b32 m0, s22
	v_lshl_add_u64 v[158:159], s[78:79], 0, v[240:241]
	global_load_lds_dwordx4 v240, s[78:79]
	s_mov_b32 m0, s23
	v_lshl_add_u64 v[214:215], s[78:79], 0, v[242:243]
	global_load_lds_dwordx4 v242, s[78:79]
	s_waitcnt lgkmcnt(0)
	s_waitcnt vmcnt(8)
	s_barrier
; #define G_STAGE(bufoff, gbase, voff) do { _Pragma("unroll") for (int _i = 0; _i < 2; ++_i) \
;         __builtin_amdgcn_global_load_lds((const unsigned*)((const char*)(gbase) + (voff)[_i]), (LAS unsigned*)(lds + (bufoff) + ldsw + _i * 8192), 16, 0, 0); } while (0)
; #define G_LDA(dst, b, h) do { _Pragma("unroll") for (int m = 0; m < 4; ++m) G_LD8(dst[m], lds + G_SA(b, h) + aoff + m * 2048); } while (0)
; #define G_LDB(dst, b, h) do { _Pragma("unroll") for (int n = 0; n < 2; ++n) G_LD8(dst[n], lds + G_SB(b, h) + boff + n * 2048); } while (0)
; #define G_WAIT_V(n) asm volatile("s_waitcnt vmcnt(" #n ")" ::: "memory")
; #define G_WAIT_L(n) asm volatile("s_waitcnt lgkmcnt(" #n ")" ::: "memory")
; #define G_BAR __builtin_amdgcn_s_barrier()
; #define G_SCHED __builtin_amdgcn_sched_barrier(0)
;     ...
;             G_WAIT_L(0); G_BAR; G_MMA(1, 0, At, B0); G_MMA(1, 1, At, B1); G_WAIT_V(8); G_BAR; G_SCHED;
;             G_LDB(B0, 1, 0); G_LDB(B1, 1, 1); G_SCHED; G_LDA(At, 1, 0); G_STAGE(G_SA(0, 1), a12, vA1);
;             G_WAIT_L(0); G_BAR; G_MMA(0, 0, At, B0); G_MMA(0, 1, At, B1); G_WAIT_V(8); G_BAR; G_SCHED;
	s_setprio 1
	s_waitcnt lgkmcnt(0)
	v_mfma_i32_16x16x64_i8 v[76:79], v[34:37], v[174:177], v[76:79]
	v_mfma_i32_16x16x64_i8 v[68:71], v[42:45], v[174:177], v[68:71]
	v_mfma_i32_16x16x64_i8 v[60:63], v[34:37], v[182:185], v[60:63]
	v_mfma_i32_16x16x64_i8 v[52:55], v[42:45], v[182:185], v[52:55]
	v_mfma_i32_16x16x64_i8 v[28:31], v[34:37], v[190:193], v[28:31]
	v_mfma_i32_16x16x64_i8 v[20:23], v[42:45], v[190:193], v[20:23]
	v_mfma_i32_16x16x64_i8 v[12:15], v[34:37], v[198:201], v[12:15]
	v_mfma_i32_16x16x64_i8 v[4:7], v[42:45], v[198:201], v[4:7]
	v_mfma_i32_16x16x64_i8 v[76:79], v[38:41], v[178:181], v[76:79]
	v_mfma_i32_16x16x64_i8 v[68:71], v[144:147], v[178:181], v[68:71]
	v_mfma_i32_16x16x64_i8 v[60:63], v[38:41], v[186:189], v[60:63]
	v_mfma_i32_16x16x64_i8 v[52:55], v[144:147], v[186:189], v[52:55]
	v_mfma_i32_16x16x64_i8 v[28:31], v[38:41], v[194:197], v[28:31]
	v_mfma_i32_16x16x64_i8 v[20:23], v[144:147], v[194:197], v[20:23]
	v_mfma_i32_16x16x64_i8 v[12:15], v[38:41], v[202:205], v[12:15]
	v_mfma_i32_16x16x64_i8 v[4:7], v[144:147], v[202:205], v[4:7]
	v_mfma_i32_16x16x64_i8 v[46:49], v[166:169], v[182:185], v[48:51]
	v_mfma_i32_16x16x64_i8 v[24:27], v[150:153], v[190:193], v[24:27]
	v_mfma_i32_16x16x64_i8 v[16:19], v[166:169], v[190:193], v[16:19]
	v_mfma_i32_16x16x64_i8 v[8:11], v[150:153], v[198:201], v[8:11]
	v_mfma_i32_16x16x64_i8 v[0:3], v[166:169], v[198:201], v[0:3]
	v_mfma_i32_16x16x64_i8 v[34:37], v[150:153], v[174:177], v[72:75]
	v_mfma_i32_16x16x64_i8 v[38:41], v[166:169], v[174:177], v[64:67]
	v_mfma_i32_16x16x64_i8 v[42:45], v[150:153], v[182:185], v[56:59]
	v_mfma_i32_16x16x64_i8 v[46:49], v[170:173], v[186:189], v[46:49]
	v_mfma_i32_16x16x64_i8 v[24:27], v[154:157], v[194:197], v[24:27]
	v_mfma_i32_16x16x64_i8 v[16:19], v[170:173], v[194:197], v[16:19]
	v_mfma_i32_16x16x64_i8 v[8:11], v[154:157], v[202:205], v[8:11]
	v_mfma_i32_16x16x64_i8 v[0:3], v[170:173], v[202:205], v[0:3]
	v_mfma_i32_16x16x64_i8 v[34:37], v[154:157], v[178:181], v[34:37]
	v_mfma_i32_16x16x64_i8 v[38:41], v[170:173], v[178:181], v[38:41]
	v_mfma_i32_16x16x64_i8 v[42:45], v[154:157], v[186:189], v[42:45]
	s_setprio 0
	s_waitcnt vmcnt(8)
	s_barrier
	s_add_i32 s59, 0, 0x18000
	v_add_u32_e32 v33, s59, v163
	s_add_i32 s73, 0, 0x1c000
	ds_read_b128 v[56:59], v33
	ds_read_b128 v[64:67], v33 offset:1024
	ds_read_b128 v[72:75], v33 offset:2048
	ds_read_b128 v[144:147], v33 offset:3072
	v_add_u32_e32 v33, s73, v163
	ds_read_b128 v[150:153], v33
	ds_read_b128 v[154:157], v33 offset:1024
	ds_read_b128 v[166:169], v33 offset:2048
	ds_read_b128 v[170:173], v33 offset:3072
	s_mov_b32 m0, s55
	ds_read_b128 v[174:177], v164 offset:32768
	ds_read_b128 v[178:181], v164 offset:33792
	ds_read_b128 v[182:185], v164 offset:34816
	ds_read_b128 v[186:189], v164 offset:35840
	ds_read_b128 v[190:193], v164 offset:36864
	ds_read_b128 v[194:197], v164 offset:37888
	ds_read_b128 v[198:201], v164 offset:38912
	ds_read_b128 v[202:205], v164 offset:39936
	global_load_lds_dwordx4 v240, s[76:77]
	s_mov_b32 m0, s84
	s_nop 0
	global_load_lds_dwordx4 v242, s[76:77]
	s_waitcnt lgkmcnt(0)
	s_waitcnt vmcnt(8)
	s_barrier
	s_setprio 1
	s_waitcnt lgkmcnt(0)
	v_mfma_i32_16x16x64_i8 v[140:143], v[56:59], v[174:177], v[140:143]
	v_mfma_i32_16x16x64_i8 v[132:135], v[72:75], v[174:177], v[132:135]
	v_mfma_i32_16x16x64_i8 v[124:127], v[56:59], v[182:185], v[124:127]
	v_mfma_i32_16x16x64_i8 v[116:119], v[72:75], v[182:185], v[116:119]
	v_mfma_i32_16x16x64_i8 v[108:111], v[56:59], v[190:193], v[108:111]
	v_mfma_i32_16x16x64_i8 v[100:103], v[72:75], v[190:193], v[100:103]
	v_mfma_i32_16x16x64_i8 v[92:95], v[56:59], v[198:201], v[92:95]
	v_mfma_i32_16x16x64_i8 v[84:87], v[72:75], v[198:201], v[84:87]
	v_mfma_i32_16x16x64_i8 v[140:143], v[64:67], v[178:181], v[140:143]
	v_mfma_i32_16x16x64_i8 v[132:135], v[144:147], v[178:181], v[132:135]
	v_mfma_i32_16x16x64_i8 v[124:127], v[64:67], v[186:189], v[124:127]
	v_mfma_i32_16x16x64_i8 v[116:119], v[144:147], v[186:189], v[116:119]
	v_mfma_i32_16x16x64_i8 v[108:111], v[64:67], v[194:197], v[108:111]
	v_mfma_i32_16x16x64_i8 v[100:103], v[144:147], v[194:197], v[100:103]
	v_mfma_i32_16x16x64_i8 v[92:95], v[64:67], v[202:205], v[92:95]
	v_mfma_i32_16x16x64_i8 v[84:87], v[144:147], v[202:205], v[84:87]
	v_mfma_i32_16x16x64_i8 v[136:139], v[150:153], v[174:177], v[136:139]
	v_mfma_i32_16x16x64_i8 v[128:131], v[166:169], v[174:177], v[128:131]
	v_mfma_i32_16x16x64_i8 v[120:123], v[150:153], v[182:185], v[120:123]
	v_mfma_i32_16x16x64_i8 v[112:115], v[166:169], v[182:185], v[112:115]
	v_mfma_i32_16x16x64_i8 v[104:107], v[150:153], v[190:193], v[104:107]
	v_mfma_i32_16x16x64_i8 v[96:99], v[166:169], v[190:193], v[96:99]
	v_mfma_i32_16x16x64_i8 v[88:91], v[150:153], v[198:201], v[88:91]
	v_mfma_i32_16x16x64_i8 v[80:83], v[166:169], v[198:201], v[80:83]
	v_mfma_i32_16x16x64_i8 v[136:139], v[154:157], v[178:181], v[136:139]
	v_mfma_i32_16x16x64_i8 v[128:131], v[170:173], v[178:181], v[128:131]
	v_mfma_i32_16x16x64_i8 v[120:123], v[154:157], v[186:189], v[120:123]
	v_mfma_i32_16x16x64_i8 v[112:115], v[170:173], v[186:189], v[112:115]
	v_mfma_i32_16x16x64_i8 v[104:107], v[154:157], v[194:197], v[104:107]
	v_mfma_i32_16x16x64_i8 v[96:99], v[170:173], v[194:197], v[96:99]
	v_mfma_i32_16x16x64_i8 v[88:91], v[154:157], v[202:205], v[88:91]
	v_mfma_i32_16x16x64_i8 v[80:83], v[170:173], v[202:205], v[80:83]
	s_setprio 0
	s_waitcnt vmcnt(8)
	s_barrier
; #define G_STAGE(bufoff, gbase, voff) do { _Pragma("unroll") for (int _i = 0; _i < 2; ++_i) \
;         __builtin_amdgcn_global_load_lds((const unsigned*)((const char*)(gbase) + (voff)[_i]), (LAS unsigned*)(lds + (bufoff) + ldsw + _i * 8192), 16, 0, 0); } while (0)
; #define G_LDA(dst, b, h) do { _Pragma("unroll") for (int m = 0; m < 4; ++m) G_LD8(dst[m], lds + G_SA(b, h) + aoff + m * 2048); } while (0)
; #define G_WAIT_V(n) asm volatile("s_waitcnt vmcnt(" #n ")" ::: "memory")
; #define G_WAIT_L(n) asm volatile("s_waitcnt lgkmcnt(" #n ")" ::: "memory")
; #define G_BAR __builtin_amdgcn_s_barrier()
; #define G_SCHED __builtin_amdgcn_sched_barrier(0)
;     ...
;             G_LDA(At, 1, 1); G_STAGE(G_SB(1, 0), b02 + kstep, voffB); G_STAGE(G_SB(1, 1), b12 + kstep, voffB); G_STAGE(G_SA(1, 0), a02 + kstep, vA0);
;             G_WAIT_L(0); G_BAR; G_MMA(1, 0, At, B0); G_MMA(1, 1, At, B1); G_WAIT_V(8); G_BAR; G_SCHED;
;         }
	s_add_i32 s59, s59, s97
	v_lshl_add_u64 v[32:33], v[206:207], 0, s[46:47]
	s_mov_b32 m0, s59
	ds_read_b128 v[174:177], v164 offset:49152
	ds_read_b128 v[178:181], v164 offset:50176
	ds_read_b128 v[182:185], v164 offset:51200
	ds_read_b128 v[186:189], v164 offset:52224
	ds_read_b128 v[190:193], v164 offset:53248
	ds_read_b128 v[194:197], v164 offset:54272
	ds_read_b128 v[198:201], v164 offset:55296
	ds_read_b128 v[202:205], v164 offset:56320
	global_load_lds_dwordx4 v[32:33], off
	v_lshl_add_u64 v[32:33], v[208:209], 0, s[46:47]
	s_add_i32 m0, s59, 0x2000
	s_add_i32 s59, s73, s97
	global_load_lds_dwordx4 v[32:33], off
	v_lshl_add_u64 v[32:33], v[210:211], 0, s[46:47]
	s_mov_b32 m0, s59
	s_nop 0
	global_load_lds_dwordx4 v[32:33], off
	v_lshl_add_u64 v[32:33], v[212:213], 0, s[46:47]
	s_add_i32 m0, s59, 0x2000
	s_nop 0
	global_load_lds_dwordx4 v[32:33], off
	v_lshl_add_u64 v[32:33], v[158:159], 0, s[46:47]
	s_mov_b32 m0, s86
	s_nop 0
	global_load_lds_dwordx4 v[32:33], off
	v_lshl_add_u64 v[32:33], v[214:215], 0, s[46:47]
	s_mov_b32 m0, s87
	s_nop 0
	global_load_lds_dwordx4 v[32:33], off
	s_waitcnt lgkmcnt(0)
	s_waitcnt vmcnt(8)
	s_barrier
	s_setprio 1
	s_waitcnt lgkmcnt(0)
	v_mfma_i32_16x16x64_i8 v[76:79], v[56:59], v[174:177], v[76:79]
	v_mfma_i32_16x16x64_i8 v[68:71], v[72:75], v[174:177], v[68:71]
	v_mfma_i32_16x16x64_i8 v[60:63], v[56:59], v[182:185], v[60:63]
	v_mfma_i32_16x16x64_i8 v[50:53], v[72:75], v[182:185], v[52:55]
	v_mfma_i32_16x16x64_i8 v[28:31], v[56:59], v[190:193], v[28:31]
	v_mfma_i32_16x16x64_i8 v[20:23], v[72:75], v[190:193], v[20:23]
	v_mfma_i32_16x16x64_i8 v[12:15], v[56:59], v[198:201], v[12:15]
	v_mfma_i32_16x16x64_i8 v[4:7], v[72:75], v[198:201], v[4:7]
	v_mfma_i32_16x16x64_i8 v[76:79], v[64:67], v[178:181], v[76:79]
	v_mfma_i32_16x16x64_i8 v[68:71], v[144:147], v[178:181], v[68:71]
	v_mfma_i32_16x16x64_i8 v[60:63], v[64:67], v[186:189], v[60:63]
	v_mfma_i32_16x16x64_i8 v[52:55], v[144:147], v[186:189], v[50:53]
	v_mfma_i32_16x16x64_i8 v[28:31], v[64:67], v[194:197], v[28:31]
	v_mfma_i32_16x16x64_i8 v[20:23], v[144:147], v[194:197], v[20:23]
	v_mfma_i32_16x16x64_i8 v[12:15], v[64:67], v[202:205], v[12:15]
	v_mfma_i32_16x16x64_i8 v[4:7], v[144:147], v[202:205], v[4:7]
	v_mfma_i32_16x16x64_i8 v[32:35], v[150:153], v[174:177], v[34:37]
	v_mfma_i32_16x16x64_i8 v[72:75], v[154:157], v[178:181], v[32:35]
	v_mfma_i32_16x16x64_i8 v[32:35], v[166:169], v[174:177], v[38:41]
	v_mfma_i32_16x16x64_i8 v[64:67], v[170:173], v[178:181], v[32:35]
	v_mfma_i32_16x16x64_i8 v[32:35], v[150:153], v[182:185], v[42:45]
	v_mfma_i32_16x16x64_i8 v[56:59], v[154:157], v[186:189], v[32:35]
	v_mfma_i32_16x16x64_i8 v[32:35], v[166:169], v[182:185], v[46:49]
	v_mfma_i32_16x16x64_i8 v[24:27], v[150:153], v[190:193], v[24:27]
	v_mfma_i32_16x16x64_i8 v[16:19], v[166:169], v[190:193], v[16:19]
	v_mfma_i32_16x16x64_i8 v[8:11], v[150:153], v[198:201], v[8:11]
	v_mfma_i32_16x16x64_i8 v[0:3], v[166:169], v[198:201], v[0:3]
	v_mfma_i32_16x16x64_i8 v[48:51], v[170:173], v[186:189], v[32:35]
	v_mfma_i32_16x16x64_i8 v[24:27], v[154:157], v[194:197], v[24:27]
	v_mfma_i32_16x16x64_i8 v[16:19], v[170:173], v[194:197], v[16:19]
	v_mfma_i32_16x16x64_i8 v[8:11], v[154:157], v[202:205], v[8:11]
	v_mfma_i32_16x16x64_i8 v[0:3], v[170:173], v[202:205], v[0:3]
	s_setprio 0
	s_waitcnt vmcnt(8)
	s_barrier
	s_add_u32 s0, s0, 0x100
	s_addc_u32 s2, s2, 0
	s_add_u32 s5, s5, 0x100
	s_addc_u32 s6, s6, 0
	s_add_u32 s19, s19, 0x100
	s_addc_u32 s33, s33, 0
	s_add_u32 s74, s74, 0x100
	s_addc_u32 s75, s75, 0
	s_cmp_ge_i32 s63, s25
	s_mov_b32 s59, s63
	s_cbranch_scc0 .LBB0_179
	s_and_b64 vcc, exec, s[50:51]
	s_cbranch_vccz .LBB0_182

; #define G_STAGE(bufoff, gbase, voff) do { _Pragma("unroll") for (int _i = 0; _i < 2; ++_i) \
;         __builtin_amdgcn_global_load_lds((const unsigned*)((const char*)(gbase) + (voff)[_i]), (LAS unsigned*)(lds + (bufoff) + ldsw + _i * 8192), 16, 0, 0); } while (0)
; #define G_LDA(dst, b, h) do { _Pragma("unroll") for (int m = 0; m < 4; ++m) G_LD8(dst[m], lds + G_SA(b, h) + aoff + m * 2048); } while (0)
; #define G_LDB(dst, b, h) do { _Pragma("unroll") for (int n = 0; n < 2; ++n) G_LD8(dst[n], lds + G_SB(b, h) + boff + n * 2048); } while (0)
; #define G_WAIT_V(n) asm volatile("s_waitcnt vmcnt(" #n ")" ::: "memory")
; #define G_WAIT_L(n) asm volatile("s_waitcnt lgkmcnt(" #n ")" ::: "memory")
; #define G_BAR __builtin_amdgcn_s_barrier()
; #define G_SCHED __builtin_amdgcn_sched_barrier(0)
;     __device__ __forceinline__ unsigned row_off(const Unit& u, int r, LAS unsigned char* lds) const { return (unsigned)((const LAS int*)(lds + LDS_STAGE + u.q * 4096))[r] * (unsigned)rowbytes; }
;     ...
;             const char* a11 = cur.a1 + (size_t)(t + 1) * kstep;
;             const char* a02 = last ? nxt.a0 : cur.a0 + (size_t)(t + 2) * kstep; const char* a12 = last ? nxt.a1 : cur.a1 + (size_t)(t + 2) * kstep;
;             const char* b02 = last ? nxt.b0 : cur.b0 + (size_t)(t + 2) * kstep; const char* b12 = last ? nxt.b1 : cur.b1 + (size_t)(t + 2) * kstep;
;             G_LDB(B0, 0, 0); G_LDB(B1, 0, 1); G_SCHED; G_LDA(At, 0, 0); G_STAGE(G_SA(1, 1), a11, vA1);
;             if constexpr (GATHER) { if (last) { int tz = tid; asm volatile("" : "+v"(tz));
; #pragma unroll
;                 for (int i = 0; i < 2; ++i) { int R, C; stage_rc(tz * 16 + i * 8192, R, C); gc0[i] = S.row_off(nxt, R, lds) + (unsigned)C * 2u; gc1[i] = S.row_off(nxt, 128 + R, lds) + (unsigned)C * 2u; } } }
;             G_WAIT_L(0); G_BAR; G_MMA(0, 0, At, B0); G_MMA(0, 1, At, B1); G_WAIT_V(8); G_BAR; G_SCHED;
;             G_LDA(At, 0, 1); G_STAGE(G_SB(0, 0), b02, voffB); G_STAGE(G_SB(0, 1), b12, voffB); G_STAGE(G_SA(0, 0), a02, vA0);
;             G_WAIT_L(0); G_BAR; G_MMA(1, 0, At, B0); G_MMA(1, 1, At, B1); G_WAIT_V(8); G_BAR; G_SCHED;
.LBB0_249:
	v_add_u32_e32 v144, s23, v151
	v_add_u32_e32 v166, s24, v151
	ds_read_b128 v[132:135], v144
	ds_read_b128 v[136:139], v144 offset:1024
	ds_read_b128 v[140:143], v144 offset:2048
	ds_read_b128 v[144:147], v144 offset:3072
	ds_read_b128 v[154:157], v166
	ds_read_b128 v[158:161], v166 offset:1024
	ds_read_b128 v[162:165], v166 offset:2048
	ds_read_b128 v[166:169], v166 offset:3072
	s_add_i32 s68, s58, 2
	s_add_u32 s69, s56, 0x80
	s_addc_u32 s59, s57, 0
	s_add_i32 s71, s23, s97
	s_add_i32 m0, s2, 0xc000
	s_add_i32 s70, s2, 0xe000
	s_add_i32 s72, s71, 0x2000
	s_cmp_eq_u32 s22, s58
	s_cselect_b32 s58, s46, s69
	s_cselect_b32 s61, s45, s67
	s_cselect_b32 s60, s44, s66
	s_cselect_b32 s63, s49, s55
	s_cselect_b32 s62, s48, s43
	s_cselect_b32 s59, s47, s59
	ds_read_b128 v[170:173], v152
	ds_read_b128 v[174:177], v152 offset:1024
	ds_read_b128 v[178:181], v152 offset:2048
	ds_read_b128 v[182:185], v152 offset:3072
	ds_read_b128 v[186:189], v152 offset:4096
	ds_read_b128 v[190:193], v152 offset:5120
	ds_read_b128 v[194:197], v152 offset:6144
	ds_read_b128 v[198:201], v152 offset:7168
	global_load_lds_dwordx4 v240, s[56:57]
	s_mov_b32 m0, s70
	s_nop 0
	global_load_lds_dwordx4 v242, s[56:57]
	s_waitcnt lgkmcnt(0)
	v_mov_b32_e32 v131, v129
	s_waitcnt vmcnt(8)
	s_barrier
	s_setprio 1
	s_waitcnt lgkmcnt(0)
	v_mfma_i32_16x16x64_i8 v[124:127], v[132:135], v[170:173], v[124:127]
	v_mfma_i32_16x16x64_i8 v[120:123], v[140:143], v[170:173], v[120:123]
	v_mfma_i32_16x16x64_i8 v[108:111], v[132:135], v[178:181], v[108:111]
	v_mfma_i32_16x16x64_i8 v[104:107], v[140:143], v[178:181], v[104:107]
	v_mfma_i32_16x16x64_i8 v[92:95], v[132:135], v[186:189], v[92:95]
	v_mfma_i32_16x16x64_i8 v[88:91], v[140:143], v[186:189], v[88:91]
	v_mfma_i32_16x16x64_i8 v[76:79], v[132:135], v[194:197], v[76:79]
	v_mfma_i32_16x16x64_i8 v[72:75], v[140:143], v[194:197], v[72:75]
	v_mfma_i32_16x16x64_i8 v[124:127], v[136:139], v[174:177], v[124:127]
	v_mfma_i32_16x16x64_i8 v[120:123], v[144:147], v[174:177], v[120:123]
	v_mfma_i32_16x16x64_i8 v[108:111], v[136:139], v[182:185], v[108:111]
	v_mfma_i32_16x16x64_i8 v[104:107], v[144:147], v[182:185], v[104:107]
	v_mfma_i32_16x16x64_i8 v[92:95], v[136:139], v[190:193], v[92:95]
	v_mfma_i32_16x16x64_i8 v[88:91], v[144:147], v[190:193], v[88:91]
	v_mfma_i32_16x16x64_i8 v[76:79], v[136:139], v[198:201], v[76:79]
	v_mfma_i32_16x16x64_i8 v[72:75], v[144:147], v[198:201], v[72:75]
	v_mfma_i32_16x16x64_i8 v[116:119], v[154:157], v[170:173], v[116:119]
	v_mfma_i32_16x16x64_i8 v[112:115], v[162:165], v[170:173], v[112:115]
	v_mfma_i32_16x16x64_i8 v[100:103], v[154:157], v[178:181], v[100:103]
	v_mfma_i32_16x16x64_i8 v[96:99], v[162:165], v[178:181], v[96:99]
	v_mfma_i32_16x16x64_i8 v[84:87], v[154:157], v[186:189], v[84:87]
	v_mfma_i32_16x16x64_i8 v[80:83], v[162:165], v[186:189], v[80:83]
	v_mfma_i32_16x16x64_i8 v[68:71], v[154:157], v[194:197], v[68:71]
	v_mfma_i32_16x16x64_i8 v[64:67], v[162:165], v[194:197], v[64:67]
	v_mfma_i32_16x16x64_i8 v[116:119], v[158:161], v[174:177], v[116:119]
	v_mfma_i32_16x16x64_i8 v[112:115], v[166:169], v[174:177], v[112:115]
	v_mfma_i32_16x16x64_i8 v[100:103], v[158:161], v[182:185], v[100:103]
	v_mfma_i32_16x16x64_i8 v[96:99], v[166:169], v[182:185], v[96:99]
	v_mfma_i32_16x16x64_i8 v[84:87], v[158:161], v[190:193], v[84:87]
	v_mfma_i32_16x16x64_i8 v[80:83], v[166:169], v[190:193], v[80:83]
	v_mfma_i32_16x16x64_i8 v[68:71], v[158:161], v[198:201], v[68:71]
	v_mfma_i32_16x16x64_i8 v[64:67], v[166:169], v[198:201], v[64:67]
	s_setprio 0
	s_waitcnt vmcnt(8)
	s_barrier
	s_mov_b32 m0, s71
	ds_read_b128 v[170:173], v152 offset:16384
	ds_read_b128 v[174:177], v152 offset:17408
	ds_read_b128 v[178:181], v152 offset:18432
	ds_read_b128 v[182:185], v152 offset:19456
	ds_read_b128 v[186:189], v152 offset:20480
	ds_read_b128 v[190:193], v152 offset:21504
	ds_read_b128 v[194:197], v152 offset:22528
	ds_read_b128 v[198:201], v152 offset:23552
	v_mov_b32_e32 v203, v129
	global_load_lds_dwordx4 v244, s[62:63]
	v_mov_b32_e32 v205, v129
	s_mov_b32 m0, s72
	v_lshl_add_u64 v[206:207], s[62:63], 0, v[244:245]
	v_lshl_add_u64 v[208:209], s[62:63], 0, v[246:247]
	global_load_lds_dwordx4 v246, s[62:63]
	s_cselect_b32 s63, s51, s65
	s_cselect_b32 s62, s50, s64
	s_add_i32 s69, s24, s97
	s_mov_b32 m0, s69
	v_lshl_add_u64 v[210:211], s[62:63], 0, v[244:245]
	global_load_lds_dwordx4 v244, s[62:63]
	s_add_i32 m0, s69, 0x2000
	v_lshl_add_u64 v[202:203], s[62:63], 0, v[246:247]
	global_load_lds_dwordx4 v246, s[62:63]
	s_mov_b32 m0, s2
	v_lshl_add_u64 v[204:205], s[60:61], 0, v[240:241]
	global_load_lds_dwordx4 v240, s[60:61]
	s_mov_b32 m0, s10
	v_lshl_add_u64 v[212:213], s[60:61], 0, v[242:243]
	global_load_lds_dwordx4 v242, s[60:61]
	s_waitcnt lgkmcnt(0)
	s_waitcnt vmcnt(8)
	s_barrier
; #define G_STAGE(bufoff, gbase, voff) do { _Pragma("unroll") for (int _i = 0; _i < 2; ++_i) \
;         __builtin_amdgcn_global_load_lds((const unsigned*)((const char*)(gbase) + (voff)[_i]), (LAS unsigned*)(lds + (bufoff) + ldsw + _i * 8192), 16, 0, 0); } while (0)
; #define G_LDA(dst, b, h) do { _Pragma("unroll") for (int m = 0; m < 4; ++m) G_LD8(dst[m], lds + G_SA(b, h) + aoff + m * 2048); } while (0)
; #define G_LDB(dst, b, h) do { _Pragma("unroll") for (int n = 0; n < 2; ++n) G_LD8(dst[n], lds + G_SB(b, h) + boff + n * 2048); } while (0)
; #define G_WAIT_V(n) asm volatile("s_waitcnt vmcnt(" #n ")" ::: "memory")
; #define G_WAIT_L(n) asm volatile("s_waitcnt lgkmcnt(" #n ")" ::: "memory")
; #define G_BAR __builtin_amdgcn_s_barrier()
; #define G_SCHED __builtin_amdgcn_sched_barrier(0)
;     ...
;             G_WAIT_L(0); G_BAR; G_MMA(1, 0, At, B0); G_MMA(1, 1, At, B1); G_WAIT_V(8); G_BAR; G_SCHED;
;             G_LDB(B0, 1, 0); G_LDB(B1, 1, 1); G_SCHED; G_LDA(At, 1, 0); G_STAGE(G_SA(0, 1), a12, vA1);
;             G_WAIT_L(0); G_BAR; G_MMA(0, 0, At, B0); G_MMA(0, 1, At, B1); G_WAIT_V(8); G_BAR; G_SCHED;
	s_setprio 1
	s_waitcnt lgkmcnt(0)
	v_mfma_i32_16x16x64_i8 v[60:63], v[132:135], v[170:173], v[60:63]
	v_mfma_i32_16x16x64_i8 v[56:59], v[140:143], v[170:173], v[56:59]
	v_mfma_i32_16x16x64_i8 v[44:47], v[132:135], v[178:181], v[44:47]
	v_mfma_i32_16x16x64_i8 v[40:43], v[140:143], v[178:181], v[40:43]
	v_mfma_i32_16x16x64_i8 v[28:31], v[132:135], v[186:189], v[28:31]
	v_mfma_i32_16x16x64_i8 v[24:27], v[140:143], v[186:189], v[24:27]
	v_mfma_i32_16x16x64_i8 v[12:15], v[132:135], v[194:197], v[12:15]
	v_mfma_i32_16x16x64_i8 v[8:11], v[140:143], v[194:197], v[8:11]
	v_mfma_i32_16x16x64_i8 v[60:63], v[136:139], v[174:177], v[60:63]
	v_mfma_i32_16x16x64_i8 v[56:59], v[144:147], v[174:177], v[56:59]
	v_mfma_i32_16x16x64_i8 v[44:47], v[136:139], v[182:185], v[44:47]
	v_mfma_i32_16x16x64_i8 v[40:43], v[144:147], v[182:185], v[40:43]
	v_mfma_i32_16x16x64_i8 v[28:31], v[136:139], v[190:193], v[28:31]
	v_mfma_i32_16x16x64_i8 v[24:27], v[144:147], v[190:193], v[24:27]
	v_mfma_i32_16x16x64_i8 v[12:15], v[136:139], v[198:201], v[12:15]
	v_mfma_i32_16x16x64_i8 v[8:11], v[144:147], v[198:201], v[8:11]
	v_mfma_i32_16x16x64_i8 v[52:55], v[154:157], v[170:173], v[52:55]
	v_mfma_i32_16x16x64_i8 v[48:51], v[162:165], v[170:173], v[48:51]
	v_mfma_i32_16x16x64_i8 v[36:39], v[154:157], v[178:181], v[36:39]
	v_mfma_i32_16x16x64_i8 v[32:35], v[162:165], v[178:181], v[32:35]
	v_mfma_i32_16x16x64_i8 v[20:23], v[154:157], v[186:189], v[20:23]
	v_mfma_i32_16x16x64_i8 v[16:19], v[162:165], v[186:189], v[16:19]
	v_mfma_i32_16x16x64_i8 v[4:7], v[154:157], v[194:197], v[4:7]
	v_mfma_i32_16x16x64_i8 v[0:3], v[162:165], v[194:197], v[0:3]
	v_mfma_i32_16x16x64_i8 v[52:55], v[158:161], v[174:177], v[52:55]
	v_mfma_i32_16x16x64_i8 v[48:51], v[166:169], v[174:177], v[48:51]
	v_mfma_i32_16x16x64_i8 v[36:39], v[158:161], v[182:185], v[36:39]
	v_mfma_i32_16x16x64_i8 v[32:35], v[166:169], v[182:185], v[32:35]
	v_mfma_i32_16x16x64_i8 v[20:23], v[158:161], v[190:193], v[20:23]
	v_mfma_i32_16x16x64_i8 v[16:19], v[166:169], v[190:193], v[16:19]
	v_mfma_i32_16x16x64_i8 v[4:7], v[158:161], v[198:201], v[4:7]
	v_mfma_i32_16x16x64_i8 v[0:3], v[166:169], v[198:201], v[0:3]
	s_setprio 0
	s_waitcnt vmcnt(8)
	s_barrier
	s_add_i32 s60, 0, 0x18000
	v_add_u32_e32 v131, s60, v151
	s_add_i32 s61, 0, 0x1c000
	ds_read_b128 v[132:135], v131
	ds_read_b128 v[136:139], v131 offset:1024
	ds_read_b128 v[140:143], v131 offset:2048
	ds_read_b128 v[144:147], v131 offset:3072
	v_add_u32_e32 v131, s61, v151
	ds_read_b128 v[154:157], v131
	ds_read_b128 v[158:161], v131 offset:1024
	ds_read_b128 v[162:165], v131 offset:2048
	ds_read_b128 v[166:169], v131 offset:3072
	s_mov_b32 m0, s11
	ds_read_b128 v[170:173], v152 offset:32768
	ds_read_b128 v[174:177], v152 offset:33792
	ds_read_b128 v[178:181], v152 offset:34816
	ds_read_b128 v[182:185], v152 offset:35840
	ds_read_b128 v[186:189], v152 offset:36864
	ds_read_b128 v[190:193], v152 offset:37888
	ds_read_b128 v[194:197], v152 offset:38912
	ds_read_b128 v[198:201], v152 offset:39936
	global_load_lds_dwordx4 v240, s[58:59]
	s_mov_b32 m0, s18
	s_nop 0
	global_load_lds_dwordx4 v242, s[58:59]
	s_waitcnt lgkmcnt(0)
	s_waitcnt vmcnt(8)
	s_barrier
	s_setprio 1
	s_waitcnt lgkmcnt(0)
	v_mfma_i32_16x16x64_i8 v[124:127], v[132:135], v[170:173], v[124:127]
	v_mfma_i32_16x16x64_i8 v[120:123], v[140:143], v[170:173], v[120:123]
	v_mfma_i32_16x16x64_i8 v[108:111], v[132:135], v[178:181], v[108:111]
	v_mfma_i32_16x16x64_i8 v[104:107], v[140:143], v[178:181], v[104:107]
	v_mfma_i32_16x16x64_i8 v[92:95], v[132:135], v[186:189], v[92:95]
	v_mfma_i32_16x16x64_i8 v[88:91], v[140:143], v[186:189], v[88:91]
	v_mfma_i32_16x16x64_i8 v[76:79], v[132:135], v[194:197], v[76:79]
	v_mfma_i32_16x16x64_i8 v[72:75], v[140:143], v[194:197], v[72:75]
	v_mfma_i32_16x16x64_i8 v[124:127], v[136:139], v[174:177], v[124:127]
	v_mfma_i32_16x16x64_i8 v[120:123], v[144:147], v[174:177], v[120:123]
	v_mfma_i32_16x16x64_i8 v[108:111], v[136:139], v[182:185], v[108:111]
	v_mfma_i32_16x16x64_i8 v[104:107], v[144:147], v[182:185], v[104:107]
	v_mfma_i32_16x16x64_i8 v[92:95], v[136:139], v[190:193], v[92:95]
	v_mfma_i32_16x16x64_i8 v[88:91], v[144:147], v[190:193], v[88:91]
	v_mfma_i32_16x16x64_i8 v[76:79], v[136:139], v[198:201], v[76:79]
	v_mfma_i32_16x16x64_i8 v[72:75], v[144:147], v[198:201], v[72:75]
	v_mfma_i32_16x16x64_i8 v[116:119], v[154:157], v[170:173], v[116:119]
	v_mfma_i32_16x16x64_i8 v[112:115], v[162:165], v[170:173], v[112:115]
	v_mfma_i32_16x16x64_i8 v[100:103], v[154:157], v[178:181], v[100:103]
	v_mfma_i32_16x16x64_i8 v[96:99], v[162:165], v[178:181], v[96:99]
	v_mfma_i32_16x16x64_i8 v[84:87], v[154:157], v[186:189], v[84:87]
	v_mfma_i32_16x16x64_i8 v[80:83], v[162:165], v[186:189], v[80:83]
	v_mfma_i32_16x16x64_i8 v[68:71], v[154:157], v[194:197], v[68:71]
	v_mfma_i32_16x16x64_i8 v[64:67], v[162:165], v[194:197], v[64:67]
	v_mfma_i32_16x16x64_i8 v[116:119], v[158:161], v[174:177], v[116:119]
	v_mfma_i32_16x16x64_i8 v[112:115], v[166:169], v[174:177], v[112:115]
	v_mfma_i32_16x16x64_i8 v[100:103], v[158:161], v[182:185], v[100:103]
	v_mfma_i32_16x16x64_i8 v[96:99], v[166:169], v[182:185], v[96:99]
	v_mfma_i32_16x16x64_i8 v[84:87], v[158:161], v[190:193], v[84:87]
	v_mfma_i32_16x16x64_i8 v[80:83], v[166:169], v[190:193], v[80:83]
	v_mfma_i32_16x16x64_i8 v[68:71], v[158:161], v[198:201], v[68:71]
	v_mfma_i32_16x16x64_i8 v[64:67], v[166:169], v[198:201], v[64:67]
	s_setprio 0
	s_waitcnt vmcnt(8)
	s_barrier
; #define G_STAGE(bufoff, gbase, voff) do { _Pragma("unroll") for (int _i = 0; _i < 2; ++_i) \
;         __builtin_amdgcn_global_load_lds((const unsigned*)((const char*)(gbase) + (voff)[_i]), (LAS unsigned*)(lds + (bufoff) + ldsw + _i * 8192), 16, 0, 0); } while (0)
; #define G_LDA(dst, b, h) do { _Pragma("unroll") for (int m = 0; m < 4; ++m) G_LD8(dst[m], lds + G_SA(b, h) + aoff + m * 2048); } while (0)
; #define G_WAIT_V(n) asm volatile("s_waitcnt vmcnt(" #n ")" ::: "memory")
; #define G_WAIT_L(n) asm volatile("s_waitcnt lgkmcnt(" #n ")" ::: "memory")
; #define G_BAR __builtin_amdgcn_s_barrier()
; #define G_SCHED __builtin_amdgcn_sched_barrier(0)
;     ...
;             G_LDA(At, 1, 1); G_STAGE(G_SB(1, 0), b02 + kstep, voffB); G_STAGE(G_SB(1, 1), b12 + kstep, voffB); G_STAGE(G_SA(1, 0), a02 + kstep, vA0);
;             G_WAIT_L(0); G_BAR; G_MMA(1, 0, At, B0); G_MMA(1, 1, At, B1); G_WAIT_V(8); G_BAR; G_SCHED;
;         }
	s_add_i32 s58, s60, s97
	v_lshl_add_u64 v[130:131], v[206:207], 0, s[8:9]
	s_mov_b32 m0, s58
	ds_read_b128 v[170:173], v152 offset:49152
	ds_read_b128 v[174:177], v152 offset:50176
	ds_read_b128 v[178:181], v152 offset:51200
	ds_read_b128 v[182:185], v152 offset:52224
	ds_read_b128 v[186:189], v152 offset:53248
	ds_read_b128 v[190:193], v152 offset:54272
	ds_read_b128 v[194:197], v152 offset:55296
	ds_read_b128 v[198:201], v152 offset:56320
	global_load_lds_dwordx4 v[130:131], off
	v_lshl_add_u64 v[130:131], v[208:209], 0, s[8:9]
	s_add_i32 m0, s58, 0x2000
	s_add_i32 s58, s61, s97
	global_load_lds_dwordx4 v[130:131], off
	v_lshl_add_u64 v[130:131], v[210:211], 0, s[8:9]
	s_mov_b32 m0, s58
	s_nop 0
	global_load_lds_dwordx4 v[130:131], off
	v_lshl_add_u64 v[130:131], v[202:203], 0, s[8:9]
	s_add_i32 m0, s58, 0x2000
	s_nop 0
	global_load_lds_dwordx4 v[130:131], off
	v_lshl_add_u64 v[130:131], v[204:205], 0, s[8:9]
	s_mov_b32 m0, s20
	s_nop 0
	global_load_lds_dwordx4 v[130:131], off
	v_lshl_add_u64 v[130:131], v[212:213], 0, s[8:9]
	s_mov_b32 m0, s21
	s_nop 0
	global_load_lds_dwordx4 v[130:131], off
	s_waitcnt lgkmcnt(0)
	s_waitcnt vmcnt(8)
	s_barrier
	s_setprio 1
	s_waitcnt lgkmcnt(0)
	v_mfma_i32_16x16x64_i8 v[60:63], v[132:135], v[170:173], v[60:63]
	v_mfma_i32_16x16x64_i8 v[56:59], v[140:143], v[170:173], v[56:59]
	v_mfma_i32_16x16x64_i8 v[44:47], v[132:135], v[178:181], v[44:47]
	v_mfma_i32_16x16x64_i8 v[40:43], v[140:143], v[178:181], v[40:43]
	v_mfma_i32_16x16x64_i8 v[28:31], v[132:135], v[186:189], v[28:31]
	v_mfma_i32_16x16x64_i8 v[24:27], v[140:143], v[186:189], v[24:27]
	v_mfma_i32_16x16x64_i8 v[12:15], v[132:135], v[194:197], v[12:15]
	v_mfma_i32_16x16x64_i8 v[8:11], v[140:143], v[194:197], v[8:11]
	v_mfma_i32_16x16x64_i8 v[60:63], v[136:139], v[174:177], v[60:63]
	v_mfma_i32_16x16x64_i8 v[56:59], v[144:147], v[174:177], v[56:59]
	v_mfma_i32_16x16x64_i8 v[44:47], v[136:139], v[182:185], v[44:47]
	v_mfma_i32_16x16x64_i8 v[40:43], v[144:147], v[182:185], v[40:43]
	v_mfma_i32_16x16x64_i8 v[28:31], v[136:139], v[190:193], v[28:31]
	v_mfma_i32_16x16x64_i8 v[24:27], v[144:147], v[190:193], v[24:27]
	v_mfma_i32_16x16x64_i8 v[12:15], v[136:139], v[198:201], v[12:15]
	v_mfma_i32_16x16x64_i8 v[8:11], v[144:147], v[198:201], v[8:11]
	v_mfma_i32_16x16x64_i8 v[52:55], v[154:157], v[170:173], v[52:55]
	v_mfma_i32_16x16x64_i8 v[48:51], v[162:165], v[170:173], v[48:51]
	v_mfma_i32_16x16x64_i8 v[36:39], v[154:157], v[178:181], v[36:39]
	v_mfma_i32_16x16x64_i8 v[32:35], v[162:165], v[178:181], v[32:35]
	v_mfma_i32_16x16x64_i8 v[20:23], v[154:157], v[186:189], v[20:23]
	v_mfma_i32_16x16x64_i8 v[16:19], v[162:165], v[186:189], v[16:19]
	v_mfma_i32_16x16x64_i8 v[4:7], v[154:157], v[194:197], v[4:7]
	v_mfma_i32_16x16x64_i8 v[0:3], v[162:165], v[194:197], v[0:3]
	v_mfma_i32_16x16x64_i8 v[52:55], v[158:161], v[174:177], v[52:55]
	v_mfma_i32_16x16x64_i8 v[48:51], v[166:169], v[174:177], v[48:51]
	v_mfma_i32_16x16x64_i8 v[36:39], v[158:161], v[182:185], v[36:39]
	v_mfma_i32_16x16x64_i8 v[32:35], v[166:169], v[182:185], v[32:35]
	v_mfma_i32_16x16x64_i8 v[20:23], v[158:161], v[190:193], v[20:23]
	v_mfma_i32_16x16x64_i8 v[16:19], v[166:169], v[190:193], v[16:19]
	v_mfma_i32_16x16x64_i8 v[4:7], v[158:161], v[198:201], v[4:7]
	v_mfma_i32_16x16x64_i8 v[0:3], v[166:169], v[198:201], v[0:3]
	s_setprio 0
	s_waitcnt vmcnt(8)
	s_barrier
	s_add_u32 s43, s43, 0x100
	s_addc_u32 s55, s55, 0
	s_add_u32 s64, s64, 0x100
	s_addc_u32 s65, s65, 0
	s_add_u32 s66, s66, 0x100
	s_addc_u32 s67, s67, 0
	s_add_u32 s56, s56, 0x100
	s_addc_u32 s57, s57, 0
	s_cmp_ge_i32 s68, s0
	s_mov_b32 s58, s68
	s_cbranch_scc0 .LBB0_249
	s_and_b64 vcc, exec, s[40:41]
	s_cbranch_vccz .LBB0_252

; #define G_STAGE(bufoff, gbase, voff) do { _Pragma("unroll") for (int _i = 0; _i < 2; ++_i) \
;         __builtin_amdgcn_global_load_lds((const unsigned*)((const char*)(gbase) + (voff)[_i]), (LAS unsigned*)(lds + (bufoff) + ldsw + _i * 8192), 16, 0, 0); } while (0)
; #define G_LDA(dst, b, h) do { _Pragma("unroll") for (int m = 0; m < 4; ++m) G_LD8(dst[m], lds + G_SA(b, h) + aoff + m * 2048); } while (0)
; #define G_LDB(dst, b, h) do { _Pragma("unroll") for (int n = 0; n < 2; ++n) G_LD8(dst[n], lds + G_SB(b, h) + boff + n * 2048); } while (0)
; #define G_WAIT_V(n) asm volatile("s_waitcnt vmcnt(" #n ")" ::: "memory")
; #define G_WAIT_L(n) asm volatile("s_waitcnt lgkmcnt(" #n ")" ::: "memory")
; #define G_BAR __builtin_amdgcn_s_barrier()
; #define G_SCHED __builtin_amdgcn_sched_barrier(0)
;     __device__ __forceinline__ unsigned row_off(const Unit& u, int r, LAS unsigned char* lds) const { return (unsigned)((const LAS int*)(lds + LDS_STAGE + u.q * 4096))[r] * (unsigned)rowbytes; }
;     ...
;             const char* a11 = cur.a1 + (size_t)(t + 1) * kstep;
;             const char* a02 = last ? nxt.a0 : cur.a0 + (size_t)(t + 2) * kstep; const char* a12 = last ? nxt.a1 : cur.a1 + (size_t)(t + 2) * kstep;
;             const char* b02 = last ? nxt.b0 : cur.b0 + (size_t)(t + 2) * kstep; const char* b12 = last ? nxt.b1 : cur.b1 + (size_t)(t + 2) * kstep;
;             G_LDB(B0, 0, 0); G_LDB(B1, 0, 1); G_SCHED; G_LDA(At, 0, 0); G_STAGE(G_SA(1, 1), a11, vA1);
;             if constexpr (GATHER) { if (last) { int tz = tid; asm volatile("" : "+v"(tz));
; #pragma unroll
;                 for (int i = 0; i < 2; ++i) { int R, C; stage_rc(tz * 16 + i * 8192, R, C); gc0[i] = S.row_off(nxt, R, lds) + (unsigned)C * 2u; gc1[i] = S.row_off(nxt, 128 + R, lds) + (unsigned)C * 2u; } } }
;             G_WAIT_L(0); G_BAR; G_MMA(0, 0, At, B0); G_MMA(0, 1, At, B1); G_WAIT_V(8); G_BAR; G_SCHED;
;             G_LDA(At, 0, 1); G_STAGE(G_SB(0, 0), b02, voffB); G_STAGE(G_SB(0, 1), b12, voffB); G_STAGE(G_SA(0, 0), a02, vA0);
;             G_WAIT_L(0); G_BAR; G_MMA(1, 0, At, B0); G_MMA(1, 1, At, B1); G_WAIT_V(8); G_BAR; G_SCHED;
.LBB0_284:
	v_add_u32_e32 v144, s24, v157
	v_add_u32_e32 v168, s25, v157
	ds_read_b128 v[100:103], v144
	ds_read_b128 v[112:115], v144 offset:1024
	ds_read_b128 v[120:123], v144 offset:2048
	ds_read_b128 v[144:147], v144 offset:3072
	ds_read_b128 v[150:153], v168
	ds_read_b128 v[160:163], v168 offset:1024
	ds_read_b128 v[164:167], v168 offset:2048
	ds_read_b128 v[168:171], v168 offset:3072
	s_add_i32 s76, s64, 2
	s_add_u32 s77, s62, 0x80
	s_addc_u32 s65, s63, 0
	s_add_i32 s79, s24, s97
	s_add_i32 m0, s0, 0xc000
	s_add_i32 s78, s0, 0xe000
	s_add_i32 s80, s79, 0x2000
	s_cmp_eq_u32 s23, s64
	s_cselect_b32 s64, s50, s77
	s_cselect_b32 s67, s49, s75
	s_cselect_b32 s66, s48, s71
	s_cselect_b32 s69, s53, s59
	s_cselect_b32 s68, s52, s45
	s_cselect_b32 s65, s51, s65
	ds_read_b128 v[172:175], v158
	ds_read_b128 v[176:179], v158 offset:1024
	ds_read_b128 v[180:183], v158 offset:2048
	ds_read_b128 v[184:187], v158 offset:3072
	ds_read_b128 v[188:191], v158 offset:4096
	ds_read_b128 v[192:195], v158 offset:5120
	ds_read_b128 v[196:199], v158 offset:6144
	ds_read_b128 v[200:203], v158 offset:7168
	global_load_lds_dwordx4 v240, s[62:63]
	s_mov_b32 m0, s78
	s_nop 0
	global_load_lds_dwordx4 v242, s[62:63]
	s_waitcnt lgkmcnt(0)
	v_mov_b32_e32 v93, v149
	s_waitcnt vmcnt(8)
	s_barrier
	s_setprio 1
	s_waitcnt lgkmcnt(0)
	v_mfma_i32_16x16x64_i8 v[140:143], v[100:103], v[172:175], v[140:143]
	v_mfma_i32_16x16x64_i8 v[132:135], v[120:123], v[172:175], v[132:135]
	v_mfma_i32_16x16x64_i8 v[94:97], v[100:103], v[180:183], v[96:99]
	v_mfma_i32_16x16x64_i8 v[88:91], v[120:123], v[180:183], v[88:91]
	v_mfma_i32_16x16x64_i8 v[60:63], v[100:103], v[188:191], v[60:63]
	v_mfma_i32_16x16x64_i8 v[56:59], v[120:123], v[188:191], v[56:59]
	v_mfma_i32_16x16x64_i8 v[28:31], v[100:103], v[196:199], v[28:31]
	v_mfma_i32_16x16x64_i8 v[24:27], v[120:123], v[196:199], v[24:27]
	v_mfma_i32_16x16x64_i8 v[140:143], v[112:115], v[176:179], v[140:143]
	v_mfma_i32_16x16x64_i8 v[132:135], v[144:147], v[176:179], v[132:135]
	v_mfma_i32_16x16x64_i8 v[94:97], v[112:115], v[184:187], v[94:97]
	v_mfma_i32_16x16x64_i8 v[88:91], v[144:147], v[184:187], v[88:91]
	v_mfma_i32_16x16x64_i8 v[60:63], v[112:115], v[192:195], v[60:63]
	v_mfma_i32_16x16x64_i8 v[56:59], v[144:147], v[192:195], v[56:59]
	v_mfma_i32_16x16x64_i8 v[28:31], v[112:115], v[200:203], v[28:31]
	v_mfma_i32_16x16x64_i8 v[24:27], v[144:147], v[200:203], v[24:27]
	v_mfma_i32_16x16x64_i8 v[124:127], v[150:153], v[172:175], v[124:127]
	v_mfma_i32_16x16x64_i8 v[108:111], v[164:167], v[172:175], v[108:111]
	v_mfma_i32_16x16x64_i8 v[76:79], v[150:153], v[180:183], v[76:79]
	v_mfma_i32_16x16x64_i8 v[72:75], v[164:167], v[180:183], v[72:75]
	v_mfma_i32_16x16x64_i8 v[44:47], v[150:153], v[188:191], v[44:47]
	v_mfma_i32_16x16x64_i8 v[40:43], v[164:167], v[188:191], v[40:43]
	v_mfma_i32_16x16x64_i8 v[12:15], v[150:153], v[196:199], v[12:15]
	v_mfma_i32_16x16x64_i8 v[8:11], v[164:167], v[196:199], v[8:11]
	v_mfma_i32_16x16x64_i8 v[124:127], v[160:163], v[176:179], v[124:127]
	v_mfma_i32_16x16x64_i8 v[108:111], v[168:171], v[176:179], v[108:111]
	v_mfma_i32_16x16x64_i8 v[76:79], v[160:163], v[184:187], v[76:79]
	v_mfma_i32_16x16x64_i8 v[72:75], v[168:171], v[184:187], v[72:75]
	v_mfma_i32_16x16x64_i8 v[44:47], v[160:163], v[192:195], v[44:47]
	v_mfma_i32_16x16x64_i8 v[40:43], v[168:171], v[192:195], v[40:43]
	v_mfma_i32_16x16x64_i8 v[12:15], v[160:163], v[200:203], v[12:15]
	v_mfma_i32_16x16x64_i8 v[8:11], v[168:171], v[200:203], v[8:11]
	s_setprio 0
	s_waitcnt vmcnt(8)
	s_barrier
	s_mov_b32 m0, s79
	ds_read_b128 v[172:175], v158 offset:16384
	ds_read_b128 v[176:179], v158 offset:17408
	ds_read_b128 v[180:183], v158 offset:18432
	ds_read_b128 v[184:187], v158 offset:19456
	ds_read_b128 v[188:191], v158 offset:20480
	ds_read_b128 v[192:195], v158 offset:21504
	ds_read_b128 v[196:199], v158 offset:22528
	ds_read_b128 v[200:203], v158 offset:23552
	v_mov_b32_e32 v205, v149
	global_load_lds_dwordx4 v244, s[68:69]
	v_mov_b32_e32 v207, v149
	s_mov_b32 m0, s80
	v_lshl_add_u64 v[208:209], s[68:69], 0, v[244:245]
	v_lshl_add_u64 v[210:211], s[68:69], 0, v[246:247]
	global_load_lds_dwordx4 v246, s[68:69]
	s_cselect_b32 s69, s55, s70
	s_cselect_b32 s68, s54, s61
	s_add_i32 s77, s25, s97
	s_mov_b32 m0, s77
	v_lshl_add_u64 v[212:213], s[68:69], 0, v[244:245]
	global_load_lds_dwordx4 v244, s[68:69]
	s_add_i32 m0, s77, 0x2000
	v_lshl_add_u64 v[204:205], s[68:69], 0, v[246:247]
	global_load_lds_dwordx4 v246, s[68:69]
	s_mov_b32 m0, s0
	v_lshl_add_u64 v[206:207], s[66:67], 0, v[240:241]
	global_load_lds_dwordx4 v240, s[66:67]
	s_mov_b32 m0, s11
	v_lshl_add_u64 v[214:215], s[66:67], 0, v[242:243]
	global_load_lds_dwordx4 v242, s[66:67]
	s_waitcnt lgkmcnt(0)
	s_waitcnt vmcnt(8)
	s_barrier
; #define G_STAGE(bufoff, gbase, voff) do { _Pragma("unroll") for (int _i = 0; _i < 2; ++_i) \
;         __builtin_amdgcn_global_load_lds((const unsigned*)((const char*)(gbase) + (voff)[_i]), (LAS unsigned*)(lds + (bufoff) + ldsw + _i * 8192), 16, 0, 0); } while (0)
; #define G_LDA(dst, b, h) do { _Pragma("unroll") for (int m = 0; m < 4; ++m) G_LD8(dst[m], lds + G_SA(b, h) + aoff + m * 2048); } while (0)
; #define G_LDB(dst, b, h) do { _Pragma("unroll") for (int n = 0; n < 2; ++n) G_LD8(dst[n], lds + G_SB(b, h) + boff + n * 2048); } while (0)
; #define G_WAIT_V(n) asm volatile("s_waitcnt vmcnt(" #n ")" ::: "memory")
; #define G_WAIT_L(n) asm volatile("s_waitcnt lgkmcnt(" #n ")" ::: "memory")
; #define G_BAR __builtin_amdgcn_s_barrier()
; #define G_SCHED __builtin_amdgcn_sched_barrier(0)
;     ...
;             G_WAIT_L(0); G_BAR; G_MMA(1, 0, At, B0); G_MMA(1, 1, At, B1); G_WAIT_V(8); G_BAR; G_SCHED;
;             G_LDB(B0, 1, 0); G_LDB(B1, 1, 1); G_SCHED; G_LDA(At, 1, 0); G_STAGE(G_SA(0, 1), a12, vA1);
;             G_WAIT_L(0); G_BAR; G_MMA(0, 0, At, B0); G_MMA(0, 1, At, B1); G_WAIT_V(8); G_BAR; G_SCHED;
	s_setprio 1
	s_waitcnt lgkmcnt(0)
	v_mfma_i32_16x16x64_i8 v[136:139], v[100:103], v[172:175], v[136:139]
	v_mfma_i32_16x16x64_i8 v[128:131], v[120:123], v[172:175], v[128:131]
	v_mfma_i32_16x16x64_i8 v[84:87], v[100:103], v[180:183], v[84:87]
	v_mfma_i32_16x16x64_i8 v[80:83], v[120:123], v[180:183], v[80:83]
	v_mfma_i32_16x16x64_i8 v[52:55], v[100:103], v[188:191], v[52:55]
	v_mfma_i32_16x16x64_i8 v[48:51], v[120:123], v[188:191], v[48:51]
	v_mfma_i32_16x16x64_i8 v[20:23], v[100:103], v[196:199], v[20:23]
	v_mfma_i32_16x16x64_i8 v[16:19], v[120:123], v[196:199], v[16:19]
	v_mfma_i32_16x16x64_i8 v[136:139], v[112:115], v[176:179], v[136:139]
	v_mfma_i32_16x16x64_i8 v[128:131], v[144:147], v[176:179], v[128:131]
	v_mfma_i32_16x16x64_i8 v[84:87], v[112:115], v[184:187], v[84:87]
	v_mfma_i32_16x16x64_i8 v[80:83], v[144:147], v[184:187], v[80:83]
	v_mfma_i32_16x16x64_i8 v[52:55], v[112:115], v[192:195], v[52:55]
	v_mfma_i32_16x16x64_i8 v[48:51], v[144:147], v[192:195], v[48:51]
	v_mfma_i32_16x16x64_i8 v[20:23], v[112:115], v[200:203], v[20:23]
	v_mfma_i32_16x16x64_i8 v[16:19], v[144:147], v[200:203], v[16:19]
	v_mfma_i32_16x16x64_i8 v[104:107], v[164:167], v[172:175], v[104:107]
	v_mfma_i32_16x16x64_i8 v[68:71], v[150:153], v[180:183], v[68:71]
	v_mfma_i32_16x16x64_i8 v[64:67], v[164:167], v[180:183], v[64:67]
	v_mfma_i32_16x16x64_i8 v[36:39], v[150:153], v[188:191], v[36:39]
	v_mfma_i32_16x16x64_i8 v[32:35], v[164:167], v[188:191], v[32:35]
	v_mfma_i32_16x16x64_i8 v[4:7], v[150:153], v[196:199], v[4:7]
	v_mfma_i32_16x16x64_i8 v[0:3], v[164:167], v[196:199], v[0:3]
	v_mfma_i32_16x16x64_i8 v[98:101], v[150:153], v[172:175], v[116:119]
	v_mfma_i32_16x16x64_i8 v[104:107], v[168:171], v[176:179], v[104:107]
	v_mfma_i32_16x16x64_i8 v[68:71], v[160:163], v[184:187], v[68:71]
	v_mfma_i32_16x16x64_i8 v[64:67], v[168:171], v[184:187], v[64:67]
	v_mfma_i32_16x16x64_i8 v[36:39], v[160:163], v[192:195], v[36:39]
	v_mfma_i32_16x16x64_i8 v[32:35], v[168:171], v[192:195], v[32:35]
	v_mfma_i32_16x16x64_i8 v[4:7], v[160:163], v[200:203], v[4:7]
	v_mfma_i32_16x16x64_i8 v[0:3], v[168:171], v[200:203], v[0:3]
	v_mfma_i32_16x16x64_i8 v[100:103], v[160:163], v[176:179], v[98:101]
	s_setprio 0
	s_waitcnt vmcnt(8)
	s_barrier
	s_add_i32 s66, 0, 0x18000
	v_add_u32_e32 v93, s66, v157
	s_add_i32 s67, 0, 0x1c000
	ds_read_b128 v[112:115], v93
	ds_read_b128 v[116:119], v93 offset:1024
	ds_read_b128 v[120:123], v93 offset:2048
	ds_read_b128 v[144:147], v93 offset:3072
	v_add_u32_e32 v93, s67, v157
	ds_read_b128 v[150:153], v93
	ds_read_b128 v[160:163], v93 offset:1024
	ds_read_b128 v[164:167], v93 offset:2048
	ds_read_b128 v[168:171], v93 offset:3072
	s_mov_b32 m0, s18
	ds_read_b128 v[172:175], v158 offset:32768
	ds_read_b128 v[176:179], v158 offset:33792
	ds_read_b128 v[180:183], v158 offset:34816
	ds_read_b128 v[184:187], v158 offset:35840
	ds_read_b128 v[188:191], v158 offset:36864
	ds_read_b128 v[192:195], v158 offset:37888
	ds_read_b128 v[196:199], v158 offset:38912
	ds_read_b128 v[200:203], v158 offset:39936
	global_load_lds_dwordx4 v240, s[64:65]
	s_mov_b32 m0, s19
	s_nop 0
	global_load_lds_dwordx4 v242, s[64:65]
	s_waitcnt lgkmcnt(0)
	s_waitcnt vmcnt(8)
	s_barrier
	s_setprio 1
	s_waitcnt lgkmcnt(0)
	v_mfma_i32_16x16x64_i8 v[140:143], v[112:115], v[172:175], v[140:143]
	v_mfma_i32_16x16x64_i8 v[132:135], v[120:123], v[172:175], v[132:135]
	v_mfma_i32_16x16x64_i8 v[92:95], v[112:115], v[180:183], v[94:97]
	v_mfma_i32_16x16x64_i8 v[88:91], v[120:123], v[180:183], v[88:91]
	v_mfma_i32_16x16x64_i8 v[60:63], v[112:115], v[188:191], v[60:63]
	v_mfma_i32_16x16x64_i8 v[56:59], v[120:123], v[188:191], v[56:59]
	v_mfma_i32_16x16x64_i8 v[28:31], v[112:115], v[196:199], v[28:31]
	v_mfma_i32_16x16x64_i8 v[24:27], v[120:123], v[196:199], v[24:27]
	v_mfma_i32_16x16x64_i8 v[140:143], v[116:119], v[176:179], v[140:143]
	v_mfma_i32_16x16x64_i8 v[132:135], v[144:147], v[176:179], v[132:135]
	v_mfma_i32_16x16x64_i8 v[96:99], v[116:119], v[184:187], v[92:95]
	v_mfma_i32_16x16x64_i8 v[88:91], v[144:147], v[184:187], v[88:91]
	v_mfma_i32_16x16x64_i8 v[60:63], v[116:119], v[192:195], v[60:63]
	v_mfma_i32_16x16x64_i8 v[56:59], v[144:147], v[192:195], v[56:59]
	v_mfma_i32_16x16x64_i8 v[28:31], v[116:119], v[200:203], v[28:31]
	v_mfma_i32_16x16x64_i8 v[24:27], v[144:147], v[200:203], v[24:27]
	v_mfma_i32_16x16x64_i8 v[92:95], v[150:153], v[172:175], v[124:127]
	v_mfma_i32_16x16x64_i8 v[124:127], v[160:163], v[176:179], v[92:95]
	v_mfma_i32_16x16x64_i8 v[92:95], v[164:167], v[172:175], v[108:111]
	v_mfma_i32_16x16x64_i8 v[76:79], v[150:153], v[180:183], v[76:79]
	v_mfma_i32_16x16x64_i8 v[72:75], v[164:167], v[180:183], v[72:75]
	v_mfma_i32_16x16x64_i8 v[44:47], v[150:153], v[188:191], v[44:47]
	v_mfma_i32_16x16x64_i8 v[40:43], v[164:167], v[188:191], v[40:43]
	v_mfma_i32_16x16x64_i8 v[12:15], v[150:153], v[196:199], v[12:15]
	v_mfma_i32_16x16x64_i8 v[8:11], v[164:167], v[196:199], v[8:11]
	v_mfma_i32_16x16x64_i8 v[108:111], v[168:171], v[176:179], v[92:95]
	v_mfma_i32_16x16x64_i8 v[76:79], v[160:163], v[184:187], v[76:79]
	v_mfma_i32_16x16x64_i8 v[72:75], v[168:171], v[184:187], v[72:75]
	v_mfma_i32_16x16x64_i8 v[44:47], v[160:163], v[192:195], v[44:47]
	v_mfma_i32_16x16x64_i8 v[40:43], v[168:171], v[192:195], v[40:43]
	v_mfma_i32_16x16x64_i8 v[12:15], v[160:163], v[200:203], v[12:15]
	v_mfma_i32_16x16x64_i8 v[8:11], v[168:171], v[200:203], v[8:11]
	s_setprio 0
	s_waitcnt vmcnt(8)
	s_barrier
; #define G_STAGE(bufoff, gbase, voff) do { _Pragma("unroll") for (int _i = 0; _i < 2; ++_i) \
;         __builtin_amdgcn_global_load_lds((const unsigned*)((const char*)(gbase) + (voff)[_i]), (LAS unsigned*)(lds + (bufoff) + ldsw + _i * 8192), 16, 0, 0); } while (0)
; #define G_LDA(dst, b, h) do { _Pragma("unroll") for (int m = 0; m < 4; ++m) G_LD8(dst[m], lds + G_SA(b, h) + aoff + m * 2048); } while (0)
; #define G_WAIT_V(n) asm volatile("s_waitcnt vmcnt(" #n ")" ::: "memory")
; #define G_WAIT_L(n) asm volatile("s_waitcnt lgkmcnt(" #n ")" ::: "memory")
; #define G_BAR __builtin_amdgcn_s_barrier()
; #define G_SCHED __builtin_amdgcn_sched_barrier(0)
;     ...
;             G_LDA(At, 1, 1); G_STAGE(G_SB(1, 0), b02 + kstep, voffB); G_STAGE(G_SB(1, 1), b12 + kstep, voffB); G_STAGE(G_SA(1, 0), a02 + kstep, vA0);
;             G_WAIT_L(0); G_BAR; G_MMA(1, 0, At, B0); G_MMA(1, 1, At, B1); G_WAIT_V(8); G_BAR; G_SCHED;
;         }
	s_add_i32 s64, s66, s97
	v_lshl_add_u64 v[200:201], v[208:209], 0, s[38:39]
	s_mov_b32 m0, s64
	ds_read_b128 v[92:95], v158 offset:49152
	ds_read_b128 v[172:175], v158 offset:50176
	ds_read_b128 v[176:179], v158 offset:51200
	ds_read_b128 v[180:183], v158 offset:52224
	ds_read_b128 v[184:187], v158 offset:53248
	ds_read_b128 v[188:191], v158 offset:54272
	ds_read_b128 v[192:195], v158 offset:55296
	ds_read_b128 v[196:199], v158 offset:56320
	global_load_lds_dwordx4 v[200:201], off
	v_lshl_add_u64 v[200:201], v[210:211], 0, s[38:39]
	s_add_i32 m0, s64, 0x2000
	s_add_i32 s64, s67, s97
	global_load_lds_dwordx4 v[200:201], off
	v_lshl_add_u64 v[200:201], v[212:213], 0, s[38:39]
	s_mov_b32 m0, s64
	s_nop 0
	global_load_lds_dwordx4 v[200:201], off
	v_lshl_add_u64 v[200:201], v[204:205], 0, s[38:39]
	s_add_i32 m0, s64, 0x2000
	s_nop 0
	global_load_lds_dwordx4 v[200:201], off
	v_lshl_add_u64 v[200:201], v[206:207], 0, s[38:39]
	s_mov_b32 m0, s21
	s_nop 0
	global_load_lds_dwordx4 v[200:201], off
	v_lshl_add_u64 v[200:201], v[214:215], 0, s[38:39]
	s_mov_b32 m0, s22
	s_nop 0
	global_load_lds_dwordx4 v[200:201], off
	s_waitcnt lgkmcnt(0)
	s_waitcnt vmcnt(8)
	s_barrier
	s_setprio 1
	s_waitcnt lgkmcnt(0)
	v_mfma_i32_16x16x64_i8 v[136:139], v[112:115], v[92:95], v[136:139]
	v_mfma_i32_16x16x64_i8 v[128:131], v[120:123], v[92:95], v[128:131]
	v_mfma_i32_16x16x64_i8 v[84:87], v[112:115], v[176:179], v[84:87]
	v_mfma_i32_16x16x64_i8 v[80:83], v[120:123], v[176:179], v[80:83]
	v_mfma_i32_16x16x64_i8 v[52:55], v[112:115], v[184:187], v[52:55]
	v_mfma_i32_16x16x64_i8 v[48:51], v[120:123], v[184:187], v[48:51]
	v_mfma_i32_16x16x64_i8 v[20:23], v[112:115], v[192:195], v[20:23]
	v_mfma_i32_16x16x64_i8 v[16:19], v[120:123], v[192:195], v[16:19]
	v_mfma_i32_16x16x64_i8 v[136:139], v[116:119], v[172:175], v[136:139]
	v_mfma_i32_16x16x64_i8 v[128:131], v[144:147], v[172:175], v[128:131]
	v_mfma_i32_16x16x64_i8 v[84:87], v[116:119], v[180:183], v[84:87]
	v_mfma_i32_16x16x64_i8 v[80:83], v[144:147], v[180:183], v[80:83]
	v_mfma_i32_16x16x64_i8 v[52:55], v[116:119], v[188:191], v[52:55]
	v_mfma_i32_16x16x64_i8 v[48:51], v[144:147], v[188:191], v[48:51]
	v_mfma_i32_16x16x64_i8 v[20:23], v[116:119], v[196:199], v[20:23]
	v_mfma_i32_16x16x64_i8 v[16:19], v[144:147], v[196:199], v[16:19]
	v_mfma_i32_16x16x64_i8 v[100:103], v[150:153], v[92:95], v[100:103]
	v_mfma_i32_16x16x64_i8 v[92:95], v[164:167], v[92:95], v[104:107]
	v_mfma_i32_16x16x64_i8 v[68:71], v[150:153], v[176:179], v[68:71]
	v_mfma_i32_16x16x64_i8 v[64:67], v[164:167], v[176:179], v[64:67]
	v_mfma_i32_16x16x64_i8 v[36:39], v[150:153], v[184:187], v[36:39]
	v_mfma_i32_16x16x64_i8 v[32:35], v[164:167], v[184:187], v[32:35]
	v_mfma_i32_16x16x64_i8 v[4:7], v[150:153], v[192:195], v[4:7]
	v_mfma_i32_16x16x64_i8 v[0:3], v[164:167], v[192:195], v[0:3]
	v_mfma_i32_16x16x64_i8 v[116:119], v[160:163], v[172:175], v[100:103]
	v_mfma_i32_16x16x64_i8 v[104:107], v[168:171], v[172:175], v[92:95]
	v_mfma_i32_16x16x64_i8 v[68:71], v[160:163], v[180:183], v[68:71]
	v_mfma_i32_16x16x64_i8 v[64:67], v[168:171], v[180:183], v[64:67]
	v_mfma_i32_16x16x64_i8 v[36:39], v[160:163], v[188:191], v[36:39]
	v_mfma_i32_16x16x64_i8 v[32:35], v[168:171], v[188:191], v[32:35]
	v_mfma_i32_16x16x64_i8 v[4:7], v[160:163], v[196:199], v[4:7]
	v_mfma_i32_16x16x64_i8 v[0:3], v[168:171], v[196:199], v[0:3]
	s_setprio 0
	s_waitcnt vmcnt(8)
	s_barrier
	s_add_u32 s45, s45, 0x100
	s_addc_u32 s59, s59, 0
	s_add_u32 s61, s61, 0x100
	s_addc_u32 s70, s70, 0
	s_add_u32 s71, s71, 0x100
	s_addc_u32 s75, s75, 0
	s_add_u32 s62, s62, 0x100
	s_addc_u32 s63, s63, 0
	s_cmp_ge_i32 s76, s3
	s_mov_b32 s64, s76
	s_cbranch_scc0 .LBB0_284
	v_readlane_b32 s78, v255, 11
	v_readlane_b32 s79, v255, 13
	s_branch .LBB0_289

; #define G_STAGE(bufoff, gbase, voff) do { _Pragma("unroll") for (int _i = 0; _i < 2; ++_i) \
;         __builtin_amdgcn_global_load_lds((const unsigned*)((const char*)(gbase) + (voff)[_i]), (LAS unsigned*)(lds + (bufoff) + ldsw + _i * 8192), 16, 0, 0); } while (0)
; #define G_LDA(dst, b, h) do { _Pragma("unroll") for (int m = 0; m < 4; ++m) G_LD8(dst[m], lds + G_SA(b, h) + aoff + m * 2048); } while (0)
; #define G_LDB(dst, b, h) do { _Pragma("unroll") for (int n = 0; n < 2; ++n) G_LD8(dst[n], lds + G_SB(b, h) + boff + n * 2048); } while (0)
; #define G_WAIT_V(n) asm volatile("s_waitcnt vmcnt(" #n ")" ::: "memory")
; #define G_WAIT_L(n) asm volatile("s_waitcnt lgkmcnt(" #n ")" ::: "memory")
; #define G_BAR __builtin_amdgcn_s_barrier()
; #define G_SCHED __builtin_amdgcn_sched_barrier(0)
;     __device__ __forceinline__ unsigned row_off(const Unit& u, int r, LAS unsigned char* lds) const { return (unsigned)((const LAS int*)(lds + LDS_STAGE + u.q * 4096))[r] * (unsigned)rowbytes; }
;     ...
;             const char* a11 = cur.a1 + (size_t)(t + 1) * kstep;
;             const char* a02 = last ? nxt.a0 : cur.a0 + (size_t)(t + 2) * kstep; const char* a12 = last ? nxt.a1 : cur.a1 + (size_t)(t + 2) * kstep;
;             const char* b02 = last ? nxt.b0 : cur.b0 + (size_t)(t + 2) * kstep; const char* b12 = last ? nxt.b1 : cur.b1 + (size_t)(t + 2) * kstep;
;             G_LDB(B0, 0, 0); G_LDB(B1, 0, 1); G_SCHED; G_LDA(At, 0, 0); G_STAGE(G_SA(1, 1), a11, vA1);
;             if constexpr (GATHER) { if (last) { int tz = tid; asm volatile("" : "+v"(tz));
; #pragma unroll
;                 for (int i = 0; i < 2; ++i) { int R, C; stage_rc(tz * 16 + i * 8192, R, C); gc0[i] = S.row_off(nxt, R, lds) + (unsigned)C * 2u; gc1[i] = S.row_off(nxt, 128 + R, lds) + (unsigned)C * 2u; } } }
;             G_WAIT_L(0); G_BAR; G_MMA(0, 0, At, B0); G_MMA(0, 1, At, B1); G_WAIT_V(8); G_BAR; G_SCHED;
;             G_LDA(At, 0, 1); G_STAGE(G_SB(0, 0), b02, voffB); G_STAGE(G_SB(0, 1), b12, voffB); G_STAGE(G_SA(0, 0), a02, vA0);
;             G_WAIT_L(0); G_BAR; G_MMA(1, 0, At, B0); G_MMA(1, 1, At, B1); G_WAIT_V(8); G_BAR; G_SCHED;
.LBB0_522:
	s_add_i32 s79, s56, 2
	ds_read_b128 v[142:145], v138
	ds_read_b128 v[146:149], v138 offset:1024
	ds_read_b128 v[150:153], v138 offset:2048
	ds_read_b128 v[154:157], v138 offset:3072
	ds_read_b128 v[158:161], v139
	ds_read_b128 v[162:165], v139 offset:1024
	ds_read_b128 v[166:169], v139 offset:2048
	ds_read_b128 v[170:173], v139 offset:3072
	s_add_u32 s80, s54, 0x80
	s_addc_u32 s57, s55, 0
	s_add_i32 s82, s72, s20
	s_add_i32 m0, s27, 0xc000
	s_add_i32 s81, s27, 0xe000
	s_add_i32 s83, s82, 0x2000
	s_cmp_eq_u32 s71, s56
	s_cselect_b32 s56, s48, s80
	s_cselect_b32 s59, s51, s78
	s_cselect_b32 s58, s50, s77
	s_cselect_b32 s61, s45, s63
	s_cselect_b32 s60, s44, s62
	s_cselect_b32 s57, s49, s57
	ds_read_b128 v[174:177], v140
	ds_read_b128 v[178:181], v140 offset:1024
	ds_read_b128 v[182:185], v140 offset:2048
	ds_read_b128 v[186:189], v140 offset:3072
	ds_read_b128 v[190:193], v140 offset:4096
	ds_read_b128 v[194:197], v140 offset:5120
	ds_read_b128 v[198:201], v140 offset:6144
	ds_read_b128 v[202:205], v140 offset:7168
	global_load_lds_dwordx4 v240, s[54:55]
	s_mov_b32 m0, s81
	s_nop 0
	global_load_lds_dwordx4 v242, s[54:55]
	s_waitcnt lgkmcnt(0)
	v_mov_b32_e32 v131, v129
	s_waitcnt vmcnt(8)
	s_barrier
	s_setprio 1
	s_waitcnt lgkmcnt(0)
	v_mfma_f32_16x16x32_bf16 v[124:127], v[142:145], v[174:177], v[124:127]
	v_mfma_f32_16x16x32_bf16 v[120:123], v[150:153], v[174:177], v[120:123]
	v_mfma_f32_16x16x32_bf16 v[92:95], v[142:145], v[182:185], v[92:95]
	v_mfma_f32_16x16x32_bf16 v[88:91], v[150:153], v[182:185], v[88:91]
	v_mfma_f32_16x16x32_bf16 v[60:63], v[142:145], v[190:193], v[60:63]
	v_mfma_f32_16x16x32_bf16 v[56:59], v[150:153], v[190:193], v[56:59]
	v_mfma_f32_16x16x32_bf16 v[28:31], v[142:145], v[198:201], v[28:31]
	v_mfma_f32_16x16x32_bf16 v[24:27], v[150:153], v[198:201], v[24:27]
	v_mfma_f32_16x16x32_bf16 v[124:127], v[146:149], v[178:181], v[124:127]
	v_mfma_f32_16x16x32_bf16 v[120:123], v[154:157], v[178:181], v[120:123]
	v_mfma_f32_16x16x32_bf16 v[92:95], v[146:149], v[186:189], v[92:95]
	v_mfma_f32_16x16x32_bf16 v[88:91], v[154:157], v[186:189], v[88:91]
	v_mfma_f32_16x16x32_bf16 v[60:63], v[146:149], v[194:197], v[60:63]
	v_mfma_f32_16x16x32_bf16 v[56:59], v[154:157], v[194:197], v[56:59]
	v_mfma_f32_16x16x32_bf16 v[28:31], v[146:149], v[202:205], v[28:31]
	v_mfma_f32_16x16x32_bf16 v[24:27], v[154:157], v[202:205], v[24:27]
	v_mfma_f32_16x16x32_bf16 v[112:115], v[158:161], v[174:177], v[112:115]
	v_mfma_f32_16x16x32_bf16 v[104:107], v[166:169], v[174:177], v[104:107]
	v_mfma_f32_16x16x32_bf16 v[80:83], v[158:161], v[182:185], v[80:83]
	v_mfma_f32_16x16x32_bf16 v[72:75], v[166:169], v[182:185], v[72:75]
	v_mfma_f32_16x16x32_bf16 v[48:51], v[158:161], v[190:193], v[48:51]
	v_mfma_f32_16x16x32_bf16 v[40:43], v[166:169], v[190:193], v[40:43]
	v_mfma_f32_16x16x32_bf16 v[16:19], v[158:161], v[198:201], v[16:19]
	v_mfma_f32_16x16x32_bf16 v[8:11], v[166:169], v[198:201], v[8:11]
	v_mfma_f32_16x16x32_bf16 v[112:115], v[162:165], v[178:181], v[112:115]
	v_mfma_f32_16x16x32_bf16 v[104:107], v[170:173], v[178:181], v[104:107]
	v_mfma_f32_16x16x32_bf16 v[80:83], v[162:165], v[186:189], v[80:83]
	v_mfma_f32_16x16x32_bf16 v[72:75], v[170:173], v[186:189], v[72:75]
	v_mfma_f32_16x16x32_bf16 v[48:51], v[162:165], v[194:197], v[48:51]
	v_mfma_f32_16x16x32_bf16 v[40:43], v[170:173], v[194:197], v[40:43]
	v_mfma_f32_16x16x32_bf16 v[16:19], v[162:165], v[202:205], v[16:19]
	v_mfma_f32_16x16x32_bf16 v[8:11], v[170:173], v[202:205], v[8:11]
	s_setprio 0
	s_waitcnt vmcnt(8)
	s_barrier
	s_mov_b32 m0, s82
	ds_read_b128 v[174:177], v140 offset:16384
	ds_read_b128 v[178:181], v140 offset:17408
	ds_read_b128 v[182:185], v140 offset:18432
	ds_read_b128 v[186:189], v140 offset:19456
	ds_read_b128 v[190:193], v140 offset:20480
	ds_read_b128 v[194:197], v140 offset:21504
	ds_read_b128 v[198:201], v140 offset:22528
	ds_read_b128 v[202:205], v140 offset:23552
	v_mov_b32_e32 v133, v129
	global_load_lds_dwordx4 v244, s[60:61]
	v_mov_b32_e32 v207, v129
	s_mov_b32 m0, s83
	v_lshl_add_u64 v[208:209], s[60:61], 0, v[244:245]
	v_lshl_add_u64 v[210:211], s[60:61], 0, v[246:247]
	global_load_lds_dwordx4 v246, s[60:61]
	s_cselect_b32 s61, s47, s75
	s_cselect_b32 s60, s46, s64
	s_add_i32 s80, s73, s20
	s_mov_b32 m0, s80
	v_lshl_add_u64 v[212:213], s[60:61], 0, v[244:245]
	global_load_lds_dwordx4 v244, s[60:61]
	s_add_i32 m0, s80, 0x2000
	v_lshl_add_u64 v[214:215], s[60:61], 0, v[246:247]
	global_load_lds_dwordx4 v246, s[60:61]
	s_mov_b32 m0, s27
	v_lshl_add_u64 v[206:207], s[58:59], 0, v[240:241]
	global_load_lds_dwordx4 v240, s[58:59]
	s_mov_b32 m0, s33
	v_lshl_add_u64 v[216:217], s[58:59], 0, v[242:243]
	global_load_lds_dwordx4 v242, s[58:59]
	s_waitcnt lgkmcnt(0)
	s_waitcnt vmcnt(8)
	s_barrier
; #define G_STAGE(bufoff, gbase, voff) do { _Pragma("unroll") for (int _i = 0; _i < 2; ++_i) \
;         __builtin_amdgcn_global_load_lds((const unsigned*)((const char*)(gbase) + (voff)[_i]), (LAS unsigned*)(lds + (bufoff) + ldsw + _i * 8192), 16, 0, 0); } while (0)
; #define G_LDA(dst, b, h) do { _Pragma("unroll") for (int m = 0; m < 4; ++m) G_LD8(dst[m], lds + G_SA(b, h) + aoff + m * 2048); } while (0)
; #define G_LDB(dst, b, h) do { _Pragma("unroll") for (int n = 0; n < 2; ++n) G_LD8(dst[n], lds + G_SB(b, h) + boff + n * 2048); } while (0)
; #define G_WAIT_V(n) asm volatile("s_waitcnt vmcnt(" #n ")" ::: "memory")
; #define G_WAIT_L(n) asm volatile("s_waitcnt lgkmcnt(" #n ")" ::: "memory")
; #define G_BAR __builtin_amdgcn_s_barrier()
; #define G_SCHED __builtin_amdgcn_sched_barrier(0)
;     ...
;             G_WAIT_L(0); G_BAR; G_MMA(1, 0, At, B0); G_MMA(1, 1, At, B1); G_WAIT_V(8); G_BAR; G_SCHED;
;             G_LDB(B0, 1, 0); G_LDB(B1, 1, 1); G_SCHED; G_LDA(At, 1, 0); G_STAGE(G_SA(0, 1), a12, vA1);
;             G_WAIT_L(0); G_BAR; G_MMA(0, 0, At, B0); G_MMA(0, 1, At, B1); G_WAIT_V(8); G_BAR; G_SCHED;
	s_setprio 1
	s_waitcnt lgkmcnt(0)
	v_mfma_f32_16x16x32_bf16 v[116:119], v[142:145], v[174:177], v[116:119]
	v_mfma_f32_16x16x32_bf16 v[108:111], v[150:153], v[174:177], v[108:111]
	v_mfma_f32_16x16x32_bf16 v[84:87], v[142:145], v[182:185], v[84:87]
	v_mfma_f32_16x16x32_bf16 v[76:79], v[150:153], v[182:185], v[76:79]
	v_mfma_f32_16x16x32_bf16 v[52:55], v[142:145], v[190:193], v[52:55]
	v_mfma_f32_16x16x32_bf16 v[44:47], v[150:153], v[190:193], v[44:47]
	v_mfma_f32_16x16x32_bf16 v[20:23], v[142:145], v[198:201], v[20:23]
	v_mfma_f32_16x16x32_bf16 v[12:15], v[150:153], v[198:201], v[12:15]
	v_mfma_f32_16x16x32_bf16 v[116:119], v[146:149], v[178:181], v[116:119]
	v_mfma_f32_16x16x32_bf16 v[108:111], v[154:157], v[178:181], v[108:111]
	v_mfma_f32_16x16x32_bf16 v[84:87], v[146:149], v[186:189], v[84:87]
	v_mfma_f32_16x16x32_bf16 v[76:79], v[154:157], v[186:189], v[76:79]
	v_mfma_f32_16x16x32_bf16 v[52:55], v[146:149], v[194:197], v[52:55]
	v_mfma_f32_16x16x32_bf16 v[44:47], v[154:157], v[194:197], v[44:47]
	v_mfma_f32_16x16x32_bf16 v[20:23], v[146:149], v[202:205], v[20:23]
	v_mfma_f32_16x16x32_bf16 v[12:15], v[154:157], v[202:205], v[12:15]
	v_mfma_f32_16x16x32_bf16 v[100:103], v[158:161], v[174:177], v[100:103]
	v_mfma_f32_16x16x32_bf16 v[96:99], v[166:169], v[174:177], v[96:99]
	v_mfma_f32_16x16x32_bf16 v[68:71], v[158:161], v[182:185], v[68:71]
	v_mfma_f32_16x16x32_bf16 v[64:67], v[166:169], v[182:185], v[64:67]
	v_mfma_f32_16x16x32_bf16 v[36:39], v[158:161], v[190:193], v[36:39]
	v_mfma_f32_16x16x32_bf16 v[32:35], v[166:169], v[190:193], v[32:35]
	v_mfma_f32_16x16x32_bf16 v[4:7], v[158:161], v[198:201], v[4:7]
	v_mfma_f32_16x16x32_bf16 v[0:3], v[166:169], v[198:201], v[0:3]
	v_mfma_f32_16x16x32_bf16 v[100:103], v[162:165], v[178:181], v[100:103]
	v_mfma_f32_16x16x32_bf16 v[96:99], v[170:173], v[178:181], v[96:99]
	v_mfma_f32_16x16x32_bf16 v[68:71], v[162:165], v[186:189], v[68:71]
	v_mfma_f32_16x16x32_bf16 v[64:67], v[170:173], v[186:189], v[64:67]
	v_mfma_f32_16x16x32_bf16 v[36:39], v[162:165], v[194:197], v[36:39]
	v_mfma_f32_16x16x32_bf16 v[32:35], v[170:173], v[194:197], v[32:35]
	v_mfma_f32_16x16x32_bf16 v[4:7], v[162:165], v[202:205], v[4:7]
	v_mfma_f32_16x16x32_bf16 v[0:3], v[170:173], v[202:205], v[0:3]
	s_setprio 0
	s_waitcnt vmcnt(8)
	s_barrier
	s_add_i32 s58, 0, 0x18000
	v_add_u32_e32 v131, s58, v137
	s_add_i32 s59, 0, 0x1c000
	ds_read_b128 v[142:145], v131
	ds_read_b128 v[146:149], v131 offset:1024
	ds_read_b128 v[150:153], v131 offset:2048
	ds_read_b128 v[154:157], v131 offset:3072
	v_add_u32_e32 v131, s59, v137
	ds_read_b128 v[158:161], v131
	ds_read_b128 v[162:165], v131 offset:1024
	ds_read_b128 v[166:169], v131 offset:2048
	ds_read_b128 v[170:173], v131 offset:3072
	s_mov_b32 m0, s66
	ds_read_b128 v[174:177], v140 offset:32768
	ds_read_b128 v[178:181], v140 offset:33792
	ds_read_b128 v[182:185], v140 offset:34816
	ds_read_b128 v[186:189], v140 offset:35840
	ds_read_b128 v[190:193], v140 offset:36864
	ds_read_b128 v[194:197], v140 offset:37888
	ds_read_b128 v[198:201], v140 offset:38912
	ds_read_b128 v[202:205], v140 offset:39936
	global_load_lds_dwordx4 v240, s[56:57]
	s_mov_b32 m0, s67
	s_nop 0
	global_load_lds_dwordx4 v242, s[56:57]
	s_waitcnt lgkmcnt(0)
	s_waitcnt vmcnt(8)
	s_barrier
	s_setprio 1
	s_waitcnt lgkmcnt(0)
	v_mfma_f32_16x16x32_bf16 v[124:127], v[142:145], v[174:177], v[124:127]
	v_mfma_f32_16x16x32_bf16 v[120:123], v[150:153], v[174:177], v[120:123]
	v_mfma_f32_16x16x32_bf16 v[92:95], v[142:145], v[182:185], v[92:95]
	v_mfma_f32_16x16x32_bf16 v[88:91], v[150:153], v[182:185], v[88:91]
	v_mfma_f32_16x16x32_bf16 v[60:63], v[142:145], v[190:193], v[60:63]
	v_mfma_f32_16x16x32_bf16 v[56:59], v[150:153], v[190:193], v[56:59]
	v_mfma_f32_16x16x32_bf16 v[28:31], v[142:145], v[198:201], v[28:31]
	v_mfma_f32_16x16x32_bf16 v[24:27], v[150:153], v[198:201], v[24:27]
	v_mfma_f32_16x16x32_bf16 v[124:127], v[146:149], v[178:181], v[124:127]
	v_mfma_f32_16x16x32_bf16 v[120:123], v[154:157], v[178:181], v[120:123]
	v_mfma_f32_16x16x32_bf16 v[92:95], v[146:149], v[186:189], v[92:95]
	v_mfma_f32_16x16x32_bf16 v[88:91], v[154:157], v[186:189], v[88:91]
	v_mfma_f32_16x16x32_bf16 v[60:63], v[146:149], v[194:197], v[60:63]
	v_mfma_f32_16x16x32_bf16 v[56:59], v[154:157], v[194:197], v[56:59]
	v_mfma_f32_16x16x32_bf16 v[28:31], v[146:149], v[202:205], v[28:31]
	v_mfma_f32_16x16x32_bf16 v[24:27], v[154:157], v[202:205], v[24:27]
	v_mfma_f32_16x16x32_bf16 v[112:115], v[158:161], v[174:177], v[112:115]
	v_mfma_f32_16x16x32_bf16 v[104:107], v[166:169], v[174:177], v[104:107]
	v_mfma_f32_16x16x32_bf16 v[80:83], v[158:161], v[182:185], v[80:83]
	v_mfma_f32_16x16x32_bf16 v[72:75], v[166:169], v[182:185], v[72:75]
	v_mfma_f32_16x16x32_bf16 v[48:51], v[158:161], v[190:193], v[48:51]
	v_mfma_f32_16x16x32_bf16 v[40:43], v[166:169], v[190:193], v[40:43]
	v_mfma_f32_16x16x32_bf16 v[16:19], v[158:161], v[198:201], v[16:19]
	v_mfma_f32_16x16x32_bf16 v[8:11], v[166:169], v[198:201], v[8:11]
	v_mfma_f32_16x16x32_bf16 v[112:115], v[162:165], v[178:181], v[112:115]
	v_mfma_f32_16x16x32_bf16 v[104:107], v[170:173], v[178:181], v[104:107]
	v_mfma_f32_16x16x32_bf16 v[80:83], v[162:165], v[186:189], v[80:83]
	v_mfma_f32_16x16x32_bf16 v[72:75], v[170:173], v[186:189], v[72:75]
	v_mfma_f32_16x16x32_bf16 v[48:51], v[162:165], v[194:197], v[48:51]
	v_mfma_f32_16x16x32_bf16 v[40:43], v[170:173], v[194:197], v[40:43]
	v_mfma_f32_16x16x32_bf16 v[16:19], v[162:165], v[202:205], v[16:19]
	v_mfma_f32_16x16x32_bf16 v[8:11], v[170:173], v[202:205], v[8:11]
	s_setprio 0
	s_waitcnt vmcnt(8)
	s_barrier
; #define G_STAGE(bufoff, gbase, voff) do { _Pragma("unroll") for (int _i = 0; _i < 2; ++_i) \
;         __builtin_amdgcn_global_load_lds((const unsigned*)((const char*)(gbase) + (voff)[_i]), (LAS unsigned*)(lds + (bufoff) + ldsw + _i * 8192), 16, 0, 0); } while (0)
; #define G_LDA(dst, b, h) do { _Pragma("unroll") for (int m = 0; m < 4; ++m) G_LD8(dst[m], lds + G_SA(b, h) + aoff + m * 2048); } while (0)
; #define G_WAIT_V(n) asm volatile("s_waitcnt vmcnt(" #n ")" ::: "memory")
; #define G_WAIT_L(n) asm volatile("s_waitcnt lgkmcnt(" #n ")" ::: "memory")
; #define G_BAR __builtin_amdgcn_s_barrier()
; #define G_SCHED __builtin_amdgcn_sched_barrier(0)
;     ...
;             G_LDA(At, 1, 1); G_STAGE(G_SB(1, 0), b02 + kstep, voffB); G_STAGE(G_SB(1, 1), b12 + kstep, voffB); G_STAGE(G_SA(1, 0), a02 + kstep, vA0);
;             G_WAIT_L(0); G_BAR; G_MMA(1, 0, At, B0); G_MMA(1, 1, At, B1); G_WAIT_V(8); G_BAR; G_SCHED;
;         }
	s_add_i32 s56, s58, s20
	v_lshl_add_u64 v[202:203], v[208:209], 0, s[40:41]
	s_mov_b32 m0, s56
	ds_read_b128 v[130:133], v140 offset:49152
	ds_read_b128 v[174:177], v140 offset:50176
	ds_read_b128 v[178:181], v140 offset:51200
	ds_read_b128 v[182:185], v140 offset:52224
	ds_read_b128 v[186:189], v140 offset:53248
	ds_read_b128 v[190:193], v140 offset:54272
	ds_read_b128 v[194:197], v140 offset:55296
	ds_read_b128 v[198:201], v140 offset:56320
	global_load_lds_dwordx4 v[202:203], off
	v_lshl_add_u64 v[202:203], v[210:211], 0, s[40:41]
	s_add_i32 m0, s56, 0x2000
	s_add_i32 s56, s59, s20
	global_load_lds_dwordx4 v[202:203], off
	v_lshl_add_u64 v[202:203], v[212:213], 0, s[40:41]
	s_mov_b32 m0, s56
	s_nop 0
	global_load_lds_dwordx4 v[202:203], off
	v_lshl_add_u64 v[202:203], v[214:215], 0, s[40:41]
	s_add_i32 m0, s56, 0x2000
	s_nop 0
	global_load_lds_dwordx4 v[202:203], off
	v_lshl_add_u64 v[202:203], v[206:207], 0, s[40:41]
	s_mov_b32 m0, s69
	s_nop 0
	global_load_lds_dwordx4 v[202:203], off
	v_lshl_add_u64 v[202:203], v[216:217], 0, s[40:41]
	s_mov_b32 m0, s70
	s_nop 0
	global_load_lds_dwordx4 v[202:203], off
	s_waitcnt lgkmcnt(0)
	s_waitcnt vmcnt(8)
	s_barrier
	s_setprio 1
	s_waitcnt lgkmcnt(0)
	v_mfma_f32_16x16x32_bf16 v[116:119], v[142:145], v[130:133], v[116:119]
	v_mfma_f32_16x16x32_bf16 v[108:111], v[150:153], v[130:133], v[108:111]
	v_mfma_f32_16x16x32_bf16 v[84:87], v[142:145], v[178:181], v[84:87]
	v_mfma_f32_16x16x32_bf16 v[76:79], v[150:153], v[178:181], v[76:79]
	v_mfma_f32_16x16x32_bf16 v[52:55], v[142:145], v[186:189], v[52:55]
	v_mfma_f32_16x16x32_bf16 v[44:47], v[150:153], v[186:189], v[44:47]
	v_mfma_f32_16x16x32_bf16 v[20:23], v[142:145], v[194:197], v[20:23]
	v_mfma_f32_16x16x32_bf16 v[12:15], v[150:153], v[194:197], v[12:15]
	v_mfma_f32_16x16x32_bf16 v[116:119], v[146:149], v[174:177], v[116:119]
	v_mfma_f32_16x16x32_bf16 v[108:111], v[154:157], v[174:177], v[108:111]
	v_mfma_f32_16x16x32_bf16 v[84:87], v[146:149], v[182:185], v[84:87]
	v_mfma_f32_16x16x32_bf16 v[76:79], v[154:157], v[182:185], v[76:79]
	v_mfma_f32_16x16x32_bf16 v[52:55], v[146:149], v[190:193], v[52:55]
	v_mfma_f32_16x16x32_bf16 v[44:47], v[154:157], v[190:193], v[44:47]
	v_mfma_f32_16x16x32_bf16 v[20:23], v[146:149], v[198:201], v[20:23]
	v_mfma_f32_16x16x32_bf16 v[12:15], v[154:157], v[198:201], v[12:15]
	v_mfma_f32_16x16x32_bf16 v[100:103], v[158:161], v[130:133], v[100:103]
	v_mfma_f32_16x16x32_bf16 v[96:99], v[166:169], v[130:133], v[96:99]
	v_mfma_f32_16x16x32_bf16 v[68:71], v[158:161], v[178:181], v[68:71]
	v_mfma_f32_16x16x32_bf16 v[64:67], v[166:169], v[178:181], v[64:67]
	v_mfma_f32_16x16x32_bf16 v[36:39], v[158:161], v[186:189], v[36:39]
	v_mfma_f32_16x16x32_bf16 v[32:35], v[166:169], v[186:189], v[32:35]
	v_mfma_f32_16x16x32_bf16 v[4:7], v[158:161], v[194:197], v[4:7]
	v_mfma_f32_16x16x32_bf16 v[0:3], v[166:169], v[194:197], v[0:3]
	v_mfma_f32_16x16x32_bf16 v[100:103], v[162:165], v[174:177], v[100:103]
	v_mfma_f32_16x16x32_bf16 v[96:99], v[170:173], v[174:177], v[96:99]
	v_mfma_f32_16x16x32_bf16 v[68:71], v[162:165], v[182:185], v[68:71]
	v_mfma_f32_16x16x32_bf16 v[64:67], v[170:173], v[182:185], v[64:67]
	v_mfma_f32_16x16x32_bf16 v[36:39], v[162:165], v[190:193], v[36:39]
	v_mfma_f32_16x16x32_bf16 v[32:35], v[170:173], v[190:193], v[32:35]
	v_mfma_f32_16x16x32_bf16 v[4:7], v[162:165], v[198:201], v[4:7]
	v_mfma_f32_16x16x32_bf16 v[0:3], v[170:173], v[198:201], v[0:3]
	s_setprio 0
	s_waitcnt vmcnt(8)
	s_barrier
	s_add_u32 s62, s62, 0x100
	s_addc_u32 s63, s63, 0
	s_add_u32 s64, s64, 0x100
	s_addc_u32 s75, s75, 0
	s_add_u32 s77, s77, 0x100
	s_addc_u32 s78, s78, 0
	s_add_u32 s54, s54, 0x100
	s_addc_u32 s55, s55, 0
	s_cmp_ge_i32 s79, s0
	s_mov_b32 s56, s79
	s_cbranch_scc0 .LBB0_522
	v_readlane_b32 s78, v255, 11
	v_readlane_b32 s79, v255, 13
	s_and_b64 vcc, exec, s[42:43]
	s_cbranch_vccz .LBB0_525

; #define G_STAGE(bufoff, gbase, voff) do { _Pragma("unroll") for (int _i = 0; _i < 2; ++_i) \
;         __builtin_amdgcn_global_load_lds((const unsigned*)((const char*)(gbase) + (voff)[_i]), (LAS unsigned*)(lds + (bufoff) + ldsw + _i * 8192), 16, 0, 0); } while (0)
; #define G_LDA(dst, b, h) do { _Pragma("unroll") for (int m = 0; m < 4; ++m) G_LD8(dst[m], lds + G_SA(b, h) + aoff + m * 2048); } while (0)
; #define G_LDB(dst, b, h) do { _Pragma("unroll") for (int n = 0; n < 2; ++n) G_LD8(dst[n], lds + G_SB(b, h) + boff + n * 2048); } while (0)
; #define G_WAIT_V(n) asm volatile("s_waitcnt vmcnt(" #n ")" ::: "memory")
; #define G_WAIT_L(n) asm volatile("s_waitcnt lgkmcnt(" #n ")" ::: "memory")
; #define G_BAR __builtin_amdgcn_s_barrier()
; #define G_SCHED __builtin_amdgcn_sched_barrier(0)
;     __device__ __forceinline__ unsigned row_off(const Unit& u, int r, LAS unsigned char* lds) const { return (unsigned)((const LAS int*)(lds + LDS_STAGE + u.q * 4096))[r] * (unsigned)rowbytes; }
;     ...
;             const char* a11 = cur.a1 + (size_t)(t + 1) * kstep;
;             const char* a02 = last ? nxt.a0 : cur.a0 + (size_t)(t + 2) * kstep; const char* a12 = last ? nxt.a1 : cur.a1 + (size_t)(t + 2) * kstep;
;             const char* b02 = last ? nxt.b0 : cur.b0 + (size_t)(t + 2) * kstep; const char* b12 = last ? nxt.b1 : cur.b1 + (size_t)(t + 2) * kstep;
;             G_LDB(B0, 0, 0); G_LDB(B1, 0, 1); G_SCHED; G_LDA(At, 0, 0); G_STAGE(G_SA(1, 1), a11, vA1);
;             if constexpr (GATHER) { if (last) { int tz = tid; asm volatile("" : "+v"(tz));
; #pragma unroll
;                 for (int i = 0; i < 2; ++i) { int R, C; stage_rc(tz * 16 + i * 8192, R, C); gc0[i] = S.row_off(nxt, R, lds) + (unsigned)C * 2u; gc1[i] = S.row_off(nxt, 128 + R, lds) + (unsigned)C * 2u; } } }
;             G_WAIT_L(0); G_BAR; G_MMA(0, 0, At, B0); G_MMA(0, 1, At, B1); G_WAIT_V(8); G_BAR; G_SCHED;
;             G_LDA(At, 0, 1); G_STAGE(G_SB(0, 0), b02, voffB); G_STAGE(G_SB(0, 1), b12, voffB); G_STAGE(G_SA(0, 0), a02, vA0);
;             G_WAIT_L(0); G_BAR; G_MMA(1, 0, At, B0); G_MMA(1, 1, At, B1); G_WAIT_V(8); G_BAR; G_SCHED;
.LBB0_549:
	s_add_i32 s80, s58, 2
	ds_read_b128 v[130:133], v138
	ds_read_b128 v[142:145], v138 offset:1024
	ds_read_b128 v[146:149], v138 offset:2048
	ds_read_b128 v[150:153], v138 offset:3072
	ds_read_b128 v[154:157], v139
	ds_read_b128 v[158:161], v139 offset:1024
	ds_read_b128 v[162:165], v139 offset:2048
	ds_read_b128 v[166:169], v139 offset:3072
	s_add_u32 s81, s56, 0x80
	s_addc_u32 s59, s57, 0
	s_add_i32 s83, s75, s20
	s_add_i32 m0, s67, 0xc000
	s_add_i32 s82, s67, 0xe000
	s_add_i32 s84, s83, 0x2000
	s_cmp_eq_u32 s74, s58
	s_cselect_b32 s58, s44, s81
	s_cselect_b32 s61, s43, s79
	s_cselect_b32 s60, s42, s65
	s_cselect_b32 s63, s47, s53
	s_cselect_b32 s62, s46, s41
	s_cselect_b32 s59, s45, s59
	ds_read_b128 v[170:173], v140
	ds_read_b128 v[174:177], v140 offset:1024
	ds_read_b128 v[178:181], v140 offset:2048
	ds_read_b128 v[182:185], v140 offset:3072
	ds_read_b128 v[186:189], v140 offset:4096
	ds_read_b128 v[190:193], v140 offset:5120
	ds_read_b128 v[194:197], v140 offset:6144
	ds_read_b128 v[198:201], v140 offset:7168
	global_load_lds_dwordx4 v240, s[56:57]
	s_mov_b32 m0, s82
	v_mov_b32_e32 v205, v129
	global_load_lds_dwordx4 v242, s[56:57]
	s_waitcnt lgkmcnt(0)
	s_waitcnt vmcnt(8)
	s_barrier
	s_setprio 1
	s_waitcnt lgkmcnt(0)
	v_mfma_f32_16x16x32_bf16 v[124:127], v[130:133], v[170:173], v[124:127]
	v_mfma_f32_16x16x32_bf16 v[120:123], v[146:149], v[170:173], v[120:123]
	v_mfma_f32_16x16x32_bf16 v[108:111], v[130:133], v[178:181], v[108:111]
	v_mfma_f32_16x16x32_bf16 v[104:107], v[146:149], v[178:181], v[104:107]
	v_mfma_f32_16x16x32_bf16 v[92:95], v[130:133], v[186:189], v[92:95]
	v_mfma_f32_16x16x32_bf16 v[88:91], v[146:149], v[186:189], v[88:91]
	v_mfma_f32_16x16x32_bf16 v[76:79], v[130:133], v[194:197], v[76:79]
	v_mfma_f32_16x16x32_bf16 v[72:75], v[146:149], v[194:197], v[72:75]
	v_mfma_f32_16x16x32_bf16 v[124:127], v[142:145], v[174:177], v[124:127]
	v_mfma_f32_16x16x32_bf16 v[120:123], v[150:153], v[174:177], v[120:123]
	v_mfma_f32_16x16x32_bf16 v[108:111], v[142:145], v[182:185], v[108:111]
	v_mfma_f32_16x16x32_bf16 v[104:107], v[150:153], v[182:185], v[104:107]
	v_mfma_f32_16x16x32_bf16 v[92:95], v[142:145], v[190:193], v[92:95]
	v_mfma_f32_16x16x32_bf16 v[88:91], v[150:153], v[190:193], v[88:91]
	v_mfma_f32_16x16x32_bf16 v[76:79], v[142:145], v[198:201], v[76:79]
	v_mfma_f32_16x16x32_bf16 v[72:75], v[150:153], v[198:201], v[72:75]
	v_mfma_f32_16x16x32_bf16 v[116:119], v[154:157], v[170:173], v[116:119]
	v_mfma_f32_16x16x32_bf16 v[112:115], v[162:165], v[170:173], v[112:115]
	v_mfma_f32_16x16x32_bf16 v[100:103], v[154:157], v[178:181], v[100:103]
	v_mfma_f32_16x16x32_bf16 v[96:99], v[162:165], v[178:181], v[96:99]
	v_mfma_f32_16x16x32_bf16 v[84:87], v[154:157], v[186:189], v[84:87]
	v_mfma_f32_16x16x32_bf16 v[80:83], v[162:165], v[186:189], v[80:83]
	v_mfma_f32_16x16x32_bf16 v[68:71], v[154:157], v[194:197], v[68:71]
	v_mfma_f32_16x16x32_bf16 v[64:67], v[162:165], v[194:197], v[64:67]
	v_mfma_f32_16x16x32_bf16 v[116:119], v[158:161], v[174:177], v[116:119]
	v_mfma_f32_16x16x32_bf16 v[112:115], v[166:169], v[174:177], v[112:115]
	v_mfma_f32_16x16x32_bf16 v[100:103], v[158:161], v[182:185], v[100:103]
	v_mfma_f32_16x16x32_bf16 v[96:99], v[166:169], v[182:185], v[96:99]
	v_mfma_f32_16x16x32_bf16 v[84:87], v[158:161], v[190:193], v[84:87]
	v_mfma_f32_16x16x32_bf16 v[80:83], v[166:169], v[190:193], v[80:83]
	v_mfma_f32_16x16x32_bf16 v[68:71], v[158:161], v[198:201], v[68:71]
	v_mfma_f32_16x16x32_bf16 v[64:67], v[166:169], v[198:201], v[64:67]
	s_setprio 0
	s_waitcnt vmcnt(8)
	s_barrier
	s_mov_b32 m0, s83
	ds_read_b128 v[170:173], v140 offset:16384
	ds_read_b128 v[174:177], v140 offset:17408
	ds_read_b128 v[178:181], v140 offset:18432
	ds_read_b128 v[182:185], v140 offset:19456
	ds_read_b128 v[186:189], v140 offset:20480
	ds_read_b128 v[190:193], v140 offset:21504
	ds_read_b128 v[194:197], v140 offset:22528
	ds_read_b128 v[198:201], v140 offset:23552
	global_load_lds_dwordx4 v244, s[62:63]
	s_mov_b32 m0, s84
	s_cselect_b32 s83, s49, s64
	s_cselect_b32 s82, s48, s55
	s_add_i32 s81, s76, s20
	global_load_lds_dwordx4 v246, s[62:63]
	s_mov_b32 m0, s81
	v_mov_b32_e32 v203, v129
	global_load_lds_dwordx4 v244, s[82:83]
	s_add_i32 m0, s81, 0x2000
	v_mov_b32_e32 v207, v129
	global_load_lds_dwordx4 v246, s[82:83]
	s_mov_b32 m0, s67
	v_lshl_add_u64 v[208:209], s[62:63], 0, v[244:245]
	global_load_lds_dwordx4 v240, s[60:61]
	s_mov_b32 m0, s68
	v_lshl_add_u64 v[210:211], s[62:63], 0, v[246:247]
	global_load_lds_dwordx4 v242, s[60:61]
	s_waitcnt lgkmcnt(0)
	v_lshl_add_u64 v[202:203], s[82:83], 0, v[244:245]
	v_lshl_add_u64 v[206:207], s[82:83], 0, v[246:247]
	v_lshl_add_u64 v[212:213], s[60:61], 0, v[240:241]
	v_lshl_add_u64 v[214:215], s[60:61], 0, v[242:243]
	s_waitcnt vmcnt(8)
	s_barrier
; #define G_STAGE(bufoff, gbase, voff) do { _Pragma("unroll") for (int _i = 0; _i < 2; ++_i) \
;         __builtin_amdgcn_global_load_lds((const unsigned*)((const char*)(gbase) + (voff)[_i]), (LAS unsigned*)(lds + (bufoff) + ldsw + _i * 8192), 16, 0, 0); } while (0)
; #define G_LDA(dst, b, h) do { _Pragma("unroll") for (int m = 0; m < 4; ++m) G_LD8(dst[m], lds + G_SA(b, h) + aoff + m * 2048); } while (0)
; #define G_LDB(dst, b, h) do { _Pragma("unroll") for (int n = 0; n < 2; ++n) G_LD8(dst[n], lds + G_SB(b, h) + boff + n * 2048); } while (0)
; #define G_WAIT_V(n) asm volatile("s_waitcnt vmcnt(" #n ")" ::: "memory")
; #define G_WAIT_L(n) asm volatile("s_waitcnt lgkmcnt(" #n ")" ::: "memory")
; #define G_BAR __builtin_amdgcn_s_barrier()
; #define G_SCHED __builtin_amdgcn_sched_barrier(0)
;     ...
;             G_WAIT_L(0); G_BAR; G_MMA(1, 0, At, B0); G_MMA(1, 1, At, B1); G_WAIT_V(8); G_BAR; G_SCHED;
;             G_LDB(B0, 1, 0); G_LDB(B1, 1, 1); G_SCHED; G_LDA(At, 1, 0); G_STAGE(G_SA(0, 1), a12, vA1);
;             G_WAIT_L(0); G_BAR; G_MMA(0, 0, At, B0); G_MMA(0, 1, At, B1); G_WAIT_V(8); G_BAR; G_SCHED;
	s_setprio 1
	s_waitcnt lgkmcnt(0)
	v_mfma_f32_16x16x32_bf16 v[60:63], v[130:133], v[170:173], v[60:63]
	v_mfma_f32_16x16x32_bf16 v[56:59], v[146:149], v[170:173], v[56:59]
	v_mfma_f32_16x16x32_bf16 v[44:47], v[130:133], v[178:181], v[44:47]
	v_mfma_f32_16x16x32_bf16 v[40:43], v[146:149], v[178:181], v[40:43]
	v_mfma_f32_16x16x32_bf16 v[28:31], v[130:133], v[186:189], v[28:31]
	v_mfma_f32_16x16x32_bf16 v[24:27], v[146:149], v[186:189], v[24:27]
	v_mfma_f32_16x16x32_bf16 v[12:15], v[130:133], v[194:197], v[12:15]
	v_mfma_f32_16x16x32_bf16 v[8:11], v[146:149], v[194:197], v[8:11]
	v_mfma_f32_16x16x32_bf16 v[60:63], v[142:145], v[174:177], v[60:63]
	v_mfma_f32_16x16x32_bf16 v[56:59], v[150:153], v[174:177], v[56:59]
	v_mfma_f32_16x16x32_bf16 v[44:47], v[142:145], v[182:185], v[44:47]
	v_mfma_f32_16x16x32_bf16 v[40:43], v[150:153], v[182:185], v[40:43]
	v_mfma_f32_16x16x32_bf16 v[28:31], v[142:145], v[190:193], v[28:31]
	v_mfma_f32_16x16x32_bf16 v[24:27], v[150:153], v[190:193], v[24:27]
	v_mfma_f32_16x16x32_bf16 v[12:15], v[142:145], v[198:201], v[12:15]
	v_mfma_f32_16x16x32_bf16 v[8:11], v[150:153], v[198:201], v[8:11]
	v_mfma_f32_16x16x32_bf16 v[52:55], v[154:157], v[170:173], v[52:55]
	v_mfma_f32_16x16x32_bf16 v[48:51], v[162:165], v[170:173], v[48:51]
	v_mfma_f32_16x16x32_bf16 v[36:39], v[154:157], v[178:181], v[36:39]
	v_mfma_f32_16x16x32_bf16 v[32:35], v[162:165], v[178:181], v[32:35]
	v_mfma_f32_16x16x32_bf16 v[20:23], v[154:157], v[186:189], v[20:23]
	v_mfma_f32_16x16x32_bf16 v[16:19], v[162:165], v[186:189], v[16:19]
	v_mfma_f32_16x16x32_bf16 v[4:7], v[154:157], v[194:197], v[4:7]
	v_mfma_f32_16x16x32_bf16 v[0:3], v[162:165], v[194:197], v[0:3]
	v_mfma_f32_16x16x32_bf16 v[52:55], v[158:161], v[174:177], v[52:55]
	v_mfma_f32_16x16x32_bf16 v[48:51], v[166:169], v[174:177], v[48:51]
	v_mfma_f32_16x16x32_bf16 v[36:39], v[158:161], v[182:185], v[36:39]
	v_mfma_f32_16x16x32_bf16 v[32:35], v[166:169], v[182:185], v[32:35]
	v_mfma_f32_16x16x32_bf16 v[20:23], v[158:161], v[190:193], v[20:23]
	v_mfma_f32_16x16x32_bf16 v[16:19], v[166:169], v[190:193], v[16:19]
	v_mfma_f32_16x16x32_bf16 v[4:7], v[158:161], v[198:201], v[4:7]
	v_mfma_f32_16x16x32_bf16 v[0:3], v[166:169], v[198:201], v[0:3]
	s_setprio 0
	s_waitcnt vmcnt(8)
	s_barrier
	s_add_i32 s60, 0, 0x18000
	v_add_u32_e32 v141, s60, v137
	s_add_i32 s61, 0, 0x1c000
	ds_read_b128 v[130:133], v141
	ds_read_b128 v[142:145], v141 offset:1024
	ds_read_b128 v[146:149], v141 offset:2048
	ds_read_b128 v[150:153], v141 offset:3072
	v_add_u32_e32 v141, s61, v137
	ds_read_b128 v[154:157], v141
	ds_read_b128 v[158:161], v141 offset:1024
	ds_read_b128 v[162:165], v141 offset:2048
	ds_read_b128 v[166:169], v141 offset:3072
	s_mov_b32 m0, s69
	ds_read_b128 v[170:173], v140 offset:32768
	ds_read_b128 v[174:177], v140 offset:33792
	ds_read_b128 v[178:181], v140 offset:34816
	ds_read_b128 v[182:185], v140 offset:35840
	ds_read_b128 v[186:189], v140 offset:36864
	ds_read_b128 v[190:193], v140 offset:37888
	ds_read_b128 v[194:197], v140 offset:38912
	ds_read_b128 v[198:201], v140 offset:39936
	global_load_lds_dwordx4 v240, s[58:59]
	s_mov_b32 m0, s70
	s_nop 0
	global_load_lds_dwordx4 v242, s[58:59]
	s_waitcnt lgkmcnt(0)
	s_waitcnt vmcnt(8)
	s_barrier
	s_setprio 1
	s_waitcnt lgkmcnt(0)
	v_mfma_f32_16x16x32_bf16 v[124:127], v[130:133], v[170:173], v[124:127]
	v_mfma_f32_16x16x32_bf16 v[120:123], v[146:149], v[170:173], v[120:123]
	v_mfma_f32_16x16x32_bf16 v[108:111], v[130:133], v[178:181], v[108:111]
	v_mfma_f32_16x16x32_bf16 v[104:107], v[146:149], v[178:181], v[104:107]
	v_mfma_f32_16x16x32_bf16 v[92:95], v[130:133], v[186:189], v[92:95]
	v_mfma_f32_16x16x32_bf16 v[88:91], v[146:149], v[186:189], v[88:91]
	v_mfma_f32_16x16x32_bf16 v[76:79], v[130:133], v[194:197], v[76:79]
	v_mfma_f32_16x16x32_bf16 v[72:75], v[146:149], v[194:197], v[72:75]
	v_mfma_f32_16x16x32_bf16 v[124:127], v[142:145], v[174:177], v[124:127]
	v_mfma_f32_16x16x32_bf16 v[120:123], v[150:153], v[174:177], v[120:123]
	v_mfma_f32_16x16x32_bf16 v[108:111], v[142:145], v[182:185], v[108:111]
	v_mfma_f32_16x16x32_bf16 v[104:107], v[150:153], v[182:185], v[104:107]
	v_mfma_f32_16x16x32_bf16 v[92:95], v[142:145], v[190:193], v[92:95]
	v_mfma_f32_16x16x32_bf16 v[88:91], v[150:153], v[190:193], v[88:91]
	v_mfma_f32_16x16x32_bf16 v[76:79], v[142:145], v[198:201], v[76:79]
	v_mfma_f32_16x16x32_bf16 v[72:75], v[150:153], v[198:201], v[72:75]
	v_mfma_f32_16x16x32_bf16 v[116:119], v[154:157], v[170:173], v[116:119]
	v_mfma_f32_16x16x32_bf16 v[112:115], v[162:165], v[170:173], v[112:115]
	v_mfma_f32_16x16x32_bf16 v[100:103], v[154:157], v[178:181], v[100:103]
	v_mfma_f32_16x16x32_bf16 v[96:99], v[162:165], v[178:181], v[96:99]
	v_mfma_f32_16x16x32_bf16 v[84:87], v[154:157], v[186:189], v[84:87]
	v_mfma_f32_16x16x32_bf16 v[80:83], v[162:165], v[186:189], v[80:83]
	v_mfma_f32_16x16x32_bf16 v[68:71], v[154:157], v[194:197], v[68:71]
	v_mfma_f32_16x16x32_bf16 v[64:67], v[162:165], v[194:197], v[64:67]
	v_mfma_f32_16x16x32_bf16 v[116:119], v[158:161], v[174:177], v[116:119]
	v_mfma_f32_16x16x32_bf16 v[112:115], v[166:169], v[174:177], v[112:115]
	v_mfma_f32_16x16x32_bf16 v[100:103], v[158:161], v[182:185], v[100:103]
	v_mfma_f32_16x16x32_bf16 v[96:99], v[166:169], v[182:185], v[96:99]
	v_mfma_f32_16x16x32_bf16 v[84:87], v[158:161], v[190:193], v[84:87]
	v_mfma_f32_16x16x32_bf16 v[80:83], v[166:169], v[190:193], v[80:83]
	v_mfma_f32_16x16x32_bf16 v[68:71], v[158:161], v[198:201], v[68:71]
	v_mfma_f32_16x16x32_bf16 v[64:67], v[166:169], v[198:201], v[64:67]
	s_setprio 0
	s_waitcnt vmcnt(8)
	s_barrier
; #define G_STAGE(bufoff, gbase, voff) do { _Pragma("unroll") for (int _i = 0; _i < 2; ++_i) \
;         __builtin_amdgcn_global_load_lds((const unsigned*)((const char*)(gbase) + (voff)[_i]), (LAS unsigned*)(lds + (bufoff) + ldsw + _i * 8192), 16, 0, 0); } while (0)
; #define G_LDA(dst, b, h) do { _Pragma("unroll") for (int m = 0; m < 4; ++m) G_LD8(dst[m], lds + G_SA(b, h) + aoff + m * 2048); } while (0)
; #define G_WAIT_V(n) asm volatile("s_waitcnt vmcnt(" #n ")" ::: "memory")
; #define G_WAIT_L(n) asm volatile("s_waitcnt lgkmcnt(" #n ")" ::: "memory")
; #define G_BAR __builtin_amdgcn_s_barrier()
; #define G_SCHED __builtin_amdgcn_sched_barrier(0)
;     ...
;             G_LDA(At, 1, 1); G_STAGE(G_SB(1, 0), b02 + kstep, voffB); G_STAGE(G_SB(1, 1), b12 + kstep, voffB); G_STAGE(G_SA(1, 0), a02 + kstep, vA0);
;             G_WAIT_L(0); G_BAR; G_MMA(1, 0, At, B0); G_MMA(1, 1, At, B1); G_WAIT_V(8); G_BAR; G_SCHED;
;         }
	s_add_i32 s58, s60, s20
	v_lshl_add_u64 v[204:205], v[208:209], 0, s[8:9]
	s_mov_b32 m0, s58
	ds_read_b128 v[170:173], v140 offset:49152
	ds_read_b128 v[174:177], v140 offset:50176
	ds_read_b128 v[178:181], v140 offset:51200
	ds_read_b128 v[182:185], v140 offset:52224
	ds_read_b128 v[186:189], v140 offset:53248
	ds_read_b128 v[190:193], v140 offset:54272
	ds_read_b128 v[194:197], v140 offset:55296
	ds_read_b128 v[198:201], v140 offset:56320
	global_load_lds_dwordx4 v[204:205], off
	v_lshl_add_u64 v[204:205], v[210:211], 0, s[8:9]
	s_add_i32 m0, s58, 0x2000
	s_add_i32 s58, s61, s20
	global_load_lds_dwordx4 v[204:205], off
	v_lshl_add_u64 v[202:203], v[202:203], 0, s[8:9]
	s_mov_b32 m0, s58
	s_nop 0
	global_load_lds_dwordx4 v[202:203], off
	v_lshl_add_u64 v[202:203], v[206:207], 0, s[8:9]
	s_add_i32 m0, s58, 0x2000
	s_nop 0
	global_load_lds_dwordx4 v[202:203], off
	v_lshl_add_u64 v[202:203], v[212:213], 0, s[8:9]
	s_mov_b32 m0, s72
	s_nop 0
	global_load_lds_dwordx4 v[202:203], off
	v_lshl_add_u64 v[202:203], v[214:215], 0, s[8:9]
	s_mov_b32 m0, s73
	s_nop 0
	global_load_lds_dwordx4 v[202:203], off
	s_waitcnt lgkmcnt(0)
	s_waitcnt vmcnt(8)
	s_barrier
	s_setprio 1
	s_waitcnt lgkmcnt(0)
	v_mfma_f32_16x16x32_bf16 v[60:63], v[130:133], v[170:173], v[60:63]
	v_mfma_f32_16x16x32_bf16 v[56:59], v[146:149], v[170:173], v[56:59]
	v_mfma_f32_16x16x32_bf16 v[44:47], v[130:133], v[178:181], v[44:47]
	v_mfma_f32_16x16x32_bf16 v[40:43], v[146:149], v[178:181], v[40:43]
	v_mfma_f32_16x16x32_bf16 v[28:31], v[130:133], v[186:189], v[28:31]
	v_mfma_f32_16x16x32_bf16 v[24:27], v[146:149], v[186:189], v[24:27]
	v_mfma_f32_16x16x32_bf16 v[12:15], v[130:133], v[194:197], v[12:15]
	v_mfma_f32_16x16x32_bf16 v[8:11], v[146:149], v[194:197], v[8:11]
	v_mfma_f32_16x16x32_bf16 v[60:63], v[142:145], v[174:177], v[60:63]
	v_mfma_f32_16x16x32_bf16 v[56:59], v[150:153], v[174:177], v[56:59]
	v_mfma_f32_16x16x32_bf16 v[44:47], v[142:145], v[182:185], v[44:47]
	v_mfma_f32_16x16x32_bf16 v[40:43], v[150:153], v[182:185], v[40:43]
	v_mfma_f32_16x16x32_bf16 v[28:31], v[142:145], v[190:193], v[28:31]
	v_mfma_f32_16x16x32_bf16 v[24:27], v[150:153], v[190:193], v[24:27]
	v_mfma_f32_16x16x32_bf16 v[12:15], v[142:145], v[198:201], v[12:15]
	v_mfma_f32_16x16x32_bf16 v[8:11], v[150:153], v[198:201], v[8:11]
	v_mfma_f32_16x16x32_bf16 v[52:55], v[154:157], v[170:173], v[52:55]
	v_mfma_f32_16x16x32_bf16 v[48:51], v[162:165], v[170:173], v[48:51]
	v_mfma_f32_16x16x32_bf16 v[36:39], v[154:157], v[178:181], v[36:39]
	v_mfma_f32_16x16x32_bf16 v[32:35], v[162:165], v[178:181], v[32:35]
	v_mfma_f32_16x16x32_bf16 v[20:23], v[154:157], v[186:189], v[20:23]
	v_mfma_f32_16x16x32_bf16 v[16:19], v[162:165], v[186:189], v[16:19]
	v_mfma_f32_16x16x32_bf16 v[4:7], v[154:157], v[194:197], v[4:7]
	v_mfma_f32_16x16x32_bf16 v[0:3], v[162:165], v[194:197], v[0:3]
	v_mfma_f32_16x16x32_bf16 v[52:55], v[158:161], v[174:177], v[52:55]
	v_mfma_f32_16x16x32_bf16 v[48:51], v[166:169], v[174:177], v[48:51]
	v_mfma_f32_16x16x32_bf16 v[36:39], v[158:161], v[182:185], v[36:39]
	v_mfma_f32_16x16x32_bf16 v[32:35], v[166:169], v[182:185], v[32:35]
	v_mfma_f32_16x16x32_bf16 v[20:23], v[158:161], v[190:193], v[20:23]
	v_mfma_f32_16x16x32_bf16 v[16:19], v[166:169], v[190:193], v[16:19]
	v_mfma_f32_16x16x32_bf16 v[4:7], v[158:161], v[198:201], v[4:7]
	v_mfma_f32_16x16x32_bf16 v[0:3], v[166:169], v[198:201], v[0:3]
	s_setprio 0
	s_waitcnt vmcnt(8)
	s_barrier
	s_add_u32 s41, s41, 0x100
	s_addc_u32 s53, s53, 0
	s_add_u32 s55, s55, 0x100
	s_addc_u32 s64, s64, 0
	s_add_u32 s65, s65, 0x100
	s_addc_u32 s79, s79, 0
	s_add_u32 s56, s56, 0x100
	s_addc_u32 s57, s57, 0
	s_cmp_ge_i32 s80, s0
	s_mov_b32 s58, s80
	s_cbranch_scc0 .LBB0_549
	v_readlane_b32 s79, v255, 13
	s_and_b64 vcc, exec, s[38:39]
	s_cbranch_vccz .LBB0_552

; #define G_STAGE(bufoff, gbase, voff) do { _Pragma("unroll") for (int _i = 0; _i < 2; ++_i) \
;         __builtin_amdgcn_global_load_lds((const unsigned*)((const char*)(gbase) + (voff)[_i]), (LAS unsigned*)(lds + (bufoff) + ldsw + _i * 8192), 16, 0, 0); } while (0)
; #define G_LDA(dst, b, h) do { _Pragma("unroll") for (int m = 0; m < 4; ++m) G_LD8(dst[m], lds + G_SA(b, h) + aoff + m * 2048); } while (0)
; #define G_LDB(dst, b, h) do { _Pragma("unroll") for (int n = 0; n < 2; ++n) G_LD8(dst[n], lds + G_SB(b, h) + boff + n * 2048); } while (0)
; #define G_WAIT_V(n) asm volatile("s_waitcnt vmcnt(" #n ")" ::: "memory")
; #define G_WAIT_L(n) asm volatile("s_waitcnt lgkmcnt(" #n ")" ::: "memory")
; #define G_BAR __builtin_amdgcn_s_barrier()
; #define G_SCHED __builtin_amdgcn_sched_barrier(0)
;     __device__ __forceinline__ unsigned row_off(const Unit& u, int r, LAS unsigned char* lds) const { return (unsigned)((const LAS int*)(lds + LDS_STAGE + u.q * 4096))[r] * (unsigned)rowbytes; }
;     ...
;             const char* a11 = cur.a1 + (size_t)(t + 1) * kstep;
;             const char* a02 = last ? nxt.a0 : cur.a0 + (size_t)(t + 2) * kstep; const char* a12 = last ? nxt.a1 : cur.a1 + (size_t)(t + 2) * kstep;
;             const char* b02 = last ? nxt.b0 : cur.b0 + (size_t)(t + 2) * kstep; const char* b12 = last ? nxt.b1 : cur.b1 + (size_t)(t + 2) * kstep;
;             G_LDB(B0, 0, 0); G_LDB(B1, 0, 1); G_SCHED; G_LDA(At, 0, 0); G_STAGE(G_SA(1, 1), a11, vA1);
;             if constexpr (GATHER) { if (last) { int tz = tid; asm volatile("" : "+v"(tz));
; #pragma unroll
;                 for (int i = 0; i < 2; ++i) { int R, C; stage_rc(tz * 16 + i * 8192, R, C); gc0[i] = S.row_off(nxt, R, lds) + (unsigned)C * 2u; gc1[i] = S.row_off(nxt, 128 + R, lds) + (unsigned)C * 2u; } } }
;             G_WAIT_L(0); G_BAR; G_MMA(0, 0, At, B0); G_MMA(0, 1, At, B1); G_WAIT_V(8); G_BAR; G_SCHED;
;             G_LDA(At, 0, 1); G_STAGE(G_SB(0, 0), b02, voffB); G_STAGE(G_SB(0, 1), b12, voffB); G_STAGE(G_SA(0, 0), a02, vA0);
;             G_WAIT_L(0); G_BAR; G_MMA(1, 0, At, B0); G_MMA(1, 1, At, B1); G_WAIT_V(8); G_BAR; G_SCHED;
.LBB0_576:
	s_add_i32 s71, s52, 2
	ds_read_b128 v[138:141], v134
	ds_read_b128 v[142:145], v134 offset:1024
	ds_read_b128 v[146:149], v134 offset:2048
	ds_read_b128 v[150:153], v134 offset:3072
	ds_read_b128 v[154:157], v135
	ds_read_b128 v[158:161], v135 offset:1024
	ds_read_b128 v[162:165], v135 offset:2048
	ds_read_b128 v[166:169], v135 offset:3072
	s_add_u32 s72, s50, 0x80
	s_addc_u32 s53, s51, 0
	s_add_i32 s75, s22, s20
	s_add_i32 m0, s62, 0xc000
	s_add_i32 s74, s62, 0xe000
	s_add_i32 s76, s75, 0x2000
	s_cmp_eq_u32 s23, s52
	s_cselect_b32 s52, s38, s72
	s_cselect_b32 s55, s37, s70
	s_cselect_b32 s54, s36, s59
	s_cselect_b32 s57, s41, s45
	s_cselect_b32 s56, s40, s35
	s_cselect_b32 s53, s39, s53
	ds_read_b128 v[170:173], v136
	ds_read_b128 v[174:177], v136 offset:1024
	ds_read_b128 v[178:181], v136 offset:2048
	ds_read_b128 v[182:185], v136 offset:3072
	ds_read_b128 v[186:189], v136 offset:4096
	ds_read_b128 v[190:193], v136 offset:5120
	ds_read_b128 v[194:197], v136 offset:6144
	ds_read_b128 v[198:201], v136 offset:7168
	global_load_lds_dwordx4 v240, s[50:51]
	s_mov_b32 m0, s74
	v_mov_b32_e32 v205, v129
	global_load_lds_dwordx4 v242, s[50:51]
	s_waitcnt lgkmcnt(0)
	s_waitcnt vmcnt(8)
	s_barrier
	s_setprio 1
	s_waitcnt lgkmcnt(0)
	v_mfma_f32_16x16x32_bf16 v[124:127], v[138:141], v[170:173], v[124:127]
	v_mfma_f32_16x16x32_bf16 v[120:123], v[146:149], v[170:173], v[120:123]
	v_mfma_f32_16x16x32_bf16 v[108:111], v[138:141], v[178:181], v[108:111]
	v_mfma_f32_16x16x32_bf16 v[104:107], v[146:149], v[178:181], v[104:107]
	v_mfma_f32_16x16x32_bf16 v[92:95], v[138:141], v[186:189], v[92:95]
	v_mfma_f32_16x16x32_bf16 v[88:91], v[146:149], v[186:189], v[88:91]
	v_mfma_f32_16x16x32_bf16 v[76:79], v[138:141], v[194:197], v[76:79]
	v_mfma_f32_16x16x32_bf16 v[72:75], v[146:149], v[194:197], v[72:75]
	v_mfma_f32_16x16x32_bf16 v[124:127], v[142:145], v[174:177], v[124:127]
	v_mfma_f32_16x16x32_bf16 v[120:123], v[150:153], v[174:177], v[120:123]
	v_mfma_f32_16x16x32_bf16 v[108:111], v[142:145], v[182:185], v[108:111]
	v_mfma_f32_16x16x32_bf16 v[104:107], v[150:153], v[182:185], v[104:107]
	v_mfma_f32_16x16x32_bf16 v[92:95], v[142:145], v[190:193], v[92:95]
	v_mfma_f32_16x16x32_bf16 v[88:91], v[150:153], v[190:193], v[88:91]
	v_mfma_f32_16x16x32_bf16 v[76:79], v[142:145], v[198:201], v[76:79]
	v_mfma_f32_16x16x32_bf16 v[72:75], v[150:153], v[198:201], v[72:75]
	v_mfma_f32_16x16x32_bf16 v[116:119], v[154:157], v[170:173], v[116:119]
	v_mfma_f32_16x16x32_bf16 v[112:115], v[162:165], v[170:173], v[112:115]
	v_mfma_f32_16x16x32_bf16 v[100:103], v[154:157], v[178:181], v[100:103]
	v_mfma_f32_16x16x32_bf16 v[96:99], v[162:165], v[178:181], v[96:99]
	v_mfma_f32_16x16x32_bf16 v[84:87], v[154:157], v[186:189], v[84:87]
	v_mfma_f32_16x16x32_bf16 v[80:83], v[162:165], v[186:189], v[80:83]
	v_mfma_f32_16x16x32_bf16 v[68:71], v[154:157], v[194:197], v[68:71]
	v_mfma_f32_16x16x32_bf16 v[64:67], v[162:165], v[194:197], v[64:67]
	v_mfma_f32_16x16x32_bf16 v[116:119], v[158:161], v[174:177], v[116:119]
	v_mfma_f32_16x16x32_bf16 v[112:115], v[166:169], v[174:177], v[112:115]
	v_mfma_f32_16x16x32_bf16 v[100:103], v[158:161], v[182:185], v[100:103]
	v_mfma_f32_16x16x32_bf16 v[96:99], v[166:169], v[182:185], v[96:99]
	v_mfma_f32_16x16x32_bf16 v[84:87], v[158:161], v[190:193], v[84:87]
	v_mfma_f32_16x16x32_bf16 v[80:83], v[166:169], v[190:193], v[80:83]
	v_mfma_f32_16x16x32_bf16 v[68:71], v[158:161], v[198:201], v[68:71]
	v_mfma_f32_16x16x32_bf16 v[64:67], v[166:169], v[198:201], v[64:67]
	s_setprio 0
	s_waitcnt vmcnt(8)
	s_barrier
	s_mov_b32 m0, s75
	ds_read_b128 v[170:173], v136 offset:16384
	ds_read_b128 v[174:177], v136 offset:17408
	ds_read_b128 v[178:181], v136 offset:18432
	ds_read_b128 v[182:185], v136 offset:19456
	ds_read_b128 v[186:189], v136 offset:20480
	ds_read_b128 v[190:193], v136 offset:21504
	ds_read_b128 v[194:197], v136 offset:22528
	ds_read_b128 v[198:201], v136 offset:23552
	global_load_lds_dwordx4 v244, s[56:57]
	s_mov_b32 m0, s76
	s_cselect_b32 s73, s43, s58
	s_cselect_b32 s72, s42, s49
	s_add_i32 s74, s24, s20
	global_load_lds_dwordx4 v246, s[56:57]
	s_mov_b32 m0, s74
	v_mov_b32_e32 v203, v129
	global_load_lds_dwordx4 v244, s[72:73]
	s_add_i32 m0, s74, 0x2000
	v_mov_b32_e32 v207, v129
	global_load_lds_dwordx4 v246, s[72:73]
	s_mov_b32 m0, s62
	v_lshl_add_u64 v[208:209], s[56:57], 0, v[244:245]
	global_load_lds_dwordx4 v240, s[54:55]
	s_mov_b32 m0, s63
	v_lshl_add_u64 v[210:211], s[56:57], 0, v[246:247]
	global_load_lds_dwordx4 v242, s[54:55]
	s_waitcnt lgkmcnt(0)
	v_lshl_add_u64 v[202:203], s[72:73], 0, v[244:245]
	v_lshl_add_u64 v[206:207], s[72:73], 0, v[246:247]
	v_lshl_add_u64 v[212:213], s[54:55], 0, v[240:241]
	v_lshl_add_u64 v[214:215], s[54:55], 0, v[242:243]
	s_waitcnt vmcnt(8)
	s_barrier
; #define G_STAGE(bufoff, gbase, voff) do { _Pragma("unroll") for (int _i = 0; _i < 2; ++_i) \
;         __builtin_amdgcn_global_load_lds((const unsigned*)((const char*)(gbase) + (voff)[_i]), (LAS unsigned*)(lds + (bufoff) + ldsw + _i * 8192), 16, 0, 0); } while (0)
; #define G_LDA(dst, b, h) do { _Pragma("unroll") for (int m = 0; m < 4; ++m) G_LD8(dst[m], lds + G_SA(b, h) + aoff + m * 2048); } while (0)
; #define G_LDB(dst, b, h) do { _Pragma("unroll") for (int n = 0; n < 2; ++n) G_LD8(dst[n], lds + G_SB(b, h) + boff + n * 2048); } while (0)
; #define G_WAIT_V(n) asm volatile("s_waitcnt vmcnt(" #n ")" ::: "memory")
; #define G_WAIT_L(n) asm volatile("s_waitcnt lgkmcnt(" #n ")" ::: "memory")
; #define G_BAR __builtin_amdgcn_s_barrier()
; #define G_SCHED __builtin_amdgcn_sched_barrier(0)
;     ...
;             G_WAIT_L(0); G_BAR; G_MMA(1, 0, At, B0); G_MMA(1, 1, At, B1); G_WAIT_V(8); G_BAR; G_SCHED;
;             G_LDB(B0, 1, 0); G_LDB(B1, 1, 1); G_SCHED; G_LDA(At, 1, 0); G_STAGE(G_SA(0, 1), a12, vA1);
;             G_WAIT_L(0); G_BAR; G_MMA(0, 0, At, B0); G_MMA(0, 1, At, B1); G_WAIT_V(8); G_BAR; G_SCHED;
	s_setprio 1
	s_waitcnt lgkmcnt(0)
	v_mfma_f32_16x16x32_bf16 v[60:63], v[138:141], v[170:173], v[60:63]
	v_mfma_f32_16x16x32_bf16 v[56:59], v[146:149], v[170:173], v[56:59]
	v_mfma_f32_16x16x32_bf16 v[44:47], v[138:141], v[178:181], v[44:47]
	v_mfma_f32_16x16x32_bf16 v[40:43], v[146:149], v[178:181], v[40:43]
	v_mfma_f32_16x16x32_bf16 v[28:31], v[138:141], v[186:189], v[28:31]
	v_mfma_f32_16x16x32_bf16 v[24:27], v[146:149], v[186:189], v[24:27]
	v_mfma_f32_16x16x32_bf16 v[12:15], v[138:141], v[194:197], v[12:15]
	v_mfma_f32_16x16x32_bf16 v[8:11], v[146:149], v[194:197], v[8:11]
	v_mfma_f32_16x16x32_bf16 v[60:63], v[142:145], v[174:177], v[60:63]
	v_mfma_f32_16x16x32_bf16 v[56:59], v[150:153], v[174:177], v[56:59]
	v_mfma_f32_16x16x32_bf16 v[44:47], v[142:145], v[182:185], v[44:47]
	v_mfma_f32_16x16x32_bf16 v[40:43], v[150:153], v[182:185], v[40:43]
	v_mfma_f32_16x16x32_bf16 v[28:31], v[142:145], v[190:193], v[28:31]
	v_mfma_f32_16x16x32_bf16 v[24:27], v[150:153], v[190:193], v[24:27]
	v_mfma_f32_16x16x32_bf16 v[12:15], v[142:145], v[198:201], v[12:15]
	v_mfma_f32_16x16x32_bf16 v[8:11], v[150:153], v[198:201], v[8:11]
	v_mfma_f32_16x16x32_bf16 v[52:55], v[154:157], v[170:173], v[52:55]
	v_mfma_f32_16x16x32_bf16 v[48:51], v[162:165], v[170:173], v[48:51]
	v_mfma_f32_16x16x32_bf16 v[36:39], v[154:157], v[178:181], v[36:39]
	v_mfma_f32_16x16x32_bf16 v[32:35], v[162:165], v[178:181], v[32:35]
	v_mfma_f32_16x16x32_bf16 v[20:23], v[154:157], v[186:189], v[20:23]
	v_mfma_f32_16x16x32_bf16 v[16:19], v[162:165], v[186:189], v[16:19]
	v_mfma_f32_16x16x32_bf16 v[4:7], v[154:157], v[194:197], v[4:7]
	v_mfma_f32_16x16x32_bf16 v[0:3], v[162:165], v[194:197], v[0:3]
	v_mfma_f32_16x16x32_bf16 v[52:55], v[158:161], v[174:177], v[52:55]
	v_mfma_f32_16x16x32_bf16 v[48:51], v[166:169], v[174:177], v[48:51]
	v_mfma_f32_16x16x32_bf16 v[36:39], v[158:161], v[182:185], v[36:39]
	v_mfma_f32_16x16x32_bf16 v[32:35], v[166:169], v[182:185], v[32:35]
	v_mfma_f32_16x16x32_bf16 v[20:23], v[158:161], v[190:193], v[20:23]
	v_mfma_f32_16x16x32_bf16 v[16:19], v[166:169], v[190:193], v[16:19]
	v_mfma_f32_16x16x32_bf16 v[4:7], v[158:161], v[198:201], v[4:7]
	v_mfma_f32_16x16x32_bf16 v[0:3], v[166:169], v[198:201], v[0:3]
	s_setprio 0
	s_waitcnt vmcnt(8)
	s_barrier
	s_add_i32 s54, 0, 0x18000
	v_add_u32_e32 v137, s54, v133
	s_add_i32 s55, 0, 0x1c000
	ds_read_b128 v[138:141], v137
	ds_read_b128 v[142:145], v137 offset:1024
	ds_read_b128 v[146:149], v137 offset:2048
	ds_read_b128 v[150:153], v137 offset:3072
	v_add_u32_e32 v137, s55, v133
	ds_read_b128 v[154:157], v137
	ds_read_b128 v[158:161], v137 offset:1024
	ds_read_b128 v[162:165], v137 offset:2048
	ds_read_b128 v[166:169], v137 offset:3072
	s_mov_b32 m0, s64
	ds_read_b128 v[170:173], v136 offset:32768
	ds_read_b128 v[174:177], v136 offset:33792
	ds_read_b128 v[178:181], v136 offset:34816
	ds_read_b128 v[182:185], v136 offset:35840
	ds_read_b128 v[186:189], v136 offset:36864
	ds_read_b128 v[190:193], v136 offset:37888
	ds_read_b128 v[194:197], v136 offset:38912
	ds_read_b128 v[198:201], v136 offset:39936
	global_load_lds_dwordx4 v240, s[52:53]
	s_mov_b32 m0, s65
	s_nop 0
	global_load_lds_dwordx4 v242, s[52:53]
	s_waitcnt lgkmcnt(0)
	s_waitcnt vmcnt(8)
	s_barrier
	s_setprio 1
	s_waitcnt lgkmcnt(0)
	v_mfma_f32_16x16x32_bf16 v[124:127], v[138:141], v[170:173], v[124:127]
	v_mfma_f32_16x16x32_bf16 v[120:123], v[146:149], v[170:173], v[120:123]
	v_mfma_f32_16x16x32_bf16 v[108:111], v[138:141], v[178:181], v[108:111]
	v_mfma_f32_16x16x32_bf16 v[104:107], v[146:149], v[178:181], v[104:107]
	v_mfma_f32_16x16x32_bf16 v[92:95], v[138:141], v[186:189], v[92:95]
	v_mfma_f32_16x16x32_bf16 v[88:91], v[146:149], v[186:189], v[88:91]
	v_mfma_f32_16x16x32_bf16 v[76:79], v[138:141], v[194:197], v[76:79]
	v_mfma_f32_16x16x32_bf16 v[72:75], v[146:149], v[194:197], v[72:75]
	v_mfma_f32_16x16x32_bf16 v[124:127], v[142:145], v[174:177], v[124:127]
	v_mfma_f32_16x16x32_bf16 v[120:123], v[150:153], v[174:177], v[120:123]
	v_mfma_f32_16x16x32_bf16 v[108:111], v[142:145], v[182:185], v[108:111]
	v_mfma_f32_16x16x32_bf16 v[104:107], v[150:153], v[182:185], v[104:107]
	v_mfma_f32_16x16x32_bf16 v[92:95], v[142:145], v[190:193], v[92:95]
	v_mfma_f32_16x16x32_bf16 v[88:91], v[150:153], v[190:193], v[88:91]
	v_mfma_f32_16x16x32_bf16 v[76:79], v[142:145], v[198:201], v[76:79]
	v_mfma_f32_16x16x32_bf16 v[72:75], v[150:153], v[198:201], v[72:75]
	v_mfma_f32_16x16x32_bf16 v[116:119], v[154:157], v[170:173], v[116:119]
	v_mfma_f32_16x16x32_bf16 v[112:115], v[162:165], v[170:173], v[112:115]
	v_mfma_f32_16x16x32_bf16 v[100:103], v[154:157], v[178:181], v[100:103]
	v_mfma_f32_16x16x32_bf16 v[96:99], v[162:165], v[178:181], v[96:99]
	v_mfma_f32_16x16x32_bf16 v[84:87], v[154:157], v[186:189], v[84:87]
	v_mfma_f32_16x16x32_bf16 v[80:83], v[162:165], v[186:189], v[80:83]
	v_mfma_f32_16x16x32_bf16 v[68:71], v[154:157], v[194:197], v[68:71]
	v_mfma_f32_16x16x32_bf16 v[64:67], v[162:165], v[194:197], v[64:67]
	v_mfma_f32_16x16x32_bf16 v[116:119], v[158:161], v[174:177], v[116:119]
	v_mfma_f32_16x16x32_bf16 v[112:115], v[166:169], v[174:177], v[112:115]
	v_mfma_f32_16x16x32_bf16 v[100:103], v[158:161], v[182:185], v[100:103]
	v_mfma_f32_16x16x32_bf16 v[96:99], v[166:169], v[182:185], v[96:99]
	v_mfma_f32_16x16x32_bf16 v[84:87], v[158:161], v[190:193], v[84:87]
	v_mfma_f32_16x16x32_bf16 v[80:83], v[166:169], v[190:193], v[80:83]
	v_mfma_f32_16x16x32_bf16 v[68:71], v[158:161], v[198:201], v[68:71]
	v_mfma_f32_16x16x32_bf16 v[64:67], v[166:169], v[198:201], v[64:67]
	s_setprio 0
	s_waitcnt vmcnt(8)
	s_barrier
; #define G_STAGE(bufoff, gbase, voff) do { _Pragma("unroll") for (int _i = 0; _i < 2; ++_i) \
;         __builtin_amdgcn_global_load_lds((const unsigned*)((const char*)(gbase) + (voff)[_i]), (LAS unsigned*)(lds + (bufoff) + ldsw + _i * 8192), 16, 0, 0); } while (0)
; #define G_LDA(dst, b, h) do { _Pragma("unroll") for (int m = 0; m < 4; ++m) G_LD8(dst[m], lds + G_SA(b, h) + aoff + m * 2048); } while (0)
; #define G_WAIT_V(n) asm volatile("s_waitcnt vmcnt(" #n ")" ::: "memory")
; #define G_WAIT_L(n) asm volatile("s_waitcnt lgkmcnt(" #n ")" ::: "memory")
; #define G_BAR __builtin_amdgcn_s_barrier()
; #define G_SCHED __builtin_amdgcn_sched_barrier(0)
;     ...
;             G_LDA(At, 1, 1); G_STAGE(G_SB(1, 0), b02 + kstep, voffB); G_STAGE(G_SB(1, 1), b12 + kstep, voffB); G_STAGE(G_SA(1, 0), a02 + kstep, vA0);
;             G_WAIT_L(0); G_BAR; G_MMA(1, 0, At, B0); G_MMA(1, 1, At, B1); G_WAIT_V(8); G_BAR; G_SCHED;
;         }
	s_add_i32 s52, s54, s20
	v_lshl_add_u64 v[204:205], v[208:209], 0, s[6:7]
	s_mov_b32 m0, s52
	ds_read_b128 v[170:173], v136 offset:49152
	ds_read_b128 v[174:177], v136 offset:50176
	ds_read_b128 v[178:181], v136 offset:51200
	ds_read_b128 v[182:185], v136 offset:52224
	ds_read_b128 v[186:189], v136 offset:53248
	ds_read_b128 v[190:193], v136 offset:54272
	ds_read_b128 v[194:197], v136 offset:55296
	ds_read_b128 v[198:201], v136 offset:56320
	global_load_lds_dwordx4 v[204:205], off
	v_lshl_add_u64 v[204:205], v[210:211], 0, s[6:7]
	s_add_i32 m0, s52, 0x2000
	s_add_i32 s52, s55, s20
	global_load_lds_dwordx4 v[204:205], off
	v_lshl_add_u64 v[202:203], v[202:203], 0, s[6:7]
	s_mov_b32 m0, s52
	s_nop 0
	global_load_lds_dwordx4 v[202:203], off
	v_lshl_add_u64 v[202:203], v[206:207], 0, s[6:7]
	s_add_i32 m0, s52, 0x2000
	s_nop 0
	global_load_lds_dwordx4 v[202:203], off
	v_lshl_add_u64 v[202:203], v[212:213], 0, s[6:7]
	s_mov_b32 m0, s25
	s_nop 0
	global_load_lds_dwordx4 v[202:203], off
	v_lshl_add_u64 v[202:203], v[214:215], 0, s[6:7]
	s_mov_b32 m0, s67
	s_nop 0
	global_load_lds_dwordx4 v[202:203], off
	s_waitcnt lgkmcnt(0)
	s_waitcnt vmcnt(8)
	s_barrier
	s_setprio 1
	s_waitcnt lgkmcnt(0)
	v_mfma_f32_16x16x32_bf16 v[60:63], v[138:141], v[170:173], v[60:63]
	v_mfma_f32_16x16x32_bf16 v[56:59], v[146:149], v[170:173], v[56:59]
	v_mfma_f32_16x16x32_bf16 v[44:47], v[138:141], v[178:181], v[44:47]
	v_mfma_f32_16x16x32_bf16 v[40:43], v[146:149], v[178:181], v[40:43]
	v_mfma_f32_16x16x32_bf16 v[28:31], v[138:141], v[186:189], v[28:31]
	v_mfma_f32_16x16x32_bf16 v[24:27], v[146:149], v[186:189], v[24:27]
	v_mfma_f32_16x16x32_bf16 v[12:15], v[138:141], v[194:197], v[12:15]
	v_mfma_f32_16x16x32_bf16 v[8:11], v[146:149], v[194:197], v[8:11]
	v_mfma_f32_16x16x32_bf16 v[60:63], v[142:145], v[174:177], v[60:63]
	v_mfma_f32_16x16x32_bf16 v[56:59], v[150:153], v[174:177], v[56:59]
	v_mfma_f32_16x16x32_bf16 v[44:47], v[142:145], v[182:185], v[44:47]
	v_mfma_f32_16x16x32_bf16 v[40:43], v[150:153], v[182:185], v[40:43]
	v_mfma_f32_16x16x32_bf16 v[28:31], v[142:145], v[190:193], v[28:31]
	v_mfma_f32_16x16x32_bf16 v[24:27], v[150:153], v[190:193], v[24:27]
	v_mfma_f32_16x16x32_bf16 v[12:15], v[142:145], v[198:201], v[12:15]
	v_mfma_f32_16x16x32_bf16 v[8:11], v[150:153], v[198:201], v[8:11]
	v_mfma_f32_16x16x32_bf16 v[52:55], v[154:157], v[170:173], v[52:55]
	v_mfma_f32_16x16x32_bf16 v[48:51], v[162:165], v[170:173], v[48:51]
	v_mfma_f32_16x16x32_bf16 v[36:39], v[154:157], v[178:181], v[36:39]
	v_mfma_f32_16x16x32_bf16 v[32:35], v[162:165], v[178:181], v[32:35]
	v_mfma_f32_16x16x32_bf16 v[20:23], v[154:157], v[186:189], v[20:23]
	v_mfma_f32_16x16x32_bf16 v[16:19], v[162:165], v[186:189], v[16:19]
	v_mfma_f32_16x16x32_bf16 v[4:7], v[154:157], v[194:197], v[4:7]
	v_mfma_f32_16x16x32_bf16 v[0:3], v[162:165], v[194:197], v[0:3]
	v_mfma_f32_16x16x32_bf16 v[52:55], v[158:161], v[174:177], v[52:55]
	v_mfma_f32_16x16x32_bf16 v[48:51], v[166:169], v[174:177], v[48:51]
	v_mfma_f32_16x16x32_bf16 v[36:39], v[158:161], v[182:185], v[36:39]
	v_mfma_f32_16x16x32_bf16 v[32:35], v[166:169], v[182:185], v[32:35]
	v_mfma_f32_16x16x32_bf16 v[20:23], v[158:161], v[190:193], v[20:23]
	v_mfma_f32_16x16x32_bf16 v[16:19], v[166:169], v[190:193], v[16:19]
	v_mfma_f32_16x16x32_bf16 v[4:7], v[158:161], v[198:201], v[4:7]
	v_mfma_f32_16x16x32_bf16 v[0:3], v[166:169], v[198:201], v[0:3]
	s_setprio 0
	s_waitcnt vmcnt(8)
	s_barrier
	s_add_u32 s35, s35, 0x100
	s_addc_u32 s45, s45, 0
	s_add_u32 s49, s49, 0x100
	s_addc_u32 s58, s58, 0
	s_add_u32 s59, s59, 0x100
	s_addc_u32 s70, s70, 0
	s_add_u32 s50, s50, 0x100
	s_addc_u32 s51, s51, 0
	s_cmp_ge_i32 s71, s2
	s_mov_b32 s52, s71
	s_cbranch_scc0 .LBB0_576
	s_and_b64 vcc, exec, s[14:15]
	s_cbranch_vccz .LBB0_579

; #define G_STAGE(bufoff, gbase, voff) do { _Pragma("unroll") for (int _i = 0; _i < 2; ++_i) \
;         __builtin_amdgcn_global_load_lds((const unsigned*)((const char*)(gbase) + (voff)[_i]), (LAS unsigned*)(lds + (bufoff) + ldsw + _i * 8192), 16, 0, 0); } while (0)
; #define G_LDA(dst, b, h) do { _Pragma("unroll") for (int m = 0; m < 4; ++m) G_LD8(dst[m], lds + G_SA(b, h) + aoff + m * 2048); } while (0)
; #define G_LDB(dst, b, h) do { _Pragma("unroll") for (int n = 0; n < 2; ++n) G_LD8(dst[n], lds + G_SB(b, h) + boff + n * 2048); } while (0)
; #define G_WAIT_V(n) asm volatile("s_waitcnt vmcnt(" #n ")" ::: "memory")
; #define G_WAIT_L(n) asm volatile("s_waitcnt lgkmcnt(" #n ")" ::: "memory")
; #define G_BAR __builtin_amdgcn_s_barrier()
; #define G_SCHED __builtin_amdgcn_sched_barrier(0)
;     __device__ __forceinline__ unsigned row_off(const Unit& u, int r, LAS unsigned char* lds) const { return (unsigned)((const LAS int*)(lds + LDS_STAGE + u.q * 4096))[r] * (unsigned)rowbytes; }
;     ...
;             const char* a11 = cur.a1 + (size_t)(t + 1) * kstep;
;             const char* a02 = last ? nxt.a0 : cur.a0 + (size_t)(t + 2) * kstep; const char* a12 = last ? nxt.a1 : cur.a1 + (size_t)(t + 2) * kstep;
;             const char* b02 = last ? nxt.b0 : cur.b0 + (size_t)(t + 2) * kstep; const char* b12 = last ? nxt.b1 : cur.b1 + (size_t)(t + 2) * kstep;
;             G_LDB(B0, 0, 0); G_LDB(B1, 0, 1); G_SCHED; G_LDA(At, 0, 0); G_STAGE(G_SA(1, 1), a11, vA1);
;             if constexpr (GATHER) { if (last) { int tz = tid; asm volatile("" : "+v"(tz));
; #pragma unroll
;                 for (int i = 0; i < 2; ++i) { int R, C; stage_rc(tz * 16 + i * 8192, R, C); gc0[i] = S.row_off(nxt, R, lds) + (unsigned)C * 2u; gc1[i] = S.row_off(nxt, 128 + R, lds) + (unsigned)C * 2u; } } }
;             G_WAIT_L(0); G_BAR; G_MMA(0, 0, At, B0); G_MMA(0, 1, At, B1); G_WAIT_V(8); G_BAR; G_SCHED;
;             G_LDA(At, 0, 1); G_STAGE(G_SB(0, 0), b02, voffB); G_STAGE(G_SB(0, 1), b12, voffB); G_STAGE(G_SA(0, 0), a02, vA0);
;             G_WAIT_L(0); G_BAR; G_MMA(1, 0, At, B0); G_MMA(1, 1, At, B1); G_WAIT_V(8); G_BAR; G_SCHED;
.LBB0_812:
	s_add_i32 s74, s54, 2
	ds_read_b128 v[138:141], v134
	ds_read_b128 v[142:145], v134 offset:1024
	ds_read_b128 v[146:149], v134 offset:2048
	ds_read_b128 v[150:153], v134 offset:3072
	ds_read_b128 v[154:157], v135
	ds_read_b128 v[158:161], v135 offset:1024
	ds_read_b128 v[162:165], v135 offset:2048
	ds_read_b128 v[166:169], v135 offset:3072
	s_add_u32 s75, s52, 0x80
	s_addc_u32 s55, s53, 0
	s_add_i32 s78, s68, s20
	s_add_i32 m0, s22, 0xc000
	s_add_i32 s77, s22, 0xe000
	s_add_i32 s79, s78, 0x2000
	s_cmp_eq_u32 s67, s54
	s_cselect_b32 s54, s46, s75
	s_cselect_b32 s57, s49, s73
	s_cselect_b32 s56, s48, s72
	s_cselect_b32 s59, s43, s61
	s_cselect_b32 s58, s42, s60
	s_cselect_b32 s55, s47, s55
	ds_read_b128 v[170:173], v136
	ds_read_b128 v[174:177], v136 offset:1024
	ds_read_b128 v[178:181], v136 offset:2048
	ds_read_b128 v[182:185], v136 offset:3072
	ds_read_b128 v[186:189], v136 offset:4096
	ds_read_b128 v[190:193], v136 offset:5120
	ds_read_b128 v[194:197], v136 offset:6144
	ds_read_b128 v[198:201], v136 offset:7168
	global_load_lds_dwordx4 v240, s[52:53]
	s_mov_b32 m0, s77
	v_mov_b32_e32 v205, v129
	global_load_lds_dwordx4 v242, s[52:53]
	s_waitcnt lgkmcnt(0)
	s_waitcnt vmcnt(8)
	s_barrier
	s_setprio 1
	s_waitcnt lgkmcnt(0)
	v_mfma_f32_16x16x32_bf16 v[124:127], v[138:141], v[170:173], v[124:127]
	v_mfma_f32_16x16x32_bf16 v[120:123], v[146:149], v[170:173], v[120:123]
	v_mfma_f32_16x16x32_bf16 v[108:111], v[138:141], v[178:181], v[108:111]
	v_mfma_f32_16x16x32_bf16 v[104:107], v[146:149], v[178:181], v[104:107]
	v_mfma_f32_16x16x32_bf16 v[92:95], v[138:141], v[186:189], v[92:95]
	v_mfma_f32_16x16x32_bf16 v[88:91], v[146:149], v[186:189], v[88:91]
	v_mfma_f32_16x16x32_bf16 v[76:79], v[138:141], v[194:197], v[76:79]
	v_mfma_f32_16x16x32_bf16 v[72:75], v[146:149], v[194:197], v[72:75]
	v_mfma_f32_16x16x32_bf16 v[124:127], v[142:145], v[174:177], v[124:127]
	v_mfma_f32_16x16x32_bf16 v[120:123], v[150:153], v[174:177], v[120:123]
	v_mfma_f32_16x16x32_bf16 v[108:111], v[142:145], v[182:185], v[108:111]
	v_mfma_f32_16x16x32_bf16 v[104:107], v[150:153], v[182:185], v[104:107]
	v_mfma_f32_16x16x32_bf16 v[92:95], v[142:145], v[190:193], v[92:95]
	v_mfma_f32_16x16x32_bf16 v[88:91], v[150:153], v[190:193], v[88:91]
	v_mfma_f32_16x16x32_bf16 v[76:79], v[142:145], v[198:201], v[76:79]
	v_mfma_f32_16x16x32_bf16 v[72:75], v[150:153], v[198:201], v[72:75]
	v_mfma_f32_16x16x32_bf16 v[116:119], v[154:157], v[170:173], v[116:119]
	v_mfma_f32_16x16x32_bf16 v[112:115], v[162:165], v[170:173], v[112:115]
	v_mfma_f32_16x16x32_bf16 v[100:103], v[154:157], v[178:181], v[100:103]
	v_mfma_f32_16x16x32_bf16 v[96:99], v[162:165], v[178:181], v[96:99]
	v_mfma_f32_16x16x32_bf16 v[84:87], v[154:157], v[186:189], v[84:87]
	v_mfma_f32_16x16x32_bf16 v[80:83], v[162:165], v[186:189], v[80:83]
	v_mfma_f32_16x16x32_bf16 v[68:71], v[154:157], v[194:197], v[68:71]
	v_mfma_f32_16x16x32_bf16 v[64:67], v[162:165], v[194:197], v[64:67]
	v_mfma_f32_16x16x32_bf16 v[116:119], v[158:161], v[174:177], v[116:119]
	v_mfma_f32_16x16x32_bf16 v[112:115], v[166:169], v[174:177], v[112:115]
	v_mfma_f32_16x16x32_bf16 v[100:103], v[158:161], v[182:185], v[100:103]
	v_mfma_f32_16x16x32_bf16 v[96:99], v[166:169], v[182:185], v[96:99]
	v_mfma_f32_16x16x32_bf16 v[84:87], v[158:161], v[190:193], v[84:87]
	v_mfma_f32_16x16x32_bf16 v[80:83], v[166:169], v[190:193], v[80:83]
	v_mfma_f32_16x16x32_bf16 v[68:71], v[158:161], v[198:201], v[68:71]
	v_mfma_f32_16x16x32_bf16 v[64:67], v[166:169], v[198:201], v[64:67]
	s_setprio 0
	s_waitcnt vmcnt(8)
	s_barrier
	s_mov_b32 m0, s78
	ds_read_b128 v[170:173], v136 offset:16384
	ds_read_b128 v[174:177], v136 offset:17408
	ds_read_b128 v[178:181], v136 offset:18432
	ds_read_b128 v[182:185], v136 offset:19456
	ds_read_b128 v[186:189], v136 offset:20480
	ds_read_b128 v[190:193], v136 offset:21504
	ds_read_b128 v[194:197], v136 offset:22528
	ds_read_b128 v[198:201], v136 offset:23552
	global_load_lds_dwordx4 v244, s[58:59]
	s_mov_b32 m0, s79
	s_cselect_b32 s79, s45, s71
	s_cselect_b32 s78, s44, s62
	s_add_i32 s75, s69, s20
	global_load_lds_dwordx4 v246, s[58:59]
	s_mov_b32 m0, s75
	v_mov_b32_e32 v203, v129
	global_load_lds_dwordx4 v244, s[78:79]
	s_add_i32 m0, s75, 0x2000
	v_mov_b32_e32 v207, v129
	global_load_lds_dwordx4 v246, s[78:79]
	s_mov_b32 m0, s22
	v_lshl_add_u64 v[208:209], s[58:59], 0, v[244:245]
	global_load_lds_dwordx4 v240, s[56:57]
	s_mov_b32 m0, s23
	v_lshl_add_u64 v[210:211], s[58:59], 0, v[246:247]
	global_load_lds_dwordx4 v242, s[56:57]
	s_waitcnt lgkmcnt(0)
	v_lshl_add_u64 v[202:203], s[78:79], 0, v[244:245]
	v_lshl_add_u64 v[206:207], s[78:79], 0, v[246:247]
	v_lshl_add_u64 v[212:213], s[56:57], 0, v[240:241]
	v_lshl_add_u64 v[214:215], s[56:57], 0, v[242:243]
	s_waitcnt vmcnt(8)
	s_barrier
; #define G_STAGE(bufoff, gbase, voff) do { _Pragma("unroll") for (int _i = 0; _i < 2; ++_i) \
;         __builtin_amdgcn_global_load_lds((const unsigned*)((const char*)(gbase) + (voff)[_i]), (LAS unsigned*)(lds + (bufoff) + ldsw + _i * 8192), 16, 0, 0); } while (0)
; #define G_LDA(dst, b, h) do { _Pragma("unroll") for (int m = 0; m < 4; ++m) G_LD8(dst[m], lds + G_SA(b, h) + aoff + m * 2048); } while (0)
; #define G_LDB(dst, b, h) do { _Pragma("unroll") for (int n = 0; n < 2; ++n) G_LD8(dst[n], lds + G_SB(b, h) + boff + n * 2048); } while (0)
; #define G_WAIT_V(n) asm volatile("s_waitcnt vmcnt(" #n ")" ::: "memory")
; #define G_WAIT_L(n) asm volatile("s_waitcnt lgkmcnt(" #n ")" ::: "memory")
; #define G_BAR __builtin_amdgcn_s_barrier()
; #define G_SCHED __builtin_amdgcn_sched_barrier(0)
;     ...
;             G_WAIT_L(0); G_BAR; G_MMA(1, 0, At, B0); G_MMA(1, 1, At, B1); G_WAIT_V(8); G_BAR; G_SCHED;
;             G_LDB(B0, 1, 0); G_LDB(B1, 1, 1); G_SCHED; G_LDA(At, 1, 0); G_STAGE(G_SA(0, 1), a12, vA1);
;             G_WAIT_L(0); G_BAR; G_MMA(0, 0, At, B0); G_MMA(0, 1, At, B1); G_WAIT_V(8); G_BAR; G_SCHED;
	s_setprio 1
	s_waitcnt lgkmcnt(0)
	v_mfma_f32_16x16x32_bf16 v[60:63], v[138:141], v[170:173], v[60:63]
	v_mfma_f32_16x16x32_bf16 v[56:59], v[146:149], v[170:173], v[56:59]
	v_mfma_f32_16x16x32_bf16 v[44:47], v[138:141], v[178:181], v[44:47]
	v_mfma_f32_16x16x32_bf16 v[40:43], v[146:149], v[178:181], v[40:43]
	v_mfma_f32_16x16x32_bf16 v[28:31], v[138:141], v[186:189], v[28:31]
	v_mfma_f32_16x16x32_bf16 v[24:27], v[146:149], v[186:189], v[24:27]
	v_mfma_f32_16x16x32_bf16 v[12:15], v[138:141], v[194:197], v[12:15]
	v_mfma_f32_16x16x32_bf16 v[8:11], v[146:149], v[194:197], v[8:11]
	v_mfma_f32_16x16x32_bf16 v[60:63], v[142:145], v[174:177], v[60:63]
	v_mfma_f32_16x16x32_bf16 v[56:59], v[150:153], v[174:177], v[56:59]
	v_mfma_f32_16x16x32_bf16 v[44:47], v[142:145], v[182:185], v[44:47]
	v_mfma_f32_16x16x32_bf16 v[40:43], v[150:153], v[182:185], v[40:43]
	v_mfma_f32_16x16x32_bf16 v[28:31], v[142:145], v[190:193], v[28:31]
	v_mfma_f32_16x16x32_bf16 v[24:27], v[150:153], v[190:193], v[24:27]
	v_mfma_f32_16x16x32_bf16 v[12:15], v[142:145], v[198:201], v[12:15]
	v_mfma_f32_16x16x32_bf16 v[8:11], v[150:153], v[198:201], v[8:11]
	v_mfma_f32_16x16x32_bf16 v[52:55], v[154:157], v[170:173], v[52:55]
	v_mfma_f32_16x16x32_bf16 v[48:51], v[162:165], v[170:173], v[48:51]
	v_mfma_f32_16x16x32_bf16 v[36:39], v[154:157], v[178:181], v[36:39]
	v_mfma_f32_16x16x32_bf16 v[32:35], v[162:165], v[178:181], v[32:35]
	v_mfma_f32_16x16x32_bf16 v[20:23], v[154:157], v[186:189], v[20:23]
	v_mfma_f32_16x16x32_bf16 v[16:19], v[162:165], v[186:189], v[16:19]
	v_mfma_f32_16x16x32_bf16 v[4:7], v[154:157], v[194:197], v[4:7]
	v_mfma_f32_16x16x32_bf16 v[0:3], v[162:165], v[194:197], v[0:3]
	v_mfma_f32_16x16x32_bf16 v[52:55], v[158:161], v[174:177], v[52:55]
	v_mfma_f32_16x16x32_bf16 v[48:51], v[166:169], v[174:177], v[48:51]
	v_mfma_f32_16x16x32_bf16 v[36:39], v[158:161], v[182:185], v[36:39]
	v_mfma_f32_16x16x32_bf16 v[32:35], v[166:169], v[182:185], v[32:35]
	v_mfma_f32_16x16x32_bf16 v[20:23], v[158:161], v[190:193], v[20:23]
	v_mfma_f32_16x16x32_bf16 v[16:19], v[166:169], v[190:193], v[16:19]
	v_mfma_f32_16x16x32_bf16 v[4:7], v[158:161], v[198:201], v[4:7]
	v_mfma_f32_16x16x32_bf16 v[0:3], v[166:169], v[198:201], v[0:3]
	s_setprio 0
	s_waitcnt vmcnt(8)
	s_barrier
	s_add_i32 s56, 0, 0x18000
	v_add_u32_e32 v137, s56, v133
	s_add_i32 s57, 0, 0x1c000
	ds_read_b128 v[138:141], v137
	ds_read_b128 v[142:145], v137 offset:1024
	ds_read_b128 v[146:149], v137 offset:2048
	ds_read_b128 v[150:153], v137 offset:3072
	v_add_u32_e32 v137, s57, v133
	ds_read_b128 v[154:157], v137
	ds_read_b128 v[158:161], v137 offset:1024
	ds_read_b128 v[162:165], v137 offset:2048
	ds_read_b128 v[166:169], v137 offset:3072
	s_mov_b32 m0, s24
	ds_read_b128 v[170:173], v136 offset:32768
	ds_read_b128 v[174:177], v136 offset:33792
	ds_read_b128 v[178:181], v136 offset:34816
	ds_read_b128 v[182:185], v136 offset:35840
	ds_read_b128 v[186:189], v136 offset:36864
	ds_read_b128 v[190:193], v136 offset:37888
	ds_read_b128 v[194:197], v136 offset:38912
	ds_read_b128 v[198:201], v136 offset:39936
	global_load_lds_dwordx4 v240, s[54:55]
	s_mov_b32 m0, s25
	s_nop 0
	global_load_lds_dwordx4 v242, s[54:55]
	s_waitcnt lgkmcnt(0)
	s_waitcnt vmcnt(8)
	s_barrier
	s_setprio 1
	s_waitcnt lgkmcnt(0)
	v_mfma_f32_16x16x32_bf16 v[124:127], v[138:141], v[170:173], v[124:127]
	v_mfma_f32_16x16x32_bf16 v[120:123], v[146:149], v[170:173], v[120:123]
	v_mfma_f32_16x16x32_bf16 v[108:111], v[138:141], v[178:181], v[108:111]
	v_mfma_f32_16x16x32_bf16 v[104:107], v[146:149], v[178:181], v[104:107]
	v_mfma_f32_16x16x32_bf16 v[92:95], v[138:141], v[186:189], v[92:95]
	v_mfma_f32_16x16x32_bf16 v[88:91], v[146:149], v[186:189], v[88:91]
	v_mfma_f32_16x16x32_bf16 v[76:79], v[138:141], v[194:197], v[76:79]
	v_mfma_f32_16x16x32_bf16 v[72:75], v[146:149], v[194:197], v[72:75]
	v_mfma_f32_16x16x32_bf16 v[124:127], v[142:145], v[174:177], v[124:127]
	v_mfma_f32_16x16x32_bf16 v[120:123], v[150:153], v[174:177], v[120:123]
	v_mfma_f32_16x16x32_bf16 v[108:111], v[142:145], v[182:185], v[108:111]
	v_mfma_f32_16x16x32_bf16 v[104:107], v[150:153], v[182:185], v[104:107]
	v_mfma_f32_16x16x32_bf16 v[92:95], v[142:145], v[190:193], v[92:95]
	v_mfma_f32_16x16x32_bf16 v[88:91], v[150:153], v[190:193], v[88:91]
	v_mfma_f32_16x16x32_bf16 v[76:79], v[142:145], v[198:201], v[76:79]
	v_mfma_f32_16x16x32_bf16 v[72:75], v[150:153], v[198:201], v[72:75]
	v_mfma_f32_16x16x32_bf16 v[116:119], v[154:157], v[170:173], v[116:119]
	v_mfma_f32_16x16x32_bf16 v[112:115], v[162:165], v[170:173], v[112:115]
	v_mfma_f32_16x16x32_bf16 v[100:103], v[154:157], v[178:181], v[100:103]
	v_mfma_f32_16x16x32_bf16 v[96:99], v[162:165], v[178:181], v[96:99]
	v_mfma_f32_16x16x32_bf16 v[84:87], v[154:157], v[186:189], v[84:87]
	v_mfma_f32_16x16x32_bf16 v[80:83], v[162:165], v[186:189], v[80:83]
	v_mfma_f32_16x16x32_bf16 v[68:71], v[154:157], v[194:197], v[68:71]
	v_mfma_f32_16x16x32_bf16 v[64:67], v[162:165], v[194:197], v[64:67]
	v_mfma_f32_16x16x32_bf16 v[116:119], v[158:161], v[174:177], v[116:119]
	v_mfma_f32_16x16x32_bf16 v[112:115], v[166:169], v[174:177], v[112:115]
	v_mfma_f32_16x16x32_bf16 v[100:103], v[158:161], v[182:185], v[100:103]
	v_mfma_f32_16x16x32_bf16 v[96:99], v[166:169], v[182:185], v[96:99]
	v_mfma_f32_16x16x32_bf16 v[84:87], v[158:161], v[190:193], v[84:87]
	v_mfma_f32_16x16x32_bf16 v[80:83], v[166:169], v[190:193], v[80:83]
	v_mfma_f32_16x16x32_bf16 v[68:71], v[158:161], v[198:201], v[68:71]
	v_mfma_f32_16x16x32_bf16 v[64:67], v[166:169], v[198:201], v[64:67]
	s_setprio 0
	s_waitcnt vmcnt(8)
	s_barrier
; #define G_STAGE(bufoff, gbase, voff) do { _Pragma("unroll") for (int _i = 0; _i < 2; ++_i) \
;         __builtin_amdgcn_global_load_lds((const unsigned*)((const char*)(gbase) + (voff)[_i]), (LAS unsigned*)(lds + (bufoff) + ldsw + _i * 8192), 16, 0, 0); } while (0)
; #define G_LDA(dst, b, h) do { _Pragma("unroll") for (int m = 0; m < 4; ++m) G_LD8(dst[m], lds + G_SA(b, h) + aoff + m * 2048); } while (0)
; #define G_WAIT_V(n) asm volatile("s_waitcnt vmcnt(" #n ")" ::: "memory")
; #define G_WAIT_L(n) asm volatile("s_waitcnt lgkmcnt(" #n ")" ::: "memory")
; #define G_BAR __builtin_amdgcn_s_barrier()
; #define G_SCHED __builtin_amdgcn_sched_barrier(0)
;     ...
;             G_LDA(At, 1, 1); G_STAGE(G_SB(1, 0), b02 + kstep, voffB); G_STAGE(G_SB(1, 1), b12 + kstep, voffB); G_STAGE(G_SA(1, 0), a02 + kstep, vA0);
;             G_WAIT_L(0); G_BAR; G_MMA(1, 0, At, B0); G_MMA(1, 1, At, B1); G_WAIT_V(8); G_BAR; G_SCHED;
;         }
	s_add_i32 s54, s56, s20
	v_lshl_add_u64 v[204:205], v[208:209], 0, s[36:37]
	s_mov_b32 m0, s54
	ds_read_b128 v[170:173], v136 offset:49152
	ds_read_b128 v[174:177], v136 offset:50176
	ds_read_b128 v[178:181], v136 offset:51200
	ds_read_b128 v[182:185], v136 offset:52224
	ds_read_b128 v[186:189], v136 offset:53248
	ds_read_b128 v[190:193], v136 offset:54272
	ds_read_b128 v[194:197], v136 offset:55296
	ds_read_b128 v[198:201], v136 offset:56320
	global_load_lds_dwordx4 v[204:205], off
	v_lshl_add_u64 v[204:205], v[210:211], 0, s[36:37]
	s_add_i32 m0, s54, 0x2000
	s_add_i32 s54, s57, s20
	global_load_lds_dwordx4 v[204:205], off
	v_lshl_add_u64 v[202:203], v[202:203], 0, s[36:37]
	s_mov_b32 m0, s54
	s_nop 0
	global_load_lds_dwordx4 v[202:203], off
	v_lshl_add_u64 v[202:203], v[206:207], 0, s[36:37]
	s_add_i32 m0, s54, 0x2000
	s_nop 0
	global_load_lds_dwordx4 v[202:203], off
	v_lshl_add_u64 v[202:203], v[212:213], 0, s[36:37]
	s_mov_b32 m0, s65
	s_nop 0
	global_load_lds_dwordx4 v[202:203], off
	v_lshl_add_u64 v[202:203], v[214:215], 0, s[36:37]
	s_mov_b32 m0, s66
	s_nop 0
	global_load_lds_dwordx4 v[202:203], off
	s_waitcnt lgkmcnt(0)
	s_waitcnt vmcnt(8)
	s_barrier
	s_setprio 1
	s_waitcnt lgkmcnt(0)
	v_mfma_f32_16x16x32_bf16 v[60:63], v[138:141], v[170:173], v[60:63]
	v_mfma_f32_16x16x32_bf16 v[56:59], v[146:149], v[170:173], v[56:59]
	v_mfma_f32_16x16x32_bf16 v[44:47], v[138:141], v[178:181], v[44:47]
	v_mfma_f32_16x16x32_bf16 v[40:43], v[146:149], v[178:181], v[40:43]
	v_mfma_f32_16x16x32_bf16 v[28:31], v[138:141], v[186:189], v[28:31]
	v_mfma_f32_16x16x32_bf16 v[24:27], v[146:149], v[186:189], v[24:27]
	v_mfma_f32_16x16x32_bf16 v[12:15], v[138:141], v[194:197], v[12:15]
	v_mfma_f32_16x16x32_bf16 v[8:11], v[146:149], v[194:197], v[8:11]
	v_mfma_f32_16x16x32_bf16 v[60:63], v[142:145], v[174:177], v[60:63]
	v_mfma_f32_16x16x32_bf16 v[56:59], v[150:153], v[174:177], v[56:59]
	v_mfma_f32_16x16x32_bf16 v[44:47], v[142:145], v[182:185], v[44:47]
	v_mfma_f32_16x16x32_bf16 v[40:43], v[150:153], v[182:185], v[40:43]
	v_mfma_f32_16x16x32_bf16 v[28:31], v[142:145], v[190:193], v[28:31]
	v_mfma_f32_16x16x32_bf16 v[24:27], v[150:153], v[190:193], v[24:27]
	v_mfma_f32_16x16x32_bf16 v[12:15], v[142:145], v[198:201], v[12:15]
	v_mfma_f32_16x16x32_bf16 v[8:11], v[150:153], v[198:201], v[8:11]
	v_mfma_f32_16x16x32_bf16 v[52:55], v[154:157], v[170:173], v[52:55]
	v_mfma_f32_16x16x32_bf16 v[48:51], v[162:165], v[170:173], v[48:51]
	v_mfma_f32_16x16x32_bf16 v[36:39], v[154:157], v[178:181], v[36:39]
	v_mfma_f32_16x16x32_bf16 v[32:35], v[162:165], v[178:181], v[32:35]
	v_mfma_f32_16x16x32_bf16 v[20:23], v[154:157], v[186:189], v[20:23]
	v_mfma_f32_16x16x32_bf16 v[16:19], v[162:165], v[186:189], v[16:19]
	v_mfma_f32_16x16x32_bf16 v[4:7], v[154:157], v[194:197], v[4:7]
	v_mfma_f32_16x16x32_bf16 v[0:3], v[162:165], v[194:197], v[0:3]
	v_mfma_f32_16x16x32_bf16 v[52:55], v[158:161], v[174:177], v[52:55]
	v_mfma_f32_16x16x32_bf16 v[48:51], v[166:169], v[174:177], v[48:51]
	v_mfma_f32_16x16x32_bf16 v[36:39], v[158:161], v[182:185], v[36:39]
	v_mfma_f32_16x16x32_bf16 v[32:35], v[166:169], v[182:185], v[32:35]
	v_mfma_f32_16x16x32_bf16 v[20:23], v[158:161], v[190:193], v[20:23]
	v_mfma_f32_16x16x32_bf16 v[16:19], v[166:169], v[190:193], v[16:19]
	v_mfma_f32_16x16x32_bf16 v[4:7], v[158:161], v[198:201], v[4:7]
	v_mfma_f32_16x16x32_bf16 v[0:3], v[166:169], v[198:201], v[0:3]
	s_setprio 0
	s_waitcnt vmcnt(8)
	s_barrier
	s_add_u32 s60, s60, 0x100
	s_addc_u32 s61, s61, 0
	s_add_u32 s62, s62, 0x100
	s_addc_u32 s71, s71, 0
	s_add_u32 s72, s72, 0x100
	s_addc_u32 s73, s73, 0
	s_add_u32 s52, s52, 0x100
	s_addc_u32 s53, s53, 0
	s_cmp_ge_i32 s74, s0
	s_mov_b32 s54, s74
	s_cbranch_scc0 .LBB0_812
	v_readlane_b32 s78, v255, 11
	v_readlane_b32 s79, v255, 13
	s_and_b64 vcc, exec, s[40:41]
	s_cbranch_vccz .LBB0_815

; #define G_STAGE(bufoff, gbase, voff) do { _Pragma("unroll") for (int _i = 0; _i < 2; ++_i) \
;         __builtin_amdgcn_global_load_lds((const unsigned*)((const char*)(gbase) + (voff)[_i]), (LAS unsigned*)(lds + (bufoff) + ldsw + _i * 8192), 16, 0, 0); } while (0)
; #define G_LDA(dst, b, h) do { _Pragma("unroll") for (int m = 0; m < 4; ++m) G_LD8(dst[m], lds + G_SA(b, h) + aoff + m * 2048); } while (0)
; #define G_LDB(dst, b, h) do { _Pragma("unroll") for (int n = 0; n < 2; ++n) G_LD8(dst[n], lds + G_SB(b, h) + boff + n * 2048); } while (0)
; #define G_WAIT_V(n) asm volatile("s_waitcnt vmcnt(" #n ")" ::: "memory")
; #define G_WAIT_L(n) asm volatile("s_waitcnt lgkmcnt(" #n ")" ::: "memory")
; #define G_BAR __builtin_amdgcn_s_barrier()
; #define G_SCHED __builtin_amdgcn_sched_barrier(0)
;     __device__ __forceinline__ unsigned row_off(const Unit& u, int r, LAS unsigned char* lds) const { return (unsigned)((const LAS int*)(lds + LDS_STAGE + u.q * 4096))[r] * (unsigned)rowbytes; }
;     ...
;             G_LDB(B0, 0, 0); G_LDB(B1, 0, 1); G_SCHED; G_LDA(At, 0, 0); G_STAGE(G_SA(1, 1), a11, vA1);
;             if constexpr (GATHER) { if (last) { int tz = tid; asm volatile("" : "+v"(tz));
; #pragma unroll
;                 for (int i = 0; i < 2; ++i) { int R, C; stage_rc(tz * 16 + i * 8192, R, C); gc0[i] = S.row_off(nxt, R, lds) + (unsigned)C * 2u; gc1[i] = S.row_off(nxt, 128 + R, lds) + (unsigned)C * 2u; } } }
;             G_WAIT_L(0); G_BAR; G_MMA(0, 0, At, B0); G_MMA(0, 1, At, B1); G_WAIT_V(8); G_BAR; G_SCHED;
;             G_LDA(At, 0, 1); G_STAGE(G_SB(0, 0), b02, voffB); G_STAGE(G_SB(0, 1), b12, voffB); G_STAGE(G_SA(0, 0), a02, vA0);
;             G_WAIT_L(0); G_BAR; G_MMA(1, 0, At, B0); G_MMA(1, 1, At, B1); G_WAIT_V(8); G_BAR; G_SCHED;
;             G_LDB(B0, 1, 0); G_LDB(B1, 1, 1); G_SCHED; G_LDA(At, 1, 0); G_STAGE(G_SA(0, 1), a12, vA1);
.LBB0_1023:
	s_add_i32 s78, s54, 2
	ds_read_b128 v[72:75], v70
	ds_read_b128 v[76:79], v70 offset:1024
	ds_read_b128 v[80:83], v70 offset:2048
	ds_read_b128 v[84:87], v70 offset:3072
	s_add_u32 s79, s52, 0x80
	s_addc_u32 s55, s53, 0
	s_add_i32 s81, s73, s20
	s_add_i32 m0, s23, 0xc000
	s_add_i32 s80, s23, 0xe000
	s_add_i32 s82, s81, 0x2000
	s_cmp_eq_u32 s72, s54
	s_cselect_b32 s54, s44, s79
	s_cselect_b32 s57, s43, s77
	s_cselect_b32 s56, s42, s75
	s_cselect_b32 s59, s49, s61
	s_cselect_b32 s58, s48, s60
	s_cselect_b32 s55, s45, s55
	ds_read_b128 v[88:91], v71
	ds_read_b128 v[92:95], v71 offset:1024
	ds_read_b128 v[96:99], v71 offset:2048
	ds_read_b128 v[100:103], v71 offset:3072
	ds_read_b128 v[104:107], v71 offset:4096
	ds_read_b128 v[108:111], v71 offset:5120
	ds_read_b128 v[112:115], v71 offset:6144
	ds_read_b128 v[116:119], v71 offset:7168
	global_load_lds_dwordx4 v240, s[52:53]
	s_mov_b32 m0, s80
	v_mov_b32_e32 v123, v65
	global_load_lds_dwordx4 v242, s[52:53]
	s_waitcnt lgkmcnt(0)
	s_waitcnt vmcnt(8)
	s_barrier
	s_setprio 1
	s_waitcnt lgkmcnt(0)
	v_mfma_f32_16x16x32_bf16 v[60:63], v[72:75], v[88:91], v[60:63]
	v_mfma_f32_16x16x32_bf16 v[56:59], v[80:83], v[88:91], v[56:59]
	v_mfma_f32_16x16x32_bf16 v[52:55], v[72:75], v[96:99], v[52:55]
	v_mfma_f32_16x16x32_bf16 v[48:51], v[80:83], v[96:99], v[48:51]
	v_mfma_f32_16x16x32_bf16 v[44:47], v[72:75], v[104:107], v[44:47]
	v_mfma_f32_16x16x32_bf16 v[40:43], v[80:83], v[104:107], v[40:43]
	v_mfma_f32_16x16x32_bf16 v[36:39], v[72:75], v[112:115], v[36:39]
	v_mfma_f32_16x16x32_bf16 v[32:35], v[80:83], v[112:115], v[32:35]
	v_mfma_f32_16x16x32_bf16 v[60:63], v[76:79], v[92:95], v[60:63]
	v_mfma_f32_16x16x32_bf16 v[56:59], v[84:87], v[92:95], v[56:59]
	v_mfma_f32_16x16x32_bf16 v[52:55], v[76:79], v[100:103], v[52:55]
	v_mfma_f32_16x16x32_bf16 v[48:51], v[84:87], v[100:103], v[48:51]
	v_mfma_f32_16x16x32_bf16 v[44:47], v[76:79], v[108:111], v[44:47]
	v_mfma_f32_16x16x32_bf16 v[40:43], v[84:87], v[108:111], v[40:43]
	v_mfma_f32_16x16x32_bf16 v[36:39], v[76:79], v[116:119], v[36:39]
	v_mfma_f32_16x16x32_bf16 v[32:35], v[84:87], v[116:119], v[32:35]
	s_setprio 0
	s_waitcnt vmcnt(8)
	s_barrier
	s_mov_b32 m0, s81
	ds_read_b128 v[88:91], v71 offset:16384
	ds_read_b128 v[92:95], v71 offset:17408
	ds_read_b128 v[96:99], v71 offset:18432
	ds_read_b128 v[100:103], v71 offset:19456
	ds_read_b128 v[104:107], v71 offset:20480
	ds_read_b128 v[108:111], v71 offset:21504
	ds_read_b128 v[112:115], v71 offset:22528
	ds_read_b128 v[116:119], v71 offset:23552
	global_load_lds_dwordx4 v244, s[58:59]
	s_mov_b32 m0, s82
	s_cselect_b32 s81, s47, s74
	global_load_lds_dwordx4 v246, s[58:59]
	s_cselect_b32 s80, s46, s62
	s_mov_b32 m0, s24
	v_mov_b32_e32 v121, v65
	global_load_lds_dwordx4 v244, s[80:81]
	s_mov_b32 m0, s25
	v_mov_b32_e32 v125, v65
	global_load_lds_dwordx4 v246, s[80:81]
	s_mov_b32 m0, s23
	v_lshl_add_u64 v[126:127], s[58:59], 0, v[244:245]
	global_load_lds_dwordx4 v240, s[56:57]
	s_mov_b32 m0, s27
	v_lshl_add_u64 v[128:129], s[58:59], 0, v[246:247]
	global_load_lds_dwordx4 v242, s[56:57]
	s_waitcnt lgkmcnt(0)
	v_lshl_add_u64 v[120:121], s[80:81], 0, v[244:245]
	v_lshl_add_u64 v[124:125], s[80:81], 0, v[246:247]
	v_lshl_add_u64 v[130:131], s[56:57], 0, v[240:241]
	v_lshl_add_u64 v[132:133], s[56:57], 0, v[242:243]
	s_waitcnt vmcnt(8)
	s_barrier
	s_setprio 1
	s_waitcnt lgkmcnt(0)
	v_mfma_f32_16x16x32_bf16 v[28:31], v[72:75], v[88:91], v[28:31]
	v_mfma_f32_16x16x32_bf16 v[24:27], v[80:83], v[88:91], v[24:27]
	v_mfma_f32_16x16x32_bf16 v[20:23], v[72:75], v[96:99], v[20:23]
	v_mfma_f32_16x16x32_bf16 v[16:19], v[80:83], v[96:99], v[16:19]
	v_mfma_f32_16x16x32_bf16 v[12:15], v[72:75], v[104:107], v[12:15]
	v_mfma_f32_16x16x32_bf16 v[8:11], v[80:83], v[104:107], v[8:11]
	v_mfma_f32_16x16x32_bf16 v[4:7], v[72:75], v[112:115], v[4:7]
	v_mfma_f32_16x16x32_bf16 v[0:3], v[80:83], v[112:115], v[0:3]
	v_mfma_f32_16x16x32_bf16 v[28:31], v[76:79], v[92:95], v[28:31]
	v_mfma_f32_16x16x32_bf16 v[24:27], v[84:87], v[92:95], v[24:27]
	v_mfma_f32_16x16x32_bf16 v[20:23], v[76:79], v[100:103], v[20:23]
	v_mfma_f32_16x16x32_bf16 v[16:19], v[84:87], v[100:103], v[16:19]
	v_mfma_f32_16x16x32_bf16 v[12:15], v[76:79], v[108:111], v[12:15]
	v_mfma_f32_16x16x32_bf16 v[8:11], v[84:87], v[108:111], v[8:11]
	v_mfma_f32_16x16x32_bf16 v[4:7], v[76:79], v[116:119], v[4:7]
	v_mfma_f32_16x16x32_bf16 v[0:3], v[84:87], v[116:119], v[0:3]
	s_setprio 0
	s_waitcnt vmcnt(8)
	s_barrier
	s_add_i32 s56, 0, 0x18000
	v_add_u32_e32 v84, s56, v69
	ds_read_b128 v[72:75], v84
	ds_read_b128 v[76:79], v84 offset:1024
	ds_read_b128 v[80:83], v84 offset:2048
	ds_read_b128 v[84:87], v84 offset:3072
	s_mov_b32 m0, s33
	ds_read_b128 v[88:91], v71 offset:32768
	ds_read_b128 v[92:95], v71 offset:33792
	ds_read_b128 v[96:99], v71 offset:34816
	ds_read_b128 v[100:103], v71 offset:35840
	ds_read_b128 v[104:107], v71 offset:36864
	ds_read_b128 v[108:111], v71 offset:37888
	ds_read_b128 v[112:115], v71 offset:38912
	ds_read_b128 v[116:119], v71 offset:39936
	global_load_lds_dwordx4 v240, s[54:55]
	s_mov_b32 m0, s41
	s_nop 0
	global_load_lds_dwordx4 v242, s[54:55]
	s_waitcnt lgkmcnt(0)
	s_waitcnt vmcnt(8)
	s_barrier
; #define GAS __attribute__((address_space(1)))
; __device__ __forceinline__ v4u pack8(const f32x4 a, const f32x4 b) { v4u w; w.x = cvt_pk_bf16(a[0], a[1]); w.y = cvt_pk_bf16(a[2], a[3]); w.z = cvt_pk_bf16(b[0], b[1]); w.w = cvt_pk_bf16(b[2], b[3]); return w; }
; #define G_STAGE(bufoff, gbase, voff) do { _Pragma("unroll") for (int _i = 0; _i < 2; ++_i) \
;         __builtin_amdgcn_global_load_lds((const unsigned*)((const char*)(gbase) + (voff)[_i]), (LAS unsigned*)(lds + (bufoff) + ldsw + _i * 8192), 16, 0, 0); } while (0)
; #define G_LDA(dst, b, h) do { _Pragma("unroll") for (int m = 0; m < 4; ++m) G_LD8(dst[m], lds + G_SA(b, h) + aoff + m * 2048); } while (0)
; #define G_WAIT_V(n) asm volatile("s_waitcnt vmcnt(" #n ")" ::: "memory")
; #define G_BAR __builtin_amdgcn_s_barrier()
;     ...
;             G_LDB(B0, 0, 0); G_LDB(B1, 0, 1); G_SCHED; G_LDA(At, 0, 0); G_STAGE(G_SA(1, 1), a11, vA1);
;             if constexpr (GATHER) { if (last) { int tz = tid; asm volatile("" : "+v"(tz));
; #pragma unroll
;                 for (int i = 0; i < 2; ++i) { int R, C; stage_rc(tz * 16 + i * 8192, R, C); gc0[i] = S.row_off(nxt, R, lds) + (unsigned)C * 2u; gc1[i] = S.row_off(nxt, 128 + R, lds) + (unsigned)C * 2u; } } }
;             G_WAIT_L(0); G_BAR; G_MMA(0, 0, At, B0); G_MMA(0, 1, At, B1); G_WAIT_V(8); G_BAR; G_SCHED;
;             G_LDA(At, 0, 1); G_STAGE(G_SB(0, 0), b02, voffB); G_STAGE(G_SB(0, 1), b12, voffB); G_STAGE(G_SA(0, 0), a02, vA0);
;             G_WAIT_L(0); G_BAR; G_MMA(1, 0, At, B0); G_MMA(1, 1, At, B1); G_WAIT_V(8); G_BAR; G_SCHED;
;             G_LDB(B0, 1, 0); G_LDB(B1, 1, 1); G_SCHED; G_LDA(At, 1, 0); G_STAGE(G_SA(0, 1), a12, vA1);
;             G_WAIT_L(0); G_BAR; G_MMA(0, 0, At, B0); G_MMA(0, 1, At, B1); G_WAIT_V(8); G_BAR; G_SCHED;
;             G_LDA(At, 1, 1); G_STAGE(G_SB(1, 0), b02 + kstep, voffB); G_STAGE(G_SB(1, 1), b12 + kstep, voffB); G_STAGE(G_SA(1, 0), a02 + kstep, vA0);
;             G_WAIT_L(0); G_BAR; G_MMA(1, 0, At, B0); G_MMA(1, 1, At, B1); G_WAIT_V(8); G_BAR; G_SCHED;
;     __device__ __forceinline__ void operator()(Acc& acc, const Unit& u, LAS unsigned char*, int wr, int wc, int fr, int fq) const {
;     ...
;         EPI_LOOP_AM { const int R = u.p0 * 256 + 128 * ai + 64 * wr + 16 * m + fr, k = R >> 3, g = R & 7;
;             *(GAS v4u*)(y + (size_t)k * D + g * 128 + l0) = pack8(acc[ai][0][m][0] * norm, acc[ai][0][m][1] * norm); }
	s_setprio 1
	s_waitcnt lgkmcnt(0)
	v_mfma_f32_16x16x32_bf16 v[60:63], v[72:75], v[88:91], v[60:63]
	v_mfma_f32_16x16x32_bf16 v[56:59], v[80:83], v[88:91], v[56:59]
	v_mfma_f32_16x16x32_bf16 v[52:55], v[72:75], v[96:99], v[52:55]
	v_mfma_f32_16x16x32_bf16 v[48:51], v[80:83], v[96:99], v[48:51]
	v_mfma_f32_16x16x32_bf16 v[44:47], v[72:75], v[104:107], v[44:47]
	v_mfma_f32_16x16x32_bf16 v[40:43], v[80:83], v[104:107], v[40:43]
	v_mfma_f32_16x16x32_bf16 v[36:39], v[72:75], v[112:115], v[36:39]
	v_mfma_f32_16x16x32_bf16 v[32:35], v[80:83], v[112:115], v[32:35]
	v_mfma_f32_16x16x32_bf16 v[60:63], v[76:79], v[92:95], v[60:63]
	v_mfma_f32_16x16x32_bf16 v[56:59], v[84:87], v[92:95], v[56:59]
	v_mfma_f32_16x16x32_bf16 v[52:55], v[76:79], v[100:103], v[52:55]
	v_mfma_f32_16x16x32_bf16 v[48:51], v[84:87], v[100:103], v[48:51]
	v_mfma_f32_16x16x32_bf16 v[44:47], v[76:79], v[108:111], v[44:47]
	v_mfma_f32_16x16x32_bf16 v[40:43], v[84:87], v[108:111], v[40:43]
	v_mfma_f32_16x16x32_bf16 v[36:39], v[76:79], v[116:119], v[36:39]
	v_mfma_f32_16x16x32_bf16 v[32:35], v[84:87], v[116:119], v[32:35]
	s_setprio 0
	s_waitcnt vmcnt(8)
	s_barrier
	s_add_i32 s54, s56, s20
	v_lshl_add_u64 v[122:123], v[126:127], 0, s[36:37]
	s_mov_b32 m0, s54
	ds_read_b128 v[88:91], v71 offset:49152
	ds_read_b128 v[92:95], v71 offset:50176
	ds_read_b128 v[96:99], v71 offset:51200
	ds_read_b128 v[100:103], v71 offset:52224
	ds_read_b128 v[104:107], v71 offset:53248
	ds_read_b128 v[108:111], v71 offset:54272
	ds_read_b128 v[112:115], v71 offset:55296
	ds_read_b128 v[116:119], v71 offset:56320
	global_load_lds_dwordx4 v[122:123], off
	v_lshl_add_u64 v[122:123], v[128:129], 0, s[36:37]
	s_add_i32 m0, s54, 0x2000
	v_lshl_add_u64 v[120:121], v[120:121], 0, s[36:37]
	global_load_lds_dwordx4 v[122:123], off
	s_mov_b32 m0, s69
	s_nop 0
	global_load_lds_dwordx4 v[120:121], off
	v_lshl_add_u64 v[120:121], v[124:125], 0, s[36:37]
	s_mov_b32 m0, s71
	s_nop 0
	global_load_lds_dwordx4 v[120:121], off
	v_lshl_add_u64 v[120:121], v[130:131], 0, s[36:37]
	s_mov_b32 m0, s66
	s_nop 0
	global_load_lds_dwordx4 v[120:121], off
	v_lshl_add_u64 v[120:121], v[132:133], 0, s[36:37]
	s_mov_b32 m0, s67
	s_nop 0
	global_load_lds_dwordx4 v[120:121], off
	s_waitcnt lgkmcnt(0)
	s_waitcnt vmcnt(8)
	s_barrier
	s_setprio 1
	s_waitcnt lgkmcnt(0)
	v_mfma_f32_16x16x32_bf16 v[28:31], v[72:75], v[88:91], v[28:31]
	v_mfma_f32_16x16x32_bf16 v[24:27], v[80:83], v[88:91], v[24:27]
	v_mfma_f32_16x16x32_bf16 v[20:23], v[72:75], v[96:99], v[20:23]
	v_mfma_f32_16x16x32_bf16 v[16:19], v[80:83], v[96:99], v[16:19]
	v_mfma_f32_16x16x32_bf16 v[12:15], v[72:75], v[104:107], v[12:15]
	v_mfma_f32_16x16x32_bf16 v[8:11], v[80:83], v[104:107], v[8:11]
	v_mfma_f32_16x16x32_bf16 v[4:7], v[72:75], v[112:115], v[4:7]
	v_mfma_f32_16x16x32_bf16 v[0:3], v[80:83], v[112:115], v[0:3]
	v_mfma_f32_16x16x32_bf16 v[28:31], v[76:79], v[92:95], v[28:31]
	v_mfma_f32_16x16x32_bf16 v[24:27], v[84:87], v[92:95], v[24:27]
	v_mfma_f32_16x16x32_bf16 v[20:23], v[76:79], v[100:103], v[20:23]
	v_mfma_f32_16x16x32_bf16 v[16:19], v[84:87], v[100:103], v[16:19]
	v_mfma_f32_16x16x32_bf16 v[12:15], v[76:79], v[108:111], v[12:15]
	v_mfma_f32_16x16x32_bf16 v[8:11], v[84:87], v[108:111], v[8:11]
	v_mfma_f32_16x16x32_bf16 v[4:7], v[76:79], v[116:119], v[4:7]
	v_mfma_f32_16x16x32_bf16 v[0:3], v[84:87], v[116:119], v[0:3]
	s_setprio 0
	s_waitcnt vmcnt(8)
	s_barrier
	s_add_u32 s60, s60, 0x100
	s_addc_u32 s61, s61, 0
	s_add_u32 s62, s62, 0x100
	s_addc_u32 s74, s74, 0
	s_add_u32 s75, s75, 0x100
	s_addc_u32 s77, s77, 0
	s_add_u32 s52, s52, 0x100
	s_addc_u32 s53, s53, 0
	s_cmp_ge_i32 s78, s0
	s_mov_b32 s54, s78
	s_cbranch_scc0 .LBB0_1023
	v_pk_mul_f32 v[62:63], v[62:63], s[40:41] op_sel_hi:[1,0]
	v_pk_mul_f32 v[60:61], v[60:61], s[40:41] op_sel_hi:[1,0]
	v_pk_mul_f32 v[58:59], v[58:59], s[40:41] op_sel_hi:[1,0]
	v_pk_mul_f32 v[56:57], v[56:57], s[40:41] op_sel_hi:[1,0]
	v_pk_mul_f32 v[54:55], v[54:55], s[40:41] op_sel_hi:[1,0]
	v_pk_mul_f32 v[52:53], v[52:53], s[40:41] op_sel_hi:[1,0]
	v_pk_mul_f32 v[50:51], v[50:51], s[40:41] op_sel_hi:[1,0]
	v_pk_mul_f32 v[48:49], v[48:49], s[40:41] op_sel_hi:[1,0]
	v_pk_mul_f32 v[46:47], v[46:47], s[40:41] op_sel_hi:[1,0]
	v_pk_mul_f32 v[44:45], v[44:45], s[40:41] op_sel_hi:[1,0]
	v_pk_mul_f32 v[42:43], v[42:43], s[40:41] op_sel_hi:[1,0]
	v_pk_mul_f32 v[40:41], v[40:41], s[40:41] op_sel_hi:[1,0]
	v_pk_mul_f32 v[38:39], v[38:39], s[40:41] op_sel_hi:[1,0]
	v_pk_mul_f32 v[36:37], v[36:37], s[40:41] op_sel_hi:[1,0]
	v_pk_mul_f32 v[34:35], v[34:35], s[40:41] op_sel_hi:[1,0]
	v_pk_mul_f32 v[32:33], v[32:33], s[40:41] op_sel_hi:[1,0]
	v_pk_mul_f32 v[30:31], v[30:31], s[40:41] op_sel_hi:[1,0]
	v_pk_mul_f32 v[28:29], v[28:29], s[40:41] op_sel_hi:[1,0]
	v_pk_mul_f32 v[26:27], v[26:27], s[40:41] op_sel_hi:[1,0]
	v_pk_mul_f32 v[24:25], v[24:25], s[40:41] op_sel_hi:[1,0]
	v_pk_mul_f32 v[22:23], v[22:23], s[40:41] op_sel_hi:[1,0]
	v_pk_mul_f32 v[20:21], v[20:21], s[40:41] op_sel_hi:[1,0]
	v_pk_mul_f32 v[18:19], v[18:19], s[40:41] op_sel_hi:[1,0]
	v_pk_mul_f32 v[16:17], v[16:17], s[40:41] op_sel_hi:[1,0]
	v_pk_mul_f32 v[14:15], v[14:15], s[40:41] op_sel_hi:[1,0]
	v_pk_mul_f32 v[12:13], v[12:13], s[40:41] op_sel_hi:[1,0]
	v_pk_mul_f32 v[10:11], v[10:11], s[40:41] op_sel_hi:[1,0]
	v_pk_mul_f32 v[8:9], v[8:9], s[40:41] op_sel_hi:[1,0]
	v_pk_mul_f32 v[6:7], v[6:7], s[40:41] op_sel_hi:[1,0]
	v_pk_mul_f32 v[4:5], v[4:5], s[40:41] op_sel_hi:[1,0]
	v_pk_mul_f32 v[2:3], v[2:3], s[40:41] op_sel_hi:[1,0]
	v_pk_mul_f32 v[0:1], v[0:1], s[40:41] op_sel_hi:[1,0]
	v_readlane_b32 s78, v255, 11
	v_readlane_b32 s79, v255, 13
	s_and_b64 vcc, exec, s[38:39]
	s_cbranch_vccz .LBB0_1026

; #define G_STAGE(bufoff, gbase, voff) do { _Pragma("unroll") for (int _i = 0; _i < 2; ++_i) \
;         __builtin_amdgcn_global_load_lds((const unsigned*)((const char*)(gbase) + (voff)[_i]), (LAS unsigned*)(lds + (bufoff) + ldsw + _i * 8192), 16, 0, 0); } while (0)
; #define G_LDA(dst, b, h) do { _Pragma("unroll") for (int m = 0; m < 4; ++m) G_LD8(dst[m], lds + G_SA(b, h) + aoff + m * 2048); } while (0)
; #define G_LDB(dst, b, h) do { _Pragma("unroll") for (int n = 0; n < 2; ++n) G_LD8(dst[n], lds + G_SB(b, h) + boff + n * 2048); } while (0)
; #define G_WAIT_V(n) asm volatile("s_waitcnt vmcnt(" #n ")" ::: "memory")
; #define G_WAIT_L(n) asm volatile("s_waitcnt lgkmcnt(" #n ")" ::: "memory")
; #define G_BAR __builtin_amdgcn_s_barrier()
; #define G_SCHED __builtin_amdgcn_sched_barrier(0)
;     __device__ __forceinline__ unsigned row_off(const Unit& u, int r, LAS unsigned char* lds) const { return (unsigned)((const LAS int*)(lds + LDS_STAGE + u.q * 4096))[r] * (unsigned)rowbytes; }
;     ...
;             const char* a11 = cur.a1 + (size_t)(t + 1) * kstep;
;             const char* a02 = last ? nxt.a0 : cur.a0 + (size_t)(t + 2) * kstep; const char* a12 = last ? nxt.a1 : cur.a1 + (size_t)(t + 2) * kstep;
;             const char* b02 = last ? nxt.b0 : cur.b0 + (size_t)(t + 2) * kstep; const char* b12 = last ? nxt.b1 : cur.b1 + (size_t)(t + 2) * kstep;
;             G_LDB(B0, 0, 0); G_LDB(B1, 0, 1); G_SCHED; G_LDA(At, 0, 0); G_STAGE(G_SA(1, 1), a11, vA1);
;             if constexpr (GATHER) { if (last) { int tz = tid; asm volatile("" : "+v"(tz));
; #pragma unroll
;                 for (int i = 0; i < 2; ++i) { int R, C; stage_rc(tz * 16 + i * 8192, R, C); gc0[i] = S.row_off(nxt, R, lds) + (unsigned)C * 2u; gc1[i] = S.row_off(nxt, 128 + R, lds) + (unsigned)C * 2u; } } }
;             G_WAIT_L(0); G_BAR; G_MMA(0, 0, At, B0); G_MMA(0, 1, At, B1); G_WAIT_V(8); G_BAR; G_SCHED;
;             G_LDA(At, 0, 1); G_STAGE(G_SB(0, 0), b02, voffB); G_STAGE(G_SB(0, 1), b12, voffB); G_STAGE(G_SA(0, 0), a02, vA0);
;             G_WAIT_L(0); G_BAR; G_MMA(1, 0, At, B0); G_MMA(1, 1, At, B1); G_WAIT_V(8); G_BAR; G_SCHED;
.LBB0_1058:
	s_add_i32 s79, s54, 2
	ds_read_b128 v[130:133], v138
	ds_read_b128 v[144:147], v138 offset:1024
	ds_read_b128 v[148:151], v138 offset:2048
	ds_read_b128 v[152:155], v138 offset:3072
	ds_read_b128 v[156:159], v139
	ds_read_b128 v[160:163], v139 offset:1024
	ds_read_b128 v[164:167], v139 offset:2048
	ds_read_b128 v[168:171], v139 offset:3072
	s_add_u32 s80, s52, 0x80
	s_addc_u32 s55, s53, 0
	s_add_i32 s83, s71, s20
	s_add_i32 m0, s33, 0xc000
	s_add_i32 s82, s33, 0xe000
	s_add_i32 s84, s83, 0x2000
	s_cmp_eq_u32 s69, s54
	s_cselect_b32 s54, s44, s80
	s_cselect_b32 s57, s43, s78
	s_cselect_b32 s56, s42, s77
	s_cselect_b32 s59, s47, s41
	s_cselect_b32 s58, s46, s5
	s_cselect_b32 s55, s45, s55
	ds_read_b128 v[172:175], v140
	ds_read_b128 v[176:179], v140 offset:1024
	ds_read_b128 v[180:183], v140 offset:2048
	ds_read_b128 v[184:187], v140 offset:3072
	ds_read_b128 v[188:191], v140 offset:4096
	ds_read_b128 v[192:195], v140 offset:5120
	ds_read_b128 v[196:199], v140 offset:6144
	ds_read_b128 v[200:203], v140 offset:7168
	global_load_lds_dwordx4 v240, s[52:53]
	s_mov_b32 m0, s82
	v_mov_b32_e32 v207, v129
	global_load_lds_dwordx4 v242, s[52:53]
	s_waitcnt lgkmcnt(0)
	s_waitcnt vmcnt(8)
	s_barrier
	s_setprio 1
	s_waitcnt lgkmcnt(0)
	v_mfma_f32_16x16x32_bf16 v[124:127], v[130:133], v[172:175], v[124:127]
	v_mfma_f32_16x16x32_bf16 v[120:123], v[148:151], v[172:175], v[120:123]
	v_mfma_f32_16x16x32_bf16 v[108:111], v[130:133], v[180:183], v[108:111]
	v_mfma_f32_16x16x32_bf16 v[104:107], v[148:151], v[180:183], v[104:107]
	v_mfma_f32_16x16x32_bf16 v[92:95], v[130:133], v[188:191], v[92:95]
	v_mfma_f32_16x16x32_bf16 v[88:91], v[148:151], v[188:191], v[88:91]
	v_mfma_f32_16x16x32_bf16 v[76:79], v[130:133], v[196:199], v[76:79]
	v_mfma_f32_16x16x32_bf16 v[72:75], v[148:151], v[196:199], v[72:75]
	v_mfma_f32_16x16x32_bf16 v[124:127], v[144:147], v[176:179], v[124:127]
	v_mfma_f32_16x16x32_bf16 v[120:123], v[152:155], v[176:179], v[120:123]
	v_mfma_f32_16x16x32_bf16 v[108:111], v[144:147], v[184:187], v[108:111]
	v_mfma_f32_16x16x32_bf16 v[104:107], v[152:155], v[184:187], v[104:107]
	v_mfma_f32_16x16x32_bf16 v[92:95], v[144:147], v[192:195], v[92:95]
	v_mfma_f32_16x16x32_bf16 v[88:91], v[152:155], v[192:195], v[88:91]
	v_mfma_f32_16x16x32_bf16 v[76:79], v[144:147], v[200:203], v[76:79]
	v_mfma_f32_16x16x32_bf16 v[72:75], v[152:155], v[200:203], v[72:75]
	v_mfma_f32_16x16x32_bf16 v[116:119], v[156:159], v[172:175], v[116:119]
	v_mfma_f32_16x16x32_bf16 v[112:115], v[164:167], v[172:175], v[112:115]
	v_mfma_f32_16x16x32_bf16 v[100:103], v[156:159], v[180:183], v[100:103]
	v_mfma_f32_16x16x32_bf16 v[96:99], v[164:167], v[180:183], v[96:99]
	v_mfma_f32_16x16x32_bf16 v[84:87], v[156:159], v[188:191], v[84:87]
	v_mfma_f32_16x16x32_bf16 v[80:83], v[164:167], v[188:191], v[80:83]
	v_mfma_f32_16x16x32_bf16 v[68:71], v[156:159], v[196:199], v[68:71]
	v_mfma_f32_16x16x32_bf16 v[64:67], v[164:167], v[196:199], v[64:67]
	v_mfma_f32_16x16x32_bf16 v[116:119], v[160:163], v[176:179], v[116:119]
	v_mfma_f32_16x16x32_bf16 v[112:115], v[168:171], v[176:179], v[112:115]
	v_mfma_f32_16x16x32_bf16 v[100:103], v[160:163], v[184:187], v[100:103]
	v_mfma_f32_16x16x32_bf16 v[96:99], v[168:171], v[184:187], v[96:99]
	v_mfma_f32_16x16x32_bf16 v[84:87], v[160:163], v[192:195], v[84:87]
	v_mfma_f32_16x16x32_bf16 v[80:83], v[168:171], v[192:195], v[80:83]
	v_mfma_f32_16x16x32_bf16 v[68:71], v[160:163], v[200:203], v[68:71]
	v_mfma_f32_16x16x32_bf16 v[64:67], v[168:171], v[200:203], v[64:67]
	s_setprio 0
	s_waitcnt vmcnt(8)
	s_barrier
	s_mov_b32 m0, s83
	ds_read_b128 v[172:175], v140 offset:16384
	ds_read_b128 v[176:179], v140 offset:17408
	ds_read_b128 v[180:183], v140 offset:18432
	ds_read_b128 v[184:187], v140 offset:19456
	ds_read_b128 v[188:191], v140 offset:20480
	ds_read_b128 v[192:195], v140 offset:21504
	ds_read_b128 v[196:199], v140 offset:22528
	ds_read_b128 v[200:203], v140 offset:23552
	global_load_lds_dwordx4 v244, s[58:59]
	s_mov_b32 m0, s84
	s_cselect_b32 s81, s49, s61
	s_cselect_b32 s80, s48, s60
	s_add_i32 s82, s72, s20
	global_load_lds_dwordx4 v246, s[58:59]
	s_mov_b32 m0, s82
	v_mov_b32_e32 v205, v129
	global_load_lds_dwordx4 v244, s[80:81]
	s_add_i32 m0, s82, 0x2000
	v_mov_b32_e32 v209, v129
	global_load_lds_dwordx4 v246, s[80:81]
	s_mov_b32 m0, s33
	v_lshl_add_u64 v[210:211], s[58:59], 0, v[244:245]
	global_load_lds_dwordx4 v240, s[56:57]
	s_mov_b32 m0, s62
	v_lshl_add_u64 v[212:213], s[58:59], 0, v[246:247]
	global_load_lds_dwordx4 v242, s[56:57]
	s_waitcnt lgkmcnt(0)
	v_lshl_add_u64 v[204:205], s[80:81], 0, v[244:245]
	v_lshl_add_u64 v[208:209], s[80:81], 0, v[246:247]
	v_lshl_add_u64 v[214:215], s[56:57], 0, v[240:241]
	v_lshl_add_u64 v[216:217], s[56:57], 0, v[242:243]
	s_waitcnt vmcnt(8)
	s_barrier
; #define G_STAGE(bufoff, gbase, voff) do { _Pragma("unroll") for (int _i = 0; _i < 2; ++_i) \
;         __builtin_amdgcn_global_load_lds((const unsigned*)((const char*)(gbase) + (voff)[_i]), (LAS unsigned*)(lds + (bufoff) + ldsw + _i * 8192), 16, 0, 0); } while (0)
; #define G_LDA(dst, b, h) do { _Pragma("unroll") for (int m = 0; m < 4; ++m) G_LD8(dst[m], lds + G_SA(b, h) + aoff + m * 2048); } while (0)
; #define G_LDB(dst, b, h) do { _Pragma("unroll") for (int n = 0; n < 2; ++n) G_LD8(dst[n], lds + G_SB(b, h) + boff + n * 2048); } while (0)
; #define G_WAIT_V(n) asm volatile("s_waitcnt vmcnt(" #n ")" ::: "memory")
; #define G_WAIT_L(n) asm volatile("s_waitcnt lgkmcnt(" #n ")" ::: "memory")
; #define G_BAR __builtin_amdgcn_s_barrier()
; #define G_SCHED __builtin_amdgcn_sched_barrier(0)
;     ...
;             G_WAIT_L(0); G_BAR; G_MMA(1, 0, At, B0); G_MMA(1, 1, At, B1); G_WAIT_V(8); G_BAR; G_SCHED;
;             G_LDB(B0, 1, 0); G_LDB(B1, 1, 1); G_SCHED; G_LDA(At, 1, 0); G_STAGE(G_SA(0, 1), a12, vA1);
;             G_WAIT_L(0); G_BAR; G_MMA(0, 0, At, B0); G_MMA(0, 1, At, B1); G_WAIT_V(8); G_BAR; G_SCHED;
	s_setprio 1
	s_waitcnt lgkmcnt(0)
	v_mfma_f32_16x16x32_bf16 v[60:63], v[130:133], v[172:175], v[60:63]
	v_mfma_f32_16x16x32_bf16 v[56:59], v[148:151], v[172:175], v[56:59]
	v_mfma_f32_16x16x32_bf16 v[44:47], v[130:133], v[180:183], v[44:47]
	v_mfma_f32_16x16x32_bf16 v[40:43], v[148:151], v[180:183], v[40:43]
	v_mfma_f32_16x16x32_bf16 v[28:31], v[130:133], v[188:191], v[28:31]
	v_mfma_f32_16x16x32_bf16 v[24:27], v[148:151], v[188:191], v[24:27]
	v_mfma_f32_16x16x32_bf16 v[12:15], v[130:133], v[196:199], v[12:15]
	v_mfma_f32_16x16x32_bf16 v[8:11], v[148:151], v[196:199], v[8:11]
	v_mfma_f32_16x16x32_bf16 v[60:63], v[144:147], v[176:179], v[60:63]
	v_mfma_f32_16x16x32_bf16 v[56:59], v[152:155], v[176:179], v[56:59]
	v_mfma_f32_16x16x32_bf16 v[44:47], v[144:147], v[184:187], v[44:47]
	v_mfma_f32_16x16x32_bf16 v[40:43], v[152:155], v[184:187], v[40:43]
	v_mfma_f32_16x16x32_bf16 v[28:31], v[144:147], v[192:195], v[28:31]
	v_mfma_f32_16x16x32_bf16 v[24:27], v[152:155], v[192:195], v[24:27]
	v_mfma_f32_16x16x32_bf16 v[12:15], v[144:147], v[200:203], v[12:15]
	v_mfma_f32_16x16x32_bf16 v[8:11], v[152:155], v[200:203], v[8:11]
	v_mfma_f32_16x16x32_bf16 v[52:55], v[156:159], v[172:175], v[52:55]
	v_mfma_f32_16x16x32_bf16 v[48:51], v[164:167], v[172:175], v[48:51]
	v_mfma_f32_16x16x32_bf16 v[36:39], v[156:159], v[180:183], v[36:39]
	v_mfma_f32_16x16x32_bf16 v[32:35], v[164:167], v[180:183], v[32:35]
	v_mfma_f32_16x16x32_bf16 v[20:23], v[156:159], v[188:191], v[20:23]
	v_mfma_f32_16x16x32_bf16 v[16:19], v[164:167], v[188:191], v[16:19]
	v_mfma_f32_16x16x32_bf16 v[4:7], v[156:159], v[196:199], v[4:7]
	v_mfma_f32_16x16x32_bf16 v[0:3], v[164:167], v[196:199], v[0:3]
	v_mfma_f32_16x16x32_bf16 v[52:55], v[160:163], v[176:179], v[52:55]
	v_mfma_f32_16x16x32_bf16 v[48:51], v[168:171], v[176:179], v[48:51]
	v_mfma_f32_16x16x32_bf16 v[36:39], v[160:163], v[184:187], v[36:39]
	v_mfma_f32_16x16x32_bf16 v[32:35], v[168:171], v[184:187], v[32:35]
	v_mfma_f32_16x16x32_bf16 v[20:23], v[160:163], v[192:195], v[20:23]
	v_mfma_f32_16x16x32_bf16 v[16:19], v[168:171], v[192:195], v[16:19]
	v_mfma_f32_16x16x32_bf16 v[4:7], v[160:163], v[200:203], v[4:7]
	v_mfma_f32_16x16x32_bf16 v[0:3], v[168:171], v[200:203], v[0:3]
	s_setprio 0
	s_waitcnt vmcnt(8)
	s_barrier
	s_add_i32 s56, 0, 0x18000
	s_add_i32 s57, 0, 0x1c000
	v_add_u32_e32 v152, s56, v137
	v_add_u32_e32 v168, s57, v137
	ds_read_b128 v[130:133], v152
	ds_read_b128 v[144:147], v152 offset:1024
	ds_read_b128 v[148:151], v152 offset:2048
	ds_read_b128 v[152:155], v152 offset:3072
	ds_read_b128 v[156:159], v168
	ds_read_b128 v[160:163], v168 offset:1024
	ds_read_b128 v[164:167], v168 offset:2048
	ds_read_b128 v[168:171], v168 offset:3072
	s_mov_b32 m0, s63
	ds_read_b128 v[172:175], v140 offset:32768
	ds_read_b128 v[176:179], v140 offset:33792
	ds_read_b128 v[180:183], v140 offset:34816
	ds_read_b128 v[184:187], v140 offset:35840
	ds_read_b128 v[188:191], v140 offset:36864
	ds_read_b128 v[192:195], v140 offset:37888
	ds_read_b128 v[196:199], v140 offset:38912
	ds_read_b128 v[200:203], v140 offset:39936
	global_load_lds_dwordx4 v240, s[54:55]
	s_mov_b32 m0, s64
	s_nop 0
	global_load_lds_dwordx4 v242, s[54:55]
	s_waitcnt lgkmcnt(0)
	s_waitcnt vmcnt(8)
	s_barrier
	s_setprio 1
	s_waitcnt lgkmcnt(0)
	v_mfma_f32_16x16x32_bf16 v[124:127], v[130:133], v[172:175], v[124:127]
	v_mfma_f32_16x16x32_bf16 v[120:123], v[148:151], v[172:175], v[120:123]
	v_mfma_f32_16x16x32_bf16 v[108:111], v[130:133], v[180:183], v[108:111]
	v_mfma_f32_16x16x32_bf16 v[104:107], v[148:151], v[180:183], v[104:107]
	v_mfma_f32_16x16x32_bf16 v[92:95], v[130:133], v[188:191], v[92:95]
	v_mfma_f32_16x16x32_bf16 v[88:91], v[148:151], v[188:191], v[88:91]
	v_mfma_f32_16x16x32_bf16 v[76:79], v[130:133], v[196:199], v[76:79]
	v_mfma_f32_16x16x32_bf16 v[72:75], v[148:151], v[196:199], v[72:75]
	v_mfma_f32_16x16x32_bf16 v[124:127], v[144:147], v[176:179], v[124:127]
	v_mfma_f32_16x16x32_bf16 v[120:123], v[152:155], v[176:179], v[120:123]
	v_mfma_f32_16x16x32_bf16 v[108:111], v[144:147], v[184:187], v[108:111]
	v_mfma_f32_16x16x32_bf16 v[104:107], v[152:155], v[184:187], v[104:107]
	v_mfma_f32_16x16x32_bf16 v[92:95], v[144:147], v[192:195], v[92:95]
	v_mfma_f32_16x16x32_bf16 v[88:91], v[152:155], v[192:195], v[88:91]
	v_mfma_f32_16x16x32_bf16 v[76:79], v[144:147], v[200:203], v[76:79]
	v_mfma_f32_16x16x32_bf16 v[72:75], v[152:155], v[200:203], v[72:75]
	v_mfma_f32_16x16x32_bf16 v[116:119], v[156:159], v[172:175], v[116:119]
	v_mfma_f32_16x16x32_bf16 v[112:115], v[164:167], v[172:175], v[112:115]
	v_mfma_f32_16x16x32_bf16 v[100:103], v[156:159], v[180:183], v[100:103]
	v_mfma_f32_16x16x32_bf16 v[96:99], v[164:167], v[180:183], v[96:99]
	v_mfma_f32_16x16x32_bf16 v[84:87], v[156:159], v[188:191], v[84:87]
	v_mfma_f32_16x16x32_bf16 v[80:83], v[164:167], v[188:191], v[80:83]
	v_mfma_f32_16x16x32_bf16 v[68:71], v[156:159], v[196:199], v[68:71]
	v_mfma_f32_16x16x32_bf16 v[64:67], v[164:167], v[196:199], v[64:67]
	v_mfma_f32_16x16x32_bf16 v[116:119], v[160:163], v[176:179], v[116:119]
	v_mfma_f32_16x16x32_bf16 v[112:115], v[168:171], v[176:179], v[112:115]
	v_mfma_f32_16x16x32_bf16 v[100:103], v[160:163], v[184:187], v[100:103]
	v_mfma_f32_16x16x32_bf16 v[96:99], v[168:171], v[184:187], v[96:99]
	v_mfma_f32_16x16x32_bf16 v[84:87], v[160:163], v[192:195], v[84:87]
	v_mfma_f32_16x16x32_bf16 v[80:83], v[168:171], v[192:195], v[80:83]
	v_mfma_f32_16x16x32_bf16 v[68:71], v[160:163], v[200:203], v[68:71]
	v_mfma_f32_16x16x32_bf16 v[64:67], v[168:171], v[200:203], v[64:67]
	s_setprio 0
	s_waitcnt vmcnt(8)
	s_barrier
; #define G_STAGE(bufoff, gbase, voff) do { _Pragma("unroll") for (int _i = 0; _i < 2; ++_i) \
;         __builtin_amdgcn_global_load_lds((const unsigned*)((const char*)(gbase) + (voff)[_i]), (LAS unsigned*)(lds + (bufoff) + ldsw + _i * 8192), 16, 0, 0); } while (0)
; #define G_LDA(dst, b, h) do { _Pragma("unroll") for (int m = 0; m < 4; ++m) G_LD8(dst[m], lds + G_SA(b, h) + aoff + m * 2048); } while (0)
; #define G_WAIT_V(n) asm volatile("s_waitcnt vmcnt(" #n ")" ::: "memory")
; #define G_WAIT_L(n) asm volatile("s_waitcnt lgkmcnt(" #n ")" ::: "memory")
; #define G_BAR __builtin_amdgcn_s_barrier()
; #define G_SCHED __builtin_amdgcn_sched_barrier(0)
;     ...
;             G_LDA(At, 1, 1); G_STAGE(G_SB(1, 0), b02 + kstep, voffB); G_STAGE(G_SB(1, 1), b12 + kstep, voffB); G_STAGE(G_SA(1, 0), a02 + kstep, vA0);
;             G_WAIT_L(0); G_BAR; G_MMA(1, 0, At, B0); G_MMA(1, 1, At, B1); G_WAIT_V(8); G_BAR; G_SCHED;
;         }
;         if (wr == 0) G_BAR;
	s_add_i32 s54, s56, s20
	v_lshl_add_u64 v[206:207], v[210:211], 0, s[34:35]
	s_mov_b32 m0, s54
	ds_read_b128 v[172:175], v140 offset:49152
	ds_read_b128 v[176:179], v140 offset:50176
	ds_read_b128 v[180:183], v140 offset:51200
	ds_read_b128 v[184:187], v140 offset:52224
	ds_read_b128 v[188:191], v140 offset:53248
	ds_read_b128 v[192:195], v140 offset:54272
	ds_read_b128 v[196:199], v140 offset:55296
	ds_read_b128 v[200:203], v140 offset:56320
	global_load_lds_dwordx4 v[206:207], off
	v_lshl_add_u64 v[206:207], v[212:213], 0, s[34:35]
	s_add_i32 m0, s54, 0x2000
	s_add_i32 s54, s57, s20
	global_load_lds_dwordx4 v[206:207], off
	v_lshl_add_u64 v[204:205], v[204:205], 0, s[34:35]
	s_mov_b32 m0, s54
	s_nop 0
	global_load_lds_dwordx4 v[204:205], off
	v_lshl_add_u64 v[204:205], v[208:209], 0, s[34:35]
	s_add_i32 m0, s54, 0x2000
	s_nop 0
	global_load_lds_dwordx4 v[204:205], off
	v_lshl_add_u64 v[204:205], v[214:215], 0, s[34:35]
	s_mov_b32 m0, s66
	s_nop 0
	global_load_lds_dwordx4 v[204:205], off
	v_lshl_add_u64 v[204:205], v[216:217], 0, s[34:35]
	s_mov_b32 m0, s67
	s_nop 0
	global_load_lds_dwordx4 v[204:205], off
	s_waitcnt lgkmcnt(0)
	s_waitcnt vmcnt(8)
	s_barrier
	s_setprio 1
	s_waitcnt lgkmcnt(0)
	v_mfma_f32_16x16x32_bf16 v[60:63], v[130:133], v[172:175], v[60:63]
	v_mfma_f32_16x16x32_bf16 v[56:59], v[148:151], v[172:175], v[56:59]
	v_mfma_f32_16x16x32_bf16 v[44:47], v[130:133], v[180:183], v[44:47]
	v_mfma_f32_16x16x32_bf16 v[40:43], v[148:151], v[180:183], v[40:43]
	v_mfma_f32_16x16x32_bf16 v[28:31], v[130:133], v[188:191], v[28:31]
	v_mfma_f32_16x16x32_bf16 v[24:27], v[148:151], v[188:191], v[24:27]
	v_mfma_f32_16x16x32_bf16 v[12:15], v[130:133], v[196:199], v[12:15]
	v_mfma_f32_16x16x32_bf16 v[8:11], v[148:151], v[196:199], v[8:11]
	v_mfma_f32_16x16x32_bf16 v[60:63], v[144:147], v[176:179], v[60:63]
	v_mfma_f32_16x16x32_bf16 v[56:59], v[152:155], v[176:179], v[56:59]
	v_mfma_f32_16x16x32_bf16 v[44:47], v[144:147], v[184:187], v[44:47]
	v_mfma_f32_16x16x32_bf16 v[40:43], v[152:155], v[184:187], v[40:43]
	v_mfma_f32_16x16x32_bf16 v[28:31], v[144:147], v[192:195], v[28:31]
	v_mfma_f32_16x16x32_bf16 v[24:27], v[152:155], v[192:195], v[24:27]
	v_mfma_f32_16x16x32_bf16 v[12:15], v[144:147], v[200:203], v[12:15]
	v_mfma_f32_16x16x32_bf16 v[8:11], v[152:155], v[200:203], v[8:11]
	v_mfma_f32_16x16x32_bf16 v[52:55], v[156:159], v[172:175], v[52:55]
	v_mfma_f32_16x16x32_bf16 v[48:51], v[164:167], v[172:175], v[48:51]
	v_mfma_f32_16x16x32_bf16 v[36:39], v[156:159], v[180:183], v[36:39]
	v_mfma_f32_16x16x32_bf16 v[32:35], v[164:167], v[180:183], v[32:35]
	v_mfma_f32_16x16x32_bf16 v[20:23], v[156:159], v[188:191], v[20:23]
	v_mfma_f32_16x16x32_bf16 v[16:19], v[164:167], v[188:191], v[16:19]
	v_mfma_f32_16x16x32_bf16 v[4:7], v[156:159], v[196:199], v[4:7]
	v_mfma_f32_16x16x32_bf16 v[0:3], v[164:167], v[196:199], v[0:3]
	v_mfma_f32_16x16x32_bf16 v[52:55], v[160:163], v[176:179], v[52:55]
	v_mfma_f32_16x16x32_bf16 v[48:51], v[168:171], v[176:179], v[48:51]
	v_mfma_f32_16x16x32_bf16 v[36:39], v[160:163], v[184:187], v[36:39]
	v_mfma_f32_16x16x32_bf16 v[32:35], v[168:171], v[184:187], v[32:35]
	v_mfma_f32_16x16x32_bf16 v[20:23], v[160:163], v[192:195], v[20:23]
	v_mfma_f32_16x16x32_bf16 v[16:19], v[168:171], v[192:195], v[16:19]
	v_mfma_f32_16x16x32_bf16 v[4:7], v[160:163], v[200:203], v[4:7]
	v_mfma_f32_16x16x32_bf16 v[0:3], v[168:171], v[200:203], v[0:3]
	s_setprio 0
	s_waitcnt vmcnt(8)
	s_barrier
	s_add_u32 s5, s5, 0x100
	s_addc_u32 s41, s41, 0
	s_add_u32 s60, s60, 0x100
	s_addc_u32 s61, s61, 0
	s_add_u32 s77, s77, 0x100
	s_addc_u32 s78, s78, 0
	s_add_u32 s52, s52, 0x100
	s_addc_u32 s53, s53, 0
	s_cmp_ge_i32 s79, s24
	s_mov_b32 s54, s79
	s_cbranch_scc0 .LBB0_1058
	v_readlane_b32 s78, v255, 11
	v_readlane_b32 s79, v255, 13
	s_and_b64 vcc, exec, s[38:39]
	s_cbranch_vccz .LBB0_1061

; #define G_STAGE(bufoff, gbase, voff) do { _Pragma("unroll") for (int _i = 0; _i < 2; ++_i) \
;         __builtin_amdgcn_global_load_lds((const unsigned*)((const char*)(gbase) + (voff)[_i]), (LAS unsigned*)(lds + (bufoff) + ldsw + _i * 8192), 16, 0, 0); } while (0)
; #define G_LDA(dst, b, h) do { _Pragma("unroll") for (int m = 0; m < 4; ++m) G_LD8(dst[m], lds + G_SA(b, h) + aoff + m * 2048); } while (0)
; #define G_LDB(dst, b, h) do { _Pragma("unroll") for (int n = 0; n < 2; ++n) G_LD8(dst[n], lds + G_SB(b, h) + boff + n * 2048); } while (0)
; #define G_WAIT_V(n) asm volatile("s_waitcnt vmcnt(" #n ")" ::: "memory")
; #define G_WAIT_L(n) asm volatile("s_waitcnt lgkmcnt(" #n ")" ::: "memory")
; #define G_BAR __builtin_amdgcn_s_barrier()
; #define G_SCHED __builtin_amdgcn_sched_barrier(0)
;     __device__ __forceinline__ unsigned row_off(const Unit& u, int r, LAS unsigned char* lds) const { return (unsigned)((const LAS int*)(lds + LDS_STAGE + u.q * 4096))[r] * (unsigned)rowbytes; }
;     ...
;             const char* a11 = cur.a1 + (size_t)(t + 1) * kstep;
;             const char* a02 = last ? nxt.a0 : cur.a0 + (size_t)(t + 2) * kstep; const char* a12 = last ? nxt.a1 : cur.a1 + (size_t)(t + 2) * kstep;
;             const char* b02 = last ? nxt.b0 : cur.b0 + (size_t)(t + 2) * kstep; const char* b12 = last ? nxt.b1 : cur.b1 + (size_t)(t + 2) * kstep;
;             G_LDB(B0, 0, 0); G_LDB(B1, 0, 1); G_SCHED; G_LDA(At, 0, 0); G_STAGE(G_SA(1, 1), a11, vA1);
;             if constexpr (GATHER) { if (last) { int tz = tid; asm volatile("" : "+v"(tz));
; #pragma unroll
;                 for (int i = 0; i < 2; ++i) { int R, C; stage_rc(tz * 16 + i * 8192, R, C); gc0[i] = S.row_off(nxt, R, lds) + (unsigned)C * 2u; gc1[i] = S.row_off(nxt, 128 + R, lds) + (unsigned)C * 2u; } } }
;             G_WAIT_L(0); G_BAR; G_MMA(0, 0, At, B0); G_MMA(0, 1, At, B1); G_WAIT_V(8); G_BAR; G_SCHED;
;             G_LDA(At, 0, 1); G_STAGE(G_SB(0, 0), b02, voffB); G_STAGE(G_SB(0, 1), b12, voffB); G_STAGE(G_SA(0, 0), a02, vA0);
;             G_WAIT_L(0); G_BAR; G_MMA(1, 0, At, B0); G_MMA(1, 1, At, B1); G_WAIT_V(8); G_BAR; G_SCHED;
.LBB0_1322:
	s_add_i32 vcc_lo, s66, 2
	s_add_u32 vcc_hi, s64, 0x80
	s_addc_u32 s67, s65, 0
	s_add_i32 s68, 0, 0x10000
	s_add_i32 s1, 0, 0x14000
	v_add_u32_e32 v146, s68, v172
	v_add_u32_e32 v162, s1, v172
	ds_read_b128 v[130:133], v146
	ds_read_b128 v[134:137], v146 offset:1024
	ds_read_b128 v[138:141], v146 offset:2048
	ds_read_b128 v[146:149], v146 offset:3072
	ds_read_b128 v[150:153], v162
	ds_read_b128 v[154:157], v162 offset:1024
	ds_read_b128 v[158:161], v162 offset:2048
	ds_read_b128 v[162:165], v162 offset:3072
	s_add_i32 s11, s68, s77
	s_add_i32 m0, s10, 0xc000
	s_add_i32 s33, s10, 0xe000
	s_add_i32 s21, s11, 0x2000
	s_cmp_eq_u32 s89, s66
	s_cselect_b32 s66, s54, vcc_hi
	s_cselect_b32 s69, s53, s97
	s_cselect_b32 s68, s52, s96
	s_cselect_b32 s71, s57, s93
	s_cselect_b32 s70, s56, s9
	s_cselect_b32 s67, s55, s67
	ds_read_b128 v[174:177], v173
	ds_read_b128 v[178:181], v173 offset:1024
	ds_read_b128 v[182:185], v173 offset:2048
	ds_read_b128 v[186:189], v173 offset:3072
	ds_read_b128 v[190:193], v173 offset:4096
	ds_read_b128 v[194:197], v173 offset:5120
	ds_read_b128 v[198:201], v173 offset:6144
	ds_read_b128 v[202:205], v173 offset:7168
	global_load_lds_dwordx4 v240, s[64:65]
	s_mov_b32 m0, s33
	s_nop 0
	global_load_lds_dwordx4 v242, s[64:65]
	s_waitcnt lgkmcnt(0)
	v_mov_b32_e32 v129, v145
	s_waitcnt vmcnt(8)
	s_barrier
	s_setprio 1
	s_waitcnt lgkmcnt(0)
	v_mfma_f32_16x16x32_bf16 v[124:127], v[130:133], v[174:177], v[124:127]
	v_mfma_f32_16x16x32_bf16 v[120:123], v[138:141], v[174:177], v[120:123]
	v_mfma_f32_16x16x32_bf16 v[116:119], v[130:133], v[182:185], v[116:119]
	v_mfma_f32_16x16x32_bf16 v[112:115], v[138:141], v[182:185], v[112:115]
	v_mfma_f32_16x16x32_bf16 v[108:111], v[130:133], v[190:193], v[108:111]
	v_mfma_f32_16x16x32_bf16 v[104:107], v[138:141], v[190:193], v[104:107]
	v_mfma_f32_16x16x32_bf16 v[100:103], v[130:133], v[198:201], v[100:103]
	v_mfma_f32_16x16x32_bf16 v[96:99], v[138:141], v[198:201], v[96:99]
	v_mfma_f32_16x16x32_bf16 v[124:127], v[134:137], v[178:181], v[124:127]
	v_mfma_f32_16x16x32_bf16 v[120:123], v[146:149], v[178:181], v[120:123]
	v_mfma_f32_16x16x32_bf16 v[116:119], v[134:137], v[186:189], v[116:119]
	v_mfma_f32_16x16x32_bf16 v[112:115], v[146:149], v[186:189], v[112:115]
	v_mfma_f32_16x16x32_bf16 v[108:111], v[134:137], v[194:197], v[108:111]
	v_mfma_f32_16x16x32_bf16 v[104:107], v[146:149], v[194:197], v[104:107]
	v_mfma_f32_16x16x32_bf16 v[100:103], v[134:137], v[202:205], v[100:103]
	v_mfma_f32_16x16x32_bf16 v[96:99], v[146:149], v[202:205], v[96:99]
	v_mfma_f32_16x16x32_bf16 v[68:71], v[150:153], v[174:177], v[68:71]
	v_mfma_f32_16x16x32_bf16 v[60:63], v[158:161], v[174:177], v[60:63]
	v_mfma_f32_16x16x32_bf16 v[52:55], v[150:153], v[182:185], v[52:55]
	v_mfma_f32_16x16x32_bf16 v[48:51], v[158:161], v[182:185], v[48:51]
	v_mfma_f32_16x16x32_bf16 v[44:47], v[150:153], v[190:193], v[44:47]
	v_mfma_f32_16x16x32_bf16 v[40:43], v[158:161], v[190:193], v[40:43]
	v_mfma_f32_16x16x32_bf16 v[36:39], v[150:153], v[198:201], v[36:39]
	v_mfma_f32_16x16x32_bf16 v[32:35], v[158:161], v[198:201], v[32:35]
	v_mfma_f32_16x16x32_bf16 v[68:71], v[154:157], v[178:181], v[68:71]
	v_mfma_f32_16x16x32_bf16 v[60:63], v[162:165], v[178:181], v[60:63]
	v_mfma_f32_16x16x32_bf16 v[52:55], v[154:157], v[186:189], v[52:55]
	v_mfma_f32_16x16x32_bf16 v[48:51], v[162:165], v[186:189], v[48:51]
	v_mfma_f32_16x16x32_bf16 v[44:47], v[154:157], v[194:197], v[44:47]
	v_mfma_f32_16x16x32_bf16 v[40:43], v[162:165], v[194:197], v[40:43]
	v_mfma_f32_16x16x32_bf16 v[36:39], v[154:157], v[202:205], v[36:39]
	v_mfma_f32_16x16x32_bf16 v[32:35], v[162:165], v[202:205], v[32:35]
	s_setprio 0
	s_waitcnt vmcnt(8)
	s_barrier
	s_mov_b32 m0, s11
	ds_read_b128 v[174:177], v173 offset:16384
	ds_read_b128 v[178:181], v173 offset:17408
	ds_read_b128 v[182:185], v173 offset:18432
	ds_read_b128 v[186:189], v173 offset:19456
	ds_read_b128 v[190:193], v173 offset:20480
	ds_read_b128 v[194:197], v173 offset:21504
	ds_read_b128 v[198:201], v173 offset:22528
	ds_read_b128 v[202:205], v173 offset:23552
	v_mov_b32_e32 v143, v145
	global_load_lds_dwordx4 v244, s[70:71]
	v_mov_b32_e32 v207, v145
	s_mov_b32 m0, s21
	v_lshl_add_u64 v[208:209], s[70:71], 0, v[244:245]
	v_lshl_add_u64 v[210:211], s[70:71], 0, v[246:247]
	global_load_lds_dwordx4 v246, s[70:71]
	s_cselect_b32 s71, s59, s95
	s_cselect_b32 s70, s58, s94
	s_add_i32 s1, s1, s77
	s_mov_b32 m0, s1
	v_lshl_add_u64 v[212:213], s[70:71], 0, v[244:245]
	global_load_lds_dwordx4 v244, s[70:71]
	s_add_i32 m0, s1, 0x2000
	v_lshl_add_u64 v[142:143], s[70:71], 0, v[246:247]
	global_load_lds_dwordx4 v246, s[70:71]
	s_mov_b32 m0, s10
	v_lshl_add_u64 v[206:207], s[68:69], 0, v[240:241]
	global_load_lds_dwordx4 v240, s[68:69]
	s_mov_b32 m0, s63
	v_lshl_add_u64 v[214:215], s[68:69], 0, v[242:243]
	global_load_lds_dwordx4 v242, s[68:69]
	s_waitcnt lgkmcnt(0)
	s_waitcnt vmcnt(8)
	s_barrier
; #define G_STAGE(bufoff, gbase, voff) do { _Pragma("unroll") for (int _i = 0; _i < 2; ++_i) \
;         __builtin_amdgcn_global_load_lds((const unsigned*)((const char*)(gbase) + (voff)[_i]), (LAS unsigned*)(lds + (bufoff) + ldsw + _i * 8192), 16, 0, 0); } while (0)
; #define G_LDA(dst, b, h) do { _Pragma("unroll") for (int m = 0; m < 4; ++m) G_LD8(dst[m], lds + G_SA(b, h) + aoff + m * 2048); } while (0)
; #define G_LDB(dst, b, h) do { _Pragma("unroll") for (int n = 0; n < 2; ++n) G_LD8(dst[n], lds + G_SB(b, h) + boff + n * 2048); } while (0)
; #define G_WAIT_V(n) asm volatile("s_waitcnt vmcnt(" #n ")" ::: "memory")
; #define G_WAIT_L(n) asm volatile("s_waitcnt lgkmcnt(" #n ")" ::: "memory")
; #define G_BAR __builtin_amdgcn_s_barrier()
; #define G_SCHED __builtin_amdgcn_sched_barrier(0)
;     ...
;             G_WAIT_L(0); G_BAR; G_MMA(1, 0, At, B0); G_MMA(1, 1, At, B1); G_WAIT_V(8); G_BAR; G_SCHED;
;             G_LDB(B0, 1, 0); G_LDB(B1, 1, 1); G_SCHED; G_LDA(At, 1, 0); G_STAGE(G_SA(0, 1), a12, vA1);
;             G_WAIT_L(0); G_BAR; G_MMA(0, 0, At, B0); G_MMA(0, 1, At, B1); G_WAIT_V(8); G_BAR; G_SCHED;
	s_setprio 1
	s_waitcnt lgkmcnt(0)
	v_mfma_f32_16x16x32_bf16 v[92:95], v[130:133], v[174:177], v[92:95]
	v_mfma_f32_16x16x32_bf16 v[88:91], v[138:141], v[174:177], v[88:91]
	v_mfma_f32_16x16x32_bf16 v[84:87], v[130:133], v[182:185], v[84:87]
	v_mfma_f32_16x16x32_bf16 v[80:83], v[138:141], v[182:185], v[80:83]
	v_mfma_f32_16x16x32_bf16 v[76:79], v[130:133], v[190:193], v[76:79]
	v_mfma_f32_16x16x32_bf16 v[72:75], v[138:141], v[190:193], v[72:75]
	v_mfma_f32_16x16x32_bf16 v[64:67], v[130:133], v[198:201], v[64:67]
	v_mfma_f32_16x16x32_bf16 v[56:59], v[138:141], v[198:201], v[56:59]
	v_mfma_f32_16x16x32_bf16 v[92:95], v[134:137], v[178:181], v[92:95]
	v_mfma_f32_16x16x32_bf16 v[88:91], v[146:149], v[178:181], v[88:91]
	v_mfma_f32_16x16x32_bf16 v[84:87], v[134:137], v[186:189], v[84:87]
	v_mfma_f32_16x16x32_bf16 v[80:83], v[146:149], v[186:189], v[80:83]
	v_mfma_f32_16x16x32_bf16 v[76:79], v[134:137], v[194:197], v[76:79]
	v_mfma_f32_16x16x32_bf16 v[72:75], v[146:149], v[194:197], v[72:75]
	v_mfma_f32_16x16x32_bf16 v[64:67], v[134:137], v[202:205], v[64:67]
	v_mfma_f32_16x16x32_bf16 v[56:59], v[146:149], v[202:205], v[56:59]
	v_mfma_f32_16x16x32_bf16 v[28:31], v[150:153], v[174:177], v[28:31]
	v_mfma_f32_16x16x32_bf16 v[24:27], v[158:161], v[174:177], v[24:27]
	v_mfma_f32_16x16x32_bf16 v[20:23], v[150:153], v[182:185], v[20:23]
	v_mfma_f32_16x16x32_bf16 v[16:19], v[158:161], v[182:185], v[16:19]
	v_mfma_f32_16x16x32_bf16 v[12:15], v[150:153], v[190:193], v[12:15]
	v_mfma_f32_16x16x32_bf16 v[8:11], v[158:161], v[190:193], v[8:11]
	v_mfma_f32_16x16x32_bf16 v[4:7], v[150:153], v[198:201], v[4:7]
	v_mfma_f32_16x16x32_bf16 v[0:3], v[158:161], v[198:201], v[0:3]
	v_mfma_f32_16x16x32_bf16 v[28:31], v[154:157], v[178:181], v[28:31]
	v_mfma_f32_16x16x32_bf16 v[24:27], v[162:165], v[178:181], v[24:27]
	v_mfma_f32_16x16x32_bf16 v[20:23], v[154:157], v[186:189], v[20:23]
	v_mfma_f32_16x16x32_bf16 v[16:19], v[162:165], v[186:189], v[16:19]
	v_mfma_f32_16x16x32_bf16 v[12:15], v[154:157], v[194:197], v[12:15]
	v_mfma_f32_16x16x32_bf16 v[8:11], v[162:165], v[194:197], v[8:11]
	v_mfma_f32_16x16x32_bf16 v[4:7], v[154:157], v[202:205], v[4:7]
	v_mfma_f32_16x16x32_bf16 v[0:3], v[162:165], v[202:205], v[0:3]
	s_setprio 0
	s_waitcnt vmcnt(8)
	s_barrier
	s_add_i32 s1, 0, 0x18000
	v_add_u32_e32 v129, s1, v172
	s_add_i32 s11, 0, 0x1c000
	ds_read_b128 v[130:133], v129
	ds_read_b128 v[134:137], v129 offset:1024
	ds_read_b128 v[138:141], v129 offset:2048
	ds_read_b128 v[146:149], v129 offset:3072
	v_add_u32_e32 v129, s11, v172
	ds_read_b128 v[150:153], v129
	ds_read_b128 v[154:157], v129 offset:1024
	ds_read_b128 v[158:161], v129 offset:2048
	ds_read_b128 v[162:165], v129 offset:3072
	s_mov_b32 m0, s72
	ds_read_b128 v[174:177], v173 offset:32768
	ds_read_b128 v[178:181], v173 offset:33792
	ds_read_b128 v[182:185], v173 offset:34816
	ds_read_b128 v[186:189], v173 offset:35840
	ds_read_b128 v[190:193], v173 offset:36864
	ds_read_b128 v[194:197], v173 offset:37888
	ds_read_b128 v[198:201], v173 offset:38912
	ds_read_b128 v[202:205], v173 offset:39936
	global_load_lds_dwordx4 v240, s[66:67]
	s_mov_b32 m0, s73
	s_nop 0
	global_load_lds_dwordx4 v242, s[66:67]
	s_waitcnt lgkmcnt(0)
	s_waitcnt vmcnt(8)
	s_barrier
	s_setprio 1
	s_waitcnt lgkmcnt(0)
	v_mfma_f32_16x16x32_bf16 v[124:127], v[130:133], v[174:177], v[124:127]
	v_mfma_f32_16x16x32_bf16 v[120:123], v[138:141], v[174:177], v[120:123]
	v_mfma_f32_16x16x32_bf16 v[116:119], v[130:133], v[182:185], v[116:119]
	v_mfma_f32_16x16x32_bf16 v[112:115], v[138:141], v[182:185], v[112:115]
	v_mfma_f32_16x16x32_bf16 v[108:111], v[130:133], v[190:193], v[108:111]
	v_mfma_f32_16x16x32_bf16 v[104:107], v[138:141], v[190:193], v[104:107]
	v_mfma_f32_16x16x32_bf16 v[100:103], v[130:133], v[198:201], v[100:103]
	v_mfma_f32_16x16x32_bf16 v[96:99], v[138:141], v[198:201], v[96:99]
	v_mfma_f32_16x16x32_bf16 v[124:127], v[134:137], v[178:181], v[124:127]
	v_mfma_f32_16x16x32_bf16 v[120:123], v[146:149], v[178:181], v[120:123]
	v_mfma_f32_16x16x32_bf16 v[116:119], v[134:137], v[186:189], v[116:119]
	v_mfma_f32_16x16x32_bf16 v[112:115], v[146:149], v[186:189], v[112:115]
	v_mfma_f32_16x16x32_bf16 v[108:111], v[134:137], v[194:197], v[108:111]
	v_mfma_f32_16x16x32_bf16 v[104:107], v[146:149], v[194:197], v[104:107]
	v_mfma_f32_16x16x32_bf16 v[100:103], v[134:137], v[202:205], v[100:103]
	v_mfma_f32_16x16x32_bf16 v[96:99], v[146:149], v[202:205], v[96:99]
	v_mfma_f32_16x16x32_bf16 v[68:71], v[150:153], v[174:177], v[68:71]
	v_mfma_f32_16x16x32_bf16 v[60:63], v[158:161], v[174:177], v[60:63]
	v_mfma_f32_16x16x32_bf16 v[52:55], v[150:153], v[182:185], v[52:55]
	v_mfma_f32_16x16x32_bf16 v[48:51], v[158:161], v[182:185], v[48:51]
	v_mfma_f32_16x16x32_bf16 v[44:47], v[150:153], v[190:193], v[44:47]
	v_mfma_f32_16x16x32_bf16 v[40:43], v[158:161], v[190:193], v[40:43]
	v_mfma_f32_16x16x32_bf16 v[36:39], v[150:153], v[198:201], v[36:39]
	v_mfma_f32_16x16x32_bf16 v[32:35], v[158:161], v[198:201], v[32:35]
	v_mfma_f32_16x16x32_bf16 v[68:71], v[154:157], v[178:181], v[68:71]
	v_mfma_f32_16x16x32_bf16 v[60:63], v[162:165], v[178:181], v[60:63]
	v_mfma_f32_16x16x32_bf16 v[52:55], v[154:157], v[186:189], v[52:55]
	v_mfma_f32_16x16x32_bf16 v[48:51], v[162:165], v[186:189], v[48:51]
	v_mfma_f32_16x16x32_bf16 v[44:47], v[154:157], v[194:197], v[44:47]
	v_mfma_f32_16x16x32_bf16 v[40:43], v[162:165], v[194:197], v[40:43]
	v_mfma_f32_16x16x32_bf16 v[36:39], v[154:157], v[202:205], v[36:39]
	v_mfma_f32_16x16x32_bf16 v[32:35], v[162:165], v[202:205], v[32:35]
	s_setprio 0
	s_waitcnt vmcnt(8)
	s_barrier
; #define G_STAGE(bufoff, gbase, voff) do { _Pragma("unroll") for (int _i = 0; _i < 2; ++_i) \
;         __builtin_amdgcn_global_load_lds((const unsigned*)((const char*)(gbase) + (voff)[_i]), (LAS unsigned*)(lds + (bufoff) + ldsw + _i * 8192), 16, 0, 0); } while (0)
; #define G_LDA(dst, b, h) do { _Pragma("unroll") for (int m = 0; m < 4; ++m) G_LD8(dst[m], lds + G_SA(b, h) + aoff + m * 2048); } while (0)
; #define G_WAIT_V(n) asm volatile("s_waitcnt vmcnt(" #n ")" ::: "memory")
; #define G_WAIT_L(n) asm volatile("s_waitcnt lgkmcnt(" #n ")" ::: "memory")
; #define G_BAR __builtin_amdgcn_s_barrier()
; #define G_SCHED __builtin_amdgcn_sched_barrier(0)
;     ...
;             G_LDA(At, 1, 1); G_STAGE(G_SB(1, 0), b02 + kstep, voffB); G_STAGE(G_SB(1, 1), b12 + kstep, voffB); G_STAGE(G_SA(1, 0), a02 + kstep, vA0);
;             G_WAIT_L(0); G_BAR; G_MMA(1, 0, At, B0); G_MMA(1, 1, At, B1); G_WAIT_V(8); G_BAR; G_SCHED;
;         }
;         if (wr == 0) G_BAR;
	s_add_i32 s1, s1, s77
	v_lshl_add_u64 v[128:129], v[208:209], 0, s[48:49]
	s_mov_b32 m0, s1
	ds_read_b128 v[174:177], v173 offset:49152
	ds_read_b128 v[178:181], v173 offset:50176
	ds_read_b128 v[182:185], v173 offset:51200
	ds_read_b128 v[186:189], v173 offset:52224
	ds_read_b128 v[190:193], v173 offset:53248
	ds_read_b128 v[194:197], v173 offset:54272
	ds_read_b128 v[198:201], v173 offset:55296
	ds_read_b128 v[202:205], v173 offset:56320
	global_load_lds_dwordx4 v[128:129], off
	v_lshl_add_u64 v[128:129], v[210:211], 0, s[48:49]
	s_add_i32 m0, s1, 0x2000
	s_add_i32 s1, s11, s77
	global_load_lds_dwordx4 v[128:129], off
	v_lshl_add_u64 v[128:129], v[212:213], 0, s[48:49]
	s_mov_b32 m0, s1
	s_nop 0
	global_load_lds_dwordx4 v[128:129], off
	v_lshl_add_u64 v[128:129], v[142:143], 0, s[48:49]
	s_add_i32 m0, s1, 0x2000
	s_nop 0
	global_load_lds_dwordx4 v[128:129], off
	v_lshl_add_u64 v[128:129], v[206:207], 0, s[48:49]
	s_mov_b32 m0, s75
	s_nop 0
	global_load_lds_dwordx4 v[128:129], off
	v_lshl_add_u64 v[128:129], v[214:215], 0, s[48:49]
	s_mov_b32 m0, s76
	s_nop 0
	global_load_lds_dwordx4 v[128:129], off
	s_waitcnt lgkmcnt(0)
	s_waitcnt vmcnt(8)
	s_barrier
	s_setprio 1
	s_waitcnt lgkmcnt(0)
	v_mfma_f32_16x16x32_bf16 v[92:95], v[130:133], v[174:177], v[92:95]
	v_mfma_f32_16x16x32_bf16 v[88:91], v[138:141], v[174:177], v[88:91]
	v_mfma_f32_16x16x32_bf16 v[84:87], v[130:133], v[182:185], v[84:87]
	v_mfma_f32_16x16x32_bf16 v[80:83], v[138:141], v[182:185], v[80:83]
	v_mfma_f32_16x16x32_bf16 v[76:79], v[130:133], v[190:193], v[76:79]
	v_mfma_f32_16x16x32_bf16 v[72:75], v[138:141], v[190:193], v[72:75]
	v_mfma_f32_16x16x32_bf16 v[64:67], v[130:133], v[198:201], v[64:67]
	v_mfma_f32_16x16x32_bf16 v[56:59], v[138:141], v[198:201], v[56:59]
	v_mfma_f32_16x16x32_bf16 v[92:95], v[134:137], v[178:181], v[92:95]
	v_mfma_f32_16x16x32_bf16 v[88:91], v[146:149], v[178:181], v[88:91]
	v_mfma_f32_16x16x32_bf16 v[84:87], v[134:137], v[186:189], v[84:87]
	v_mfma_f32_16x16x32_bf16 v[80:83], v[146:149], v[186:189], v[80:83]
	v_mfma_f32_16x16x32_bf16 v[76:79], v[134:137], v[194:197], v[76:79]
	v_mfma_f32_16x16x32_bf16 v[72:75], v[146:149], v[194:197], v[72:75]
	v_mfma_f32_16x16x32_bf16 v[64:67], v[134:137], v[202:205], v[64:67]
	v_mfma_f32_16x16x32_bf16 v[56:59], v[146:149], v[202:205], v[56:59]
	v_mfma_f32_16x16x32_bf16 v[28:31], v[150:153], v[174:177], v[28:31]
	v_mfma_f32_16x16x32_bf16 v[24:27], v[158:161], v[174:177], v[24:27]
	v_mfma_f32_16x16x32_bf16 v[20:23], v[150:153], v[182:185], v[20:23]
	v_mfma_f32_16x16x32_bf16 v[16:19], v[158:161], v[182:185], v[16:19]
	v_mfma_f32_16x16x32_bf16 v[12:15], v[150:153], v[190:193], v[12:15]
	v_mfma_f32_16x16x32_bf16 v[8:11], v[158:161], v[190:193], v[8:11]
	v_mfma_f32_16x16x32_bf16 v[4:7], v[150:153], v[198:201], v[4:7]
	v_mfma_f32_16x16x32_bf16 v[0:3], v[158:161], v[198:201], v[0:3]
	v_mfma_f32_16x16x32_bf16 v[28:31], v[154:157], v[178:181], v[28:31]
	v_mfma_f32_16x16x32_bf16 v[24:27], v[162:165], v[178:181], v[24:27]
	v_mfma_f32_16x16x32_bf16 v[20:23], v[154:157], v[186:189], v[20:23]
	v_mfma_f32_16x16x32_bf16 v[16:19], v[162:165], v[186:189], v[16:19]
	v_mfma_f32_16x16x32_bf16 v[12:15], v[154:157], v[194:197], v[12:15]
	v_mfma_f32_16x16x32_bf16 v[8:11], v[162:165], v[194:197], v[8:11]
	v_mfma_f32_16x16x32_bf16 v[4:7], v[154:157], v[202:205], v[4:7]
	v_mfma_f32_16x16x32_bf16 v[0:3], v[162:165], v[202:205], v[0:3]
	s_setprio 0
	s_waitcnt vmcnt(8)
	s_barrier
	s_add_u32 s9, s9, 0x100
	s_addc_u32 s93, s93, 0
	s_add_u32 s94, s94, 0x100
	s_addc_u32 s95, s95, 0
	s_add_u32 s96, s96, 0x100
	s_addc_u32 s97, s97, 0
	s_add_u32 s64, s64, 0x100
	s_addc_u32 s65, s65, 0
	s_cmp_ge_i32 vcc_lo, s2
	s_mov_b32 s66, vcc_lo
	s_cbranch_scc0 .LBB0_1322
	v_readlane_b32 s64, v255, 9
	v_readlane_b32 s65, v255, 10
	s_load_dword s97, s[64:65], 0xa8
	s_and_b64 vcc, exec, s[46:47]
	s_cbranch_vccz .LBB0_1325

; #define G_STAGE(bufoff, gbase, voff) do { _Pragma("unroll") for (int _i = 0; _i < 2; ++_i) \
;         __builtin_amdgcn_global_load_lds((const unsigned*)((const char*)(gbase) + (voff)[_i]), (LAS unsigned*)(lds + (bufoff) + ldsw + _i * 8192), 16, 0, 0); } while (0)
; #define G_LDA(dst, b, h) do { _Pragma("unroll") for (int m = 0; m < 4; ++m) G_LD8(dst[m], lds + G_SA(b, h) + aoff + m * 2048); } while (0)
; #define G_LDB(dst, b, h) do { _Pragma("unroll") for (int n = 0; n < 2; ++n) G_LD8(dst[n], lds + G_SB(b, h) + boff + n * 2048); } while (0)
; #define G_WAIT_V(n) asm volatile("s_waitcnt vmcnt(" #n ")" ::: "memory")
; #define G_WAIT_L(n) asm volatile("s_waitcnt lgkmcnt(" #n ")" ::: "memory")
; #define G_BAR __builtin_amdgcn_s_barrier()
; #define G_SCHED __builtin_amdgcn_sched_barrier(0)
;     __device__ __forceinline__ unsigned row_off(const Unit& u, int r, LAS unsigned char* lds) const { return (unsigned)((const LAS int*)(lds + LDS_STAGE + u.q * 4096))[r] * (unsigned)rowbytes; }
;     ...
;             G_LDB(B0, 0, 0); G_LDB(B1, 0, 1); G_SCHED; G_LDA(At, 0, 0); G_STAGE(G_SA(1, 1), a11, vA1);
;             if constexpr (GATHER) { if (last) { int tz = tid; asm volatile("" : "+v"(tz));
; #pragma unroll
;                 for (int i = 0; i < 2; ++i) { int R, C; stage_rc(tz * 16 + i * 8192, R, C); gc0[i] = S.row_off(nxt, R, lds) + (unsigned)C * 2u; gc1[i] = S.row_off(nxt, 128 + R, lds) + (unsigned)C * 2u; } } }
;             G_WAIT_L(0); G_BAR; G_MMA(0, 0, At, B0); G_MMA(0, 1, At, B1); G_WAIT_V(8); G_BAR; G_SCHED;
;             G_LDA(At, 0, 1); G_STAGE(G_SB(0, 0), b02, voffB); G_STAGE(G_SB(0, 1), b12, voffB); G_STAGE(G_SA(0, 0), a02, vA0);
;             G_WAIT_L(0); G_BAR; G_MMA(1, 0, At, B0); G_MMA(1, 1, At, B1); G_WAIT_V(8); G_BAR; G_SCHED;
.LBB0_1626:
	s_add_i32 s31, s31, 2
	s_add_u32 s78, s26, s74
	s_addc_u32 s79, s27, s75
	s_add_u32 s80, s62, s74
	s_addc_u32 s81, s63, s75
	s_add_u32 s82, s80, 0x100
	s_addc_u32 s83, s81, 0
	s_add_u32 s80, s36, s74
	s_addc_u32 s81, s37, s75
	s_add_u32 vcc_lo, s87, s74
	s_waitcnt lgkmcnt(0)
	s_addc_u32 vcc_hi, s90, s75
	s_and_b64 s[76:77], s[76:77], exec
	s_cselect_b32 s79, s57, s79
	s_cselect_b32 s78, s56, s78
	s_cselect_b32 s81, s51, s81
	s_cselect_b32 s80, s50, s80
	s_cselect_b32 s77, s55, s83
	s_cselect_b32 s76, s54, s82
	s_cselect_b32 s83, s53, vcc_hi
	s_cselect_b32 s82, s52, vcc_lo
	s_waitcnt vmcnt(8)
	s_barrier
	s_setprio 1
	s_waitcnt lgkmcnt(0)
	v_mfma_i32_16x16x64_i8 v[156:159], v[88:91], v[184:187], v[156:159]
	v_mfma_i32_16x16x64_i8 v[148:151], v[96:99], v[184:187], v[148:151]
	v_mfma_i32_16x16x64_i8 v[140:143], v[88:91], v[176:179], v[140:143]
	v_mfma_i32_16x16x64_i8 v[132:135], v[96:99], v[176:179], v[132:135]
	v_mfma_i32_16x16x64_i8 v[124:127], v[88:91], v[168:171], v[124:127]
	v_mfma_i32_16x16x64_i8 v[116:119], v[96:99], v[168:171], v[116:119]
	v_mfma_i32_16x16x64_i8 v[108:111], v[88:91], v[160:163], v[108:111]
	v_mfma_i32_16x16x64_i8 v[84:87], v[96:99], v[160:163], v[84:87]
	v_mfma_i32_16x16x64_i8 v[156:159], v[92:95], v[188:191], v[156:159]
	v_mfma_i32_16x16x64_i8 v[148:151], v[100:103], v[188:191], v[148:151]
	v_mfma_i32_16x16x64_i8 v[140:143], v[92:95], v[180:183], v[140:143]
	v_mfma_i32_16x16x64_i8 v[132:135], v[100:103], v[180:183], v[132:135]
	v_mfma_i32_16x16x64_i8 v[124:127], v[92:95], v[172:175], v[124:127]
	v_mfma_i32_16x16x64_i8 v[116:119], v[100:103], v[172:175], v[116:119]
	v_mfma_i32_16x16x64_i8 v[108:111], v[92:95], v[164:167], v[108:111]
	v_mfma_i32_16x16x64_i8 v[84:87], v[100:103], v[164:167], v[84:87]
	v_mfma_i32_16x16x64_i8 v[152:155], v[64:67], v[184:187], v[152:155]
	v_mfma_i32_16x16x64_i8 v[144:147], v[72:75], v[184:187], v[144:147]
	v_mfma_i32_16x16x64_i8 v[136:139], v[64:67], v[176:179], v[136:139]
	v_mfma_i32_16x16x64_i8 v[128:131], v[72:75], v[176:179], v[128:131]
	v_mfma_i32_16x16x64_i8 v[120:123], v[64:67], v[168:171], v[120:123]
	v_mfma_i32_16x16x64_i8 v[112:115], v[72:75], v[168:171], v[112:115]
	v_mfma_i32_16x16x64_i8 v[104:107], v[64:67], v[160:163], v[104:107]
	v_mfma_i32_16x16x64_i8 v[80:83], v[72:75], v[160:163], v[80:83]
	v_mfma_i32_16x16x64_i8 v[152:155], v[68:71], v[188:191], v[152:155]
	v_mfma_i32_16x16x64_i8 v[144:147], v[76:79], v[188:191], v[144:147]
	v_mfma_i32_16x16x64_i8 v[136:139], v[68:71], v[180:183], v[136:139]
	v_mfma_i32_16x16x64_i8 v[128:131], v[76:79], v[180:183], v[128:131]
	v_mfma_i32_16x16x64_i8 v[120:123], v[68:71], v[172:175], v[120:123]
	v_mfma_i32_16x16x64_i8 v[112:115], v[76:79], v[172:175], v[112:115]
	v_mfma_i32_16x16x64_i8 v[104:107], v[68:71], v[164:167], v[104:107]
	v_mfma_i32_16x16x64_i8 v[80:83], v[76:79], v[164:167], v[80:83]
	s_setprio 0
	s_waitcnt vmcnt(8)
	s_barrier
	s_mov_b32 m0, s34
	ds_read_b128 v[160:163], v208 offset:16384
	ds_read_b128 v[164:167], v208 offset:17408
	ds_read_b128 v[168:171], v208 offset:18432
	ds_read_b128 v[172:175], v208 offset:19456
	ds_read_b128 v[176:179], v208 offset:20480
	ds_read_b128 v[180:183], v208 offset:21504
	ds_read_b128 v[184:187], v208 offset:22528
	ds_read_b128 v[188:191], v208 offset:23552
	global_load_lds_dwordx4 v244, s[80:81]
	s_mov_b32 m0, s35
	v_mov_b32_e32 v211, v193
	global_load_lds_dwordx4 v246, s[80:81]
	s_mov_b32 m0, s30
	v_mov_b32_e32 v213, v193
	global_load_lds_dwordx4 v244, s[82:83]
	s_mov_b32 m0, s0
	v_mov_b32_e32 v195, v193
	global_load_lds_dwordx4 v246, s[82:83]
	s_mov_b32 m0, s3
	v_mov_b32_e32 v197, v193
	global_load_lds_dwordx4 v194, s[78:79]
	s_mov_b32 m0, s40
	v_lshl_add_u64 v[214:215], s[80:81], 0, v[244:245]
	global_load_lds_dwordx4 v196, s[78:79]
	s_waitcnt lgkmcnt(0)
	v_lshl_add_u64 v[216:217], s[80:81], 0, v[246:247]
	v_lshl_add_u64 v[210:211], s[82:83], 0, v[244:245]
	v_lshl_add_u64 v[212:213], s[82:83], 0, v[246:247]
	v_lshl_add_u64 v[218:219], s[78:79], 0, v[194:195]
	v_lshl_add_u64 v[220:221], s[78:79], 0, v[196:197]
	s_waitcnt vmcnt(8)
	s_barrier
	s_setprio 1
	s_waitcnt lgkmcnt(0)
	v_mfma_i32_16x16x64_i8 v[60:63], v[88:91], v[160:163], v[60:63]
	v_mfma_i32_16x16x64_i8 v[52:55], v[96:99], v[160:163], v[52:55]
	v_mfma_i32_16x16x64_i8 v[44:47], v[88:91], v[168:171], v[44:47]
	v_mfma_i32_16x16x64_i8 v[36:39], v[96:99], v[168:171], v[36:39]
	v_mfma_i32_16x16x64_i8 v[28:31], v[88:91], v[176:179], v[28:31]
	v_mfma_i32_16x16x64_i8 v[20:23], v[96:99], v[176:179], v[20:23]
	v_mfma_i32_16x16x64_i8 v[12:15], v[88:91], v[184:187], v[12:15]
	v_mfma_i32_16x16x64_i8 v[4:7], v[96:99], v[184:187], v[4:7]
	v_mfma_i32_16x16x64_i8 v[60:63], v[92:95], v[164:167], v[60:63]
	v_mfma_i32_16x16x64_i8 v[52:55], v[100:103], v[164:167], v[52:55]
	v_mfma_i32_16x16x64_i8 v[44:47], v[92:95], v[172:175], v[44:47]
	v_mfma_i32_16x16x64_i8 v[36:39], v[100:103], v[172:175], v[36:39]
	v_mfma_i32_16x16x64_i8 v[28:31], v[92:95], v[180:183], v[28:31]
	v_mfma_i32_16x16x64_i8 v[20:23], v[100:103], v[180:183], v[20:23]
	v_mfma_i32_16x16x64_i8 v[12:15], v[92:95], v[188:191], v[12:15]
	v_mfma_i32_16x16x64_i8 v[4:7], v[100:103], v[188:191], v[4:7]
	v_mfma_i32_16x16x64_i8 v[56:59], v[64:67], v[160:163], v[56:59]
	v_mfma_i32_16x16x64_i8 v[48:51], v[72:75], v[160:163], v[48:51]
	v_mfma_i32_16x16x64_i8 v[40:43], v[64:67], v[168:171], v[40:43]
	v_mfma_i32_16x16x64_i8 v[32:35], v[72:75], v[168:171], v[32:35]
	v_mfma_i32_16x16x64_i8 v[24:27], v[64:67], v[176:179], v[24:27]
	v_mfma_i32_16x16x64_i8 v[16:19], v[72:75], v[176:179], v[16:19]
	v_mfma_i32_16x16x64_i8 v[8:11], v[64:67], v[184:187], v[8:11]
	v_mfma_i32_16x16x64_i8 v[0:3], v[72:75], v[184:187], v[0:3]
	v_mfma_i32_16x16x64_i8 v[56:59], v[68:71], v[164:167], v[56:59]
	v_mfma_i32_16x16x64_i8 v[48:51], v[76:79], v[164:167], v[48:51]
	v_mfma_i32_16x16x64_i8 v[40:43], v[68:71], v[172:175], v[40:43]
	v_mfma_i32_16x16x64_i8 v[32:35], v[76:79], v[172:175], v[32:35]
	v_mfma_i32_16x16x64_i8 v[24:27], v[68:71], v[180:183], v[24:27]
	v_mfma_i32_16x16x64_i8 v[16:19], v[76:79], v[180:183], v[16:19]
	v_mfma_i32_16x16x64_i8 v[8:11], v[68:71], v[188:191], v[8:11]
	v_mfma_i32_16x16x64_i8 v[0:3], v[76:79], v[188:191], v[0:3]
	s_setprio 0
	s_waitcnt vmcnt(8)
	s_barrier
; #define G_STAGE(bufoff, gbase, voff) do { _Pragma("unroll") for (int _i = 0; _i < 2; ++_i) \
;         __builtin_amdgcn_global_load_lds((const unsigned*)((const char*)(gbase) + (voff)[_i]), (LAS unsigned*)(lds + (bufoff) + ldsw + _i * 8192), 16, 0, 0); } while (0)
; #define G_LDA(dst, b, h) do { _Pragma("unroll") for (int m = 0; m < 4; ++m) G_LD8(dst[m], lds + G_SA(b, h) + aoff + m * 2048); } while (0)
; #define G_LDB(dst, b, h) do { _Pragma("unroll") for (int n = 0; n < 2; ++n) G_LD8(dst[n], lds + G_SB(b, h) + boff + n * 2048); } while (0)
; #define G_WAIT_V(n) asm volatile("s_waitcnt vmcnt(" #n ")" ::: "memory")
; #define G_WAIT_L(n) asm volatile("s_waitcnt lgkmcnt(" #n ")" ::: "memory")
; #define G_BAR __builtin_amdgcn_s_barrier()
; #define G_SCHED __builtin_amdgcn_sched_barrier(0)
;     ...
;             G_WAIT_L(0); G_BAR; G_MMA(1, 0, At, B0); G_MMA(1, 1, At, B1); G_WAIT_V(8); G_BAR; G_SCHED;
;             G_LDB(B0, 1, 0); G_LDB(B1, 1, 1); G_SCHED; G_LDA(At, 1, 0); G_STAGE(G_SA(0, 1), a12, vA1);
;             G_WAIT_L(0); G_BAR; G_MMA(0, 0, At, B0); G_MMA(0, 1, At, B1); G_WAIT_V(8); G_BAR; G_SCHED;
;             G_LDA(At, 1, 1); G_STAGE(G_SB(1, 0), b02 + kstep, voffB); G_STAGE(G_SB(1, 1), b12 + kstep, voffB); G_STAGE(G_SA(1, 0), a02 + kstep, vA0);
;             G_WAIT_L(0); G_BAR; G_MMA(1, 0, At, B0); G_MMA(1, 1, At, B1); G_WAIT_V(8); G_BAR; G_SCHED;
;         }
	s_add_i32 s78, 0, 0x18000
	s_add_i32 s79, 0, 0x1c000
	v_add_u32_e32 v76, s78, v203
	v_add_u32_e32 v100, s79, v203
	ds_read_b128 v[64:67], v76
	ds_read_b128 v[68:71], v76 offset:1024
	ds_read_b128 v[72:75], v76 offset:2048
	ds_read_b128 v[76:79], v76 offset:3072
	ds_read_b128 v[88:91], v100
	ds_read_b128 v[92:95], v100 offset:1024
	ds_read_b128 v[96:99], v100 offset:2048
	ds_read_b128 v[100:103], v100 offset:3072
	s_mov_b32 m0, s41
	v_lshl_add_u64 v[222:223], s[76:77], 0, v[192:193]
	ds_read_b128 v[160:163], v208 offset:32768
	ds_read_b128 v[164:167], v208 offset:33792
	ds_read_b128 v[168:171], v208 offset:34816
	ds_read_b128 v[172:175], v208 offset:35840
	ds_read_b128 v[176:179], v208 offset:36864
	ds_read_b128 v[180:183], v208 offset:37888
	ds_read_b128 v[184:187], v208 offset:38912
	ds_read_b128 v[188:191], v208 offset:39936
	global_load_lds_dwordx4 v[222:223], off
	v_lshl_add_u64 v[222:223], s[76:77], 0, v[198:199]
	s_mov_b32 m0, s18
	s_nop 0
	global_load_lds_dwordx4 v[222:223], off
	s_waitcnt lgkmcnt(0)
	s_waitcnt vmcnt(8)
	s_barrier
	s_setprio 1
	s_waitcnt lgkmcnt(0)
	v_mfma_i32_16x16x64_i8 v[156:159], v[64:67], v[160:163], v[156:159]
	v_mfma_i32_16x16x64_i8 v[148:151], v[72:75], v[160:163], v[148:151]
	v_mfma_i32_16x16x64_i8 v[140:143], v[64:67], v[168:171], v[140:143]
	v_mfma_i32_16x16x64_i8 v[132:135], v[72:75], v[168:171], v[132:135]
	v_mfma_i32_16x16x64_i8 v[124:127], v[64:67], v[176:179], v[124:127]
	v_mfma_i32_16x16x64_i8 v[116:119], v[72:75], v[176:179], v[116:119]
	v_mfma_i32_16x16x64_i8 v[108:111], v[64:67], v[184:187], v[108:111]
	v_mfma_i32_16x16x64_i8 v[84:87], v[72:75], v[184:187], v[84:87]
	v_mfma_i32_16x16x64_i8 v[156:159], v[68:71], v[164:167], v[156:159]
	v_mfma_i32_16x16x64_i8 v[148:151], v[76:79], v[164:167], v[148:151]
	v_mfma_i32_16x16x64_i8 v[140:143], v[68:71], v[172:175], v[140:143]
	v_mfma_i32_16x16x64_i8 v[132:135], v[76:79], v[172:175], v[132:135]
	v_mfma_i32_16x16x64_i8 v[124:127], v[68:71], v[180:183], v[124:127]
	v_mfma_i32_16x16x64_i8 v[116:119], v[76:79], v[180:183], v[116:119]
	v_mfma_i32_16x16x64_i8 v[108:111], v[68:71], v[188:191], v[108:111]
	v_mfma_i32_16x16x64_i8 v[84:87], v[76:79], v[188:191], v[84:87]
	v_mfma_i32_16x16x64_i8 v[152:155], v[88:91], v[160:163], v[152:155]
	v_mfma_i32_16x16x64_i8 v[144:147], v[96:99], v[160:163], v[144:147]
	v_mfma_i32_16x16x64_i8 v[136:139], v[88:91], v[168:171], v[136:139]
	v_mfma_i32_16x16x64_i8 v[128:131], v[96:99], v[168:171], v[128:131]
	v_mfma_i32_16x16x64_i8 v[120:123], v[88:91], v[176:179], v[120:123]
	v_mfma_i32_16x16x64_i8 v[112:115], v[96:99], v[176:179], v[112:115]
	v_mfma_i32_16x16x64_i8 v[104:107], v[88:91], v[184:187], v[104:107]
	v_mfma_i32_16x16x64_i8 v[80:83], v[96:99], v[184:187], v[80:83]
	v_mfma_i32_16x16x64_i8 v[152:155], v[92:95], v[164:167], v[152:155]
	v_mfma_i32_16x16x64_i8 v[144:147], v[100:103], v[164:167], v[144:147]
	v_mfma_i32_16x16x64_i8 v[136:139], v[92:95], v[172:175], v[136:139]
	v_mfma_i32_16x16x64_i8 v[128:131], v[100:103], v[172:175], v[128:131]
	v_mfma_i32_16x16x64_i8 v[120:123], v[92:95], v[180:183], v[120:123]
	v_mfma_i32_16x16x64_i8 v[112:115], v[100:103], v[180:183], v[112:115]
	v_mfma_i32_16x16x64_i8 v[104:107], v[92:95], v[188:191], v[104:107]
	v_mfma_i32_16x16x64_i8 v[80:83], v[100:103], v[188:191], v[80:83]
	s_setprio 0
	s_waitcnt vmcnt(8)
	s_barrier
	s_add_i32 s76, s78, s93
	v_lshl_add_u64 v[214:215], v[214:215], 0, s[44:45]
	s_mov_b32 m0, s76
	ds_read_b128 v[160:163], v208 offset:49152
	ds_read_b128 v[164:167], v208 offset:50176
	ds_read_b128 v[168:171], v208 offset:51200
	ds_read_b128 v[172:175], v208 offset:52224
	ds_read_b128 v[176:179], v208 offset:53248
	ds_read_b128 v[180:183], v208 offset:54272
	ds_read_b128 v[184:187], v208 offset:55296
	ds_read_b128 v[188:191], v208 offset:56320
	global_load_lds_dwordx4 v[214:215], off
	v_lshl_add_u64 v[214:215], v[216:217], 0, s[44:45]
	s_add_i32 m0, s76, 0x2000
	s_add_i32 s76, s79, s93
	global_load_lds_dwordx4 v[214:215], off
	v_lshl_add_u64 v[210:211], v[210:211], 0, s[44:45]
	s_mov_b32 m0, s76
	s_nop 0
	global_load_lds_dwordx4 v[210:211], off
	v_lshl_add_u64 v[210:211], v[212:213], 0, s[44:45]
	s_add_i32 m0, s76, 0x2000
	s_nop 0
	global_load_lds_dwordx4 v[210:211], off
	v_lshl_add_u64 v[210:211], v[218:219], 0, s[44:45]
	s_mov_b32 m0, s19
	s_nop 0
	global_load_lds_dwordx4 v[210:211], off
	v_lshl_add_u64 v[210:211], v[220:221], 0, s[44:45]
	s_mov_b32 m0, s89
	s_nop 0
	global_load_lds_dwordx4 v[210:211], off
	s_waitcnt lgkmcnt(0)
	s_waitcnt vmcnt(8)
	s_barrier
	s_setprio 1
	s_waitcnt lgkmcnt(0)
	v_mfma_i32_16x16x64_i8 v[60:63], v[64:67], v[160:163], v[60:63]
	v_mfma_i32_16x16x64_i8 v[52:55], v[72:75], v[160:163], v[52:55]
	v_mfma_i32_16x16x64_i8 v[44:47], v[64:67], v[168:171], v[44:47]
	v_mfma_i32_16x16x64_i8 v[36:39], v[72:75], v[168:171], v[36:39]
	v_mfma_i32_16x16x64_i8 v[28:31], v[64:67], v[176:179], v[28:31]
	v_mfma_i32_16x16x64_i8 v[20:23], v[72:75], v[176:179], v[20:23]
	v_mfma_i32_16x16x64_i8 v[12:15], v[64:67], v[184:187], v[12:15]
	v_mfma_i32_16x16x64_i8 v[4:7], v[72:75], v[184:187], v[4:7]
	v_mfma_i32_16x16x64_i8 v[60:63], v[68:71], v[164:167], v[60:63]
	v_mfma_i32_16x16x64_i8 v[52:55], v[76:79], v[164:167], v[52:55]
	v_mfma_i32_16x16x64_i8 v[44:47], v[68:71], v[172:175], v[44:47]
	v_mfma_i32_16x16x64_i8 v[36:39], v[76:79], v[172:175], v[36:39]
	v_mfma_i32_16x16x64_i8 v[28:31], v[68:71], v[180:183], v[28:31]
	v_mfma_i32_16x16x64_i8 v[20:23], v[76:79], v[180:183], v[20:23]
	v_mfma_i32_16x16x64_i8 v[12:15], v[68:71], v[188:191], v[12:15]
	v_mfma_i32_16x16x64_i8 v[4:7], v[76:79], v[188:191], v[4:7]
	v_mfma_i32_16x16x64_i8 v[56:59], v[88:91], v[160:163], v[56:59]
	v_mfma_i32_16x16x64_i8 v[48:51], v[96:99], v[160:163], v[48:51]
	v_mfma_i32_16x16x64_i8 v[40:43], v[88:91], v[168:171], v[40:43]
	v_mfma_i32_16x16x64_i8 v[32:35], v[96:99], v[168:171], v[32:35]
	v_mfma_i32_16x16x64_i8 v[24:27], v[88:91], v[176:179], v[24:27]
	v_mfma_i32_16x16x64_i8 v[16:19], v[96:99], v[176:179], v[16:19]
	v_mfma_i32_16x16x64_i8 v[8:11], v[88:91], v[184:187], v[8:11]
	v_mfma_i32_16x16x64_i8 v[0:3], v[96:99], v[184:187], v[0:3]
	v_mfma_i32_16x16x64_i8 v[56:59], v[92:95], v[164:167], v[56:59]
	v_mfma_i32_16x16x64_i8 v[48:51], v[100:103], v[164:167], v[48:51]
	v_mfma_i32_16x16x64_i8 v[40:43], v[92:95], v[172:175], v[40:43]
	v_mfma_i32_16x16x64_i8 v[32:35], v[100:103], v[172:175], v[32:35]
	v_mfma_i32_16x16x64_i8 v[24:27], v[92:95], v[180:183], v[24:27]
	v_mfma_i32_16x16x64_i8 v[16:19], v[100:103], v[180:183], v[16:19]
	v_mfma_i32_16x16x64_i8 v[8:11], v[92:95], v[188:191], v[8:11]
	v_mfma_i32_16x16x64_i8 v[0:3], v[100:103], v[188:191], v[0:3]
	s_setprio 0
	s_waitcnt vmcnt(8)
	s_barrier
	s_add_u32 s74, s74, 0x100
	s_addc_u32 s75, s75, 0
	s_cmp_ge_i32 s31, s33
	s_cbranch_scc1 .LBB0_1639

; #define G_STAGE(bufoff, gbase, voff) do { _Pragma("unroll") for (int _i = 0; _i < 2; ++_i) \
;         __builtin_amdgcn_global_load_lds((const unsigned*)((const char*)(gbase) + (voff)[_i]), (LAS unsigned*)(lds + (bufoff) + ldsw + _i * 8192), 16, 0, 0); } while (0)
; #define G_LDA(dst, b, h) do { _Pragma("unroll") for (int m = 0; m < 4; ++m) G_LD8(dst[m], lds + G_SA(b, h) + aoff + m * 2048); } while (0)
; #define G_LDB(dst, b, h) do { _Pragma("unroll") for (int n = 0; n < 2; ++n) G_LD8(dst[n], lds + G_SB(b, h) + boff + n * 2048); } while (0)
; #define G_WAIT_V(n) asm volatile("s_waitcnt vmcnt(" #n ")" ::: "memory")
; #define G_WAIT_L(n) asm volatile("s_waitcnt lgkmcnt(" #n ")" ::: "memory")
; #define G_BAR __builtin_amdgcn_s_barrier()
; #define G_SCHED __builtin_amdgcn_sched_barrier(0)
;     __device__ __forceinline__ unsigned row_off(const Unit& u, int r, LAS unsigned char* lds) const { return (unsigned)((const LAS int*)(lds + LDS_STAGE + u.q * 4096))[r] * (unsigned)rowbytes; }
;     ...
;             G_LDB(B0, 0, 0); G_LDB(B1, 0, 1); G_SCHED; G_LDA(At, 0, 0); G_STAGE(G_SA(1, 1), a11, vA1);
;             if constexpr (GATHER) { if (last) { int tz = tid; asm volatile("" : "+v"(tz));
; #pragma unroll
;                 for (int i = 0; i < 2; ++i) { int R, C; stage_rc(tz * 16 + i * 8192, R, C); gc0[i] = S.row_off(nxt, R, lds) + (unsigned)C * 2u; gc1[i] = S.row_off(nxt, 128 + R, lds) + (unsigned)C * 2u; } } }
;             G_WAIT_L(0); G_BAR; G_MMA(0, 0, At, B0); G_MMA(0, 1, At, B1); G_WAIT_V(8); G_BAR; G_SCHED;
;             G_LDA(At, 0, 1); G_STAGE(G_SB(0, 0), b02, voffB); G_STAGE(G_SB(0, 1), b12, voffB); G_STAGE(G_SA(0, 0), a02, vA0);
;             G_WAIT_L(0); G_BAR; G_MMA(1, 0, At, B0); G_MMA(1, 1, At, B1); G_WAIT_V(8); G_BAR; G_SCHED;
.LBB0_1733:
	s_add_i32 s81, s80, 2
	s_add_u32 s52, s78, s48
	s_addc_u32 s53, s79, s49
	s_add_u32 s58, s44, s48
	s_addc_u32 s59, s45, s49
	s_add_u32 s86, s58, 0x100
	v_add_u32_e32 v154, s66, v137
	v_add_u32_e32 v170, s67, v137
	s_addc_u32 s87, s59, 0
	ds_read_b128 v[142:145], v154
	ds_read_b128 v[146:149], v154 offset:1024
	ds_read_b128 v[150:153], v154 offset:2048
	ds_read_b128 v[154:157], v154 offset:3072
	ds_read_b128 v[158:161], v170
	ds_read_b128 v[162:165], v170 offset:1024
	ds_read_b128 v[166:169], v170 offset:2048
	ds_read_b128 v[170:173], v170 offset:3072
	s_add_u32 s56, s29, s48
	s_addc_u32 s57, s75, s49
	s_add_u32 s82, s76, s48
	s_addc_u32 s83, s77, s49
	s_add_i32 s90, s66, s22
	s_add_i32 m0, s23, 0xc000
	s_add_i32 s89, s23, 0xe000
	s_add_i32 s84, s90, 0x2000
	s_cmp_eq_u32 s65, s80
	s_cselect_b32 s55, s37, s53
	s_cselect_b32 s54, s36, s52
	s_cselect_b32 s57, s31, s57
	s_cselect_b32 s56, s30, s56
	s_cselect_b32 s53, s39, s87
	s_cselect_b32 s52, s38, s86
	v_lshl_add_u64 v[206:207], s[58:59], 0, v[128:129]
	v_lshl_add_u64 v[206:207], v[206:207], 0, s[10:11]
	ds_read_b128 v[174:177], v138
	ds_read_b128 v[178:181], v138 offset:1024
	ds_read_b128 v[182:185], v138 offset:2048
	ds_read_b128 v[186:189], v138 offset:3072
	ds_read_b128 v[190:193], v138 offset:4096
	ds_read_b128 v[194:197], v138 offset:5120
	ds_read_b128 v[198:201], v138 offset:6144
	ds_read_b128 v[202:205], v138 offset:7168
	global_load_lds_dwordx4 v[206:207], off
	v_lshl_add_u64 v[206:207], s[58:59], 0, v[130:131]
	v_lshl_add_u64 v[206:207], v[206:207], 0, s[10:11]
	s_mov_b32 m0, s89
	v_mov_b32_e32 v131, v129
	global_load_lds_dwordx4 v[206:207], off
	s_waitcnt lgkmcnt(0)
	s_waitcnt vmcnt(8)
	s_barrier
	s_setprio 1
	s_waitcnt lgkmcnt(0)
	v_mfma_scale_f32_16x16x128_f8f6f4 v[124:127], v[142:149], v[174:181], v[124:127], v139, v139 op_sel_hi:[0,0,0]
	v_mfma_scale_f32_16x16x128_f8f6f4 v[120:123], v[150:157], v[174:181], v[120:123], v139, v139 op_sel_hi:[0,0,0]
	v_mfma_scale_f32_16x16x128_f8f6f4 v[116:119], v[142:149], v[182:189], v[116:119], v139, v139 op_sel_hi:[0,0,0]
	v_mfma_scale_f32_16x16x128_f8f6f4 v[112:115], v[150:157], v[182:189], v[112:115], v139, v139 op_sel_hi:[0,0,0]
	v_mfma_scale_f32_16x16x128_f8f6f4 v[108:111], v[142:149], v[190:197], v[108:111], v139, v139 op_sel_hi:[0,0,0]
	v_mfma_scale_f32_16x16x128_f8f6f4 v[104:107], v[150:157], v[190:197], v[104:107], v139, v139 op_sel_hi:[0,0,0]
	v_mfma_scale_f32_16x16x128_f8f6f4 v[100:103], v[142:149], v[198:205], v[100:103], v139, v139 op_sel_hi:[0,0,0]
	v_mfma_scale_f32_16x16x128_f8f6f4 v[96:99], v[150:157], v[198:205], v[96:99], v139, v139 op_sel_hi:[0,0,0]
	v_mfma_scale_f32_16x16x128_f8f6f4 v[206:209], v[158:165], v[174:181], v[60:63], v139, v139 op_sel_hi:[0,0,0]
	v_mfma_scale_f32_16x16x128_f8f6f4 v[174:177], v[166:173], v[174:181], v[56:59], v139, v139 op_sel_hi:[0,0,0]
	v_mfma_scale_f32_16x16x128_f8f6f4 v[178:181], v[158:165], v[182:189], v[52:55], v139, v139 op_sel_hi:[0,0,0]
	v_mfma_scale_f32_16x16x128_f8f6f4 v[182:185], v[166:173], v[182:189], v[48:51], v139, v139 op_sel_hi:[0,0,0]
	v_mfma_scale_f32_16x16x128_f8f6f4 v[186:189], v[158:165], v[190:197], v[44:47], v139, v139 op_sel_hi:[0,0,0]
	v_mfma_scale_f32_16x16x128_f8f6f4 v[190:193], v[166:173], v[190:197], v[40:43], v139, v139 op_sel_hi:[0,0,0]
	v_mfma_scale_f32_16x16x128_f8f6f4 v[194:197], v[158:165], v[198:205], v[36:39], v139, v139 op_sel_hi:[0,0,0]
	v_mfma_scale_f32_16x16x128_f8f6f4 v[198:201], v[166:173], v[198:205], v[32:35], v139, v139 op_sel_hi:[0,0,0]
	s_setprio 0
	s_waitcnt vmcnt(8)
	s_barrier
	s_mov_b32 m0, s90
	s_nop 3
	ds_read_b128 v[32:35], v138 offset:16384
	ds_read_b128 v[36:39], v138 offset:17408
	ds_read_b128 v[40:43], v138 offset:18432
	ds_read_b128 v[44:47], v138 offset:19456
	ds_read_b128 v[48:51], v138 offset:20480
	ds_read_b128 v[52:55], v138 offset:21504
	ds_read_b128 v[56:59], v138 offset:22528
	ds_read_b128 v[60:63], v138 offset:23552
	global_load_lds_dwordx4 v132, s[56:57]
	s_mov_b32 m0, s84
	s_cselect_b32 s59, s35, s83
	s_cselect_b32 s58, s34, s82
	s_add_i32 s80, s67, s22
	s_add_u32 s98, s56, 0x20000
	s_addc_u32 s99, s57, 0
	global_load_lds_dwordx4 v132, s[98:99]
	s_mov_b32 m0, s80
	v_mov_b32_e32 v133, v129
	global_load_lds_dwordx4 v132, s[58:59]
	s_add_i32 m0, s80, 0x2000
	s_add_u32 s100, s58, 0x20000
	s_addc_u32 s101, s59, 0
	global_load_lds_dwordx4 v132, s[100:101]
	s_mov_b32 m0, s23
	v_lshl_add_u64 v[246:247], s[56:57], 0, v[132:133]
	global_load_lds_dwordx4 v128, s[54:55]
	s_mov_b32 m0, s24
	v_lshl_add_u64 v[248:249], s[98:99], 0, v[132:133]
	global_load_lds_dwordx4 v130, s[54:55]
	s_waitcnt lgkmcnt(0)
	v_lshl_add_u64 v[250:251], s[100:101], 0, v[132:133]
	v_lshl_add_u64 v[252:253], s[54:55], 0, v[128:129]
	v_lshl_add_u64 v[134:135], s[54:55], 0, v[130:131]
	s_waitcnt vmcnt(8)
	s_barrier
; #define G_STAGE(bufoff, gbase, voff) do { _Pragma("unroll") for (int _i = 0; _i < 2; ++_i) \
;         __builtin_amdgcn_global_load_lds((const unsigned*)((const char*)(gbase) + (voff)[_i]), (LAS unsigned*)(lds + (bufoff) + ldsw + _i * 8192), 16, 0, 0); } while (0)
; #define G_LDA(dst, b, h) do { _Pragma("unroll") for (int m = 0; m < 4; ++m) G_LD8(dst[m], lds + G_SA(b, h) + aoff + m * 2048); } while (0)
; #define G_LDB(dst, b, h) do { _Pragma("unroll") for (int n = 0; n < 2; ++n) G_LD8(dst[n], lds + G_SB(b, h) + boff + n * 2048); } while (0)
; #define G_WAIT_V(n) asm volatile("s_waitcnt vmcnt(" #n ")" ::: "memory")
; #define G_WAIT_L(n) asm volatile("s_waitcnt lgkmcnt(" #n ")" ::: "memory")
; #define G_BAR __builtin_amdgcn_s_barrier()
; #define G_SCHED __builtin_amdgcn_sched_barrier(0)
;     ...
;             G_WAIT_L(0); G_BAR; G_MMA(1, 0, At, B0); G_MMA(1, 1, At, B1); G_WAIT_V(8); G_BAR; G_SCHED;
;             G_LDB(B0, 1, 0); G_LDB(B1, 1, 1); G_SCHED; G_LDA(At, 1, 0); G_STAGE(G_SA(0, 1), a12, vA1);
;             G_WAIT_L(0); G_BAR; G_MMA(0, 0, At, B0); G_MMA(0, 1, At, B1); G_WAIT_V(8); G_BAR; G_SCHED;
	s_setprio 1
	s_waitcnt lgkmcnt(0)
	v_mfma_scale_f32_16x16x128_f8f6f4 v[92:95], v[142:149], v[32:39], v[92:95], v139, v139 op_sel_hi:[0,0,0]
	v_mfma_scale_f32_16x16x128_f8f6f4 v[88:91], v[150:157], v[32:39], v[88:91], v139, v139 op_sel_hi:[0,0,0]
	v_mfma_scale_f32_16x16x128_f8f6f4 v[84:87], v[142:149], v[40:47], v[84:87], v139, v139 op_sel_hi:[0,0,0]
	v_mfma_scale_f32_16x16x128_f8f6f4 v[80:83], v[150:157], v[40:47], v[80:83], v139, v139 op_sel_hi:[0,0,0]
	v_mfma_scale_f32_16x16x128_f8f6f4 v[76:79], v[142:149], v[48:55], v[76:79], v139, v139 op_sel_hi:[0,0,0]
	v_mfma_scale_f32_16x16x128_f8f6f4 v[72:75], v[150:157], v[48:55], v[72:75], v139, v139 op_sel_hi:[0,0,0]
	v_mfma_scale_f32_16x16x128_f8f6f4 v[202:205], v[142:149], v[56:63], v[68:71], v139, v139 op_sel_hi:[0,0,0]
	v_mfma_scale_f32_16x16x128_f8f6f4 v[210:213], v[150:157], v[56:63], v[64:67], v139, v139 op_sel_hi:[0,0,0]
	v_mfma_scale_f32_16x16x128_f8f6f4 v[214:217], v[158:165], v[32:39], v[28:31], v139, v139 op_sel_hi:[0,0,0]
	v_mfma_scale_f32_16x16x128_f8f6f4 v[218:221], v[166:173], v[32:39], v[24:27], v139, v139 op_sel_hi:[0,0,0]
	v_mfma_scale_f32_16x16x128_f8f6f4 v[222:225], v[158:165], v[40:47], v[20:23], v139, v139 op_sel_hi:[0,0,0]
	v_mfma_scale_f32_16x16x128_f8f6f4 v[226:229], v[166:173], v[40:47], v[16:19], v139, v139 op_sel_hi:[0,0,0]
	v_mfma_scale_f32_16x16x128_f8f6f4 v[230:233], v[158:165], v[48:55], v[12:15], v139, v139 op_sel_hi:[0,0,0]
	v_mfma_scale_f32_16x16x128_f8f6f4 v[234:237], v[166:173], v[48:55], v[8:11], v139, v139 op_sel_hi:[0,0,0]
	v_mfma_scale_f32_16x16x128_f8f6f4 v[238:241], v[158:165], v[56:63], v[4:7], v139, v139 op_sel_hi:[0,0,0]
	v_mfma_scale_f32_16x16x128_f8f6f4 v[242:245], v[166:173], v[56:63], v[0:3], v139, v139 op_sel_hi:[0,0,0]
	s_setprio 0
	s_waitcnt vmcnt(8)
	s_barrier
	s_add_i32 s54, 0, 0x18000
	s_add_i32 s55, 0, 0x1c000
	v_add_u32_e32 v12, s54, v137
	v_add_u32_e32 v16, s55, v137
	s_nop 0
	ds_read_b128 v[0:3], v12
	ds_read_b128 v[4:7], v12 offset:1024
	ds_read_b128 v[8:11], v12 offset:2048
	ds_read_b128 v[12:15], v12 offset:3072
	ds_read_b128 v[142:145], v16
	ds_read_b128 v[146:149], v16 offset:1024
	ds_read_b128 v[150:153], v16 offset:2048
	ds_read_b128 v[154:157], v16 offset:3072
	s_mov_b32 m0, s25
	ds_read_b128 v[16:19], v138 offset:32768
	ds_read_b128 v[20:23], v138 offset:33792
	ds_read_b128 v[24:27], v138 offset:34816
	ds_read_b128 v[28:31], v138 offset:35840
	ds_read_b128 v[32:35], v138 offset:36864
	ds_read_b128 v[36:39], v138 offset:37888
	ds_read_b128 v[64:67], v138 offset:38912
	ds_read_b128 v[68:71], v138 offset:39936
	global_load_lds_dwordx4 v128, s[52:53]
	s_mov_b32 m0, s26
	s_nop 0
	global_load_lds_dwordx4 v130, s[52:53]
	s_waitcnt lgkmcnt(0)
	s_waitcnt vmcnt(8)
	s_barrier
	s_setprio 1
	s_waitcnt lgkmcnt(0)
	v_mfma_scale_f32_16x16x128_f8f6f4 v[124:127], v[0:7], v[16:23], v[124:127], v139, v139 op_sel_hi:[0,0,0]
	v_mfma_scale_f32_16x16x128_f8f6f4 v[120:123], v[8:15], v[16:23], v[120:123], v139, v139 op_sel_hi:[0,0,0]
	v_mfma_scale_f32_16x16x128_f8f6f4 v[116:119], v[0:7], v[24:31], v[116:119], v139, v139 op_sel_hi:[0,0,0]
	v_mfma_scale_f32_16x16x128_f8f6f4 v[112:115], v[8:15], v[24:31], v[112:115], v139, v139 op_sel_hi:[0,0,0]
	v_mfma_scale_f32_16x16x128_f8f6f4 v[108:111], v[0:7], v[32:39], v[108:111], v139, v139 op_sel_hi:[0,0,0]
	v_mfma_scale_f32_16x16x128_f8f6f4 v[104:107], v[8:15], v[32:39], v[104:107], v139, v139 op_sel_hi:[0,0,0]
	v_mfma_scale_f32_16x16x128_f8f6f4 v[100:103], v[0:7], v[64:71], v[100:103], v139, v139 op_sel_hi:[0,0,0]
	v_mfma_scale_f32_16x16x128_f8f6f4 v[96:99], v[8:15], v[64:71], v[96:99], v139, v139 op_sel_hi:[0,0,0]
	v_mfma_scale_f32_16x16x128_f8f6f4 v[60:63], v[142:149], v[16:23], v[206:209], v139, v139 op_sel_hi:[0,0,0]
	v_mfma_scale_f32_16x16x128_f8f6f4 v[56:59], v[150:157], v[16:23], v[174:177], v139, v139 op_sel_hi:[0,0,0]
	v_mfma_scale_f32_16x16x128_f8f6f4 v[52:55], v[142:149], v[24:31], v[178:181], v139, v139 op_sel_hi:[0,0,0]
	v_mfma_scale_f32_16x16x128_f8f6f4 v[48:51], v[150:157], v[24:31], v[182:185], v139, v139 op_sel_hi:[0,0,0]
	v_mfma_scale_f32_16x16x128_f8f6f4 v[44:47], v[142:149], v[32:39], v[186:189], v139, v139 op_sel_hi:[0,0,0]
	v_mfma_scale_f32_16x16x128_f8f6f4 v[40:43], v[150:157], v[32:39], v[190:193], v139, v139 op_sel_hi:[0,0,0]
	v_mfma_scale_f32_16x16x128_f8f6f4 v[36:39], v[142:149], v[64:71], v[194:197], v139, v139 op_sel_hi:[0,0,0]
	v_mfma_scale_f32_16x16x128_f8f6f4 v[32:35], v[150:157], v[64:71], v[198:201], v139, v139 op_sel_hi:[0,0,0]
	s_setprio 0
	s_waitcnt vmcnt(8)
	s_barrier
; #define G_STAGE(bufoff, gbase, voff) do { _Pragma("unroll") for (int _i = 0; _i < 2; ++_i) \
;         __builtin_amdgcn_global_load_lds((const unsigned*)((const char*)(gbase) + (voff)[_i]), (LAS unsigned*)(lds + (bufoff) + ldsw + _i * 8192), 16, 0, 0); } while (0)
; #define G_LDA(dst, b, h) do { _Pragma("unroll") for (int m = 0; m < 4; ++m) G_LD8(dst[m], lds + G_SA(b, h) + aoff + m * 2048); } while (0)
; #define G_WAIT_V(n) asm volatile("s_waitcnt vmcnt(" #n ")" ::: "memory")
; #define G_WAIT_L(n) asm volatile("s_waitcnt lgkmcnt(" #n ")" ::: "memory")
; #define G_BAR __builtin_amdgcn_s_barrier()
; #define G_SCHED __builtin_amdgcn_sched_barrier(0)
;     ...
;             G_LDA(At, 1, 1); G_STAGE(G_SB(1, 0), b02 + kstep, voffB); G_STAGE(G_SB(1, 1), b12 + kstep, voffB); G_STAGE(G_SA(1, 0), a02 + kstep, vA0);
;             G_WAIT_L(0); G_BAR; G_MMA(1, 0, At, B0); G_MMA(1, 1, At, B1); G_WAIT_V(8); G_BAR; G_SCHED;
;         }
;         if (wr == 0) G_BAR;
	s_add_i32 s52, s54, s22
	v_lshl_add_u64 v[24:25], v[246:247], 0, s[10:11]
	s_mov_b32 m0, s52
	ds_read_b128 v[16:19], v138 offset:49152
	ds_read_b128 v[20:23], v138 offset:50176
	ds_read_b128 v[158:161], v138 offset:51200
	ds_read_b128 v[162:165], v138 offset:52224
	ds_read_b128 v[166:169], v138 offset:53248
	ds_read_b128 v[170:173], v138 offset:54272
	ds_read_b128 v[174:177], v138 offset:55296
	ds_read_b128 v[178:181], v138 offset:56320
	global_load_lds_dwordx4 v[24:25], off
	v_lshl_add_u64 v[24:25], v[248:249], 0, s[10:11]
	s_add_i32 m0, s52, 0x2000
	s_add_i32 s52, s55, s22
	s_sub_u32 s98, s10, 0x20000
	s_subb_u32 s99, s11, 0
	global_load_lds_dwordx4 v[24:25], off
	v_lshl_add_u64 v[24:25], v[250:251], 0, s[98:99]
	s_mov_b32 m0, s52
	s_nop 0
	global_load_lds_dwordx4 v[24:25], off
	v_lshl_add_u64 v[24:25], v[250:251], 0, s[10:11]
	s_add_i32 m0, s52, 0x2000
	s_nop 0
	global_load_lds_dwordx4 v[24:25], off
	v_lshl_add_u64 v[24:25], v[252:253], 0, s[10:11]
	s_mov_b32 m0, s62
	s_nop 0
	global_load_lds_dwordx4 v[24:25], off
	v_lshl_add_u64 v[24:25], v[134:135], 0, s[10:11]
	s_mov_b32 m0, s63
	s_nop 0
	global_load_lds_dwordx4 v[24:25], off
	s_waitcnt lgkmcnt(0)
	s_waitcnt vmcnt(8)
	s_barrier
	s_setprio 1
	s_waitcnt lgkmcnt(0)
	v_mfma_scale_f32_16x16x128_f8f6f4 v[92:95], v[0:7], v[16:23], v[92:95], v139, v139 op_sel_hi:[0,0,0]
	v_mfma_scale_f32_16x16x128_f8f6f4 v[88:91], v[8:15], v[16:23], v[88:91], v139, v139 op_sel_hi:[0,0,0]
	v_mfma_scale_f32_16x16x128_f8f6f4 v[84:87], v[0:7], v[158:165], v[84:87], v139, v139 op_sel_hi:[0,0,0]
	v_mfma_scale_f32_16x16x128_f8f6f4 v[80:83], v[8:15], v[158:165], v[80:83], v139, v139 op_sel_hi:[0,0,0]
	v_mfma_scale_f32_16x16x128_f8f6f4 v[76:79], v[0:7], v[166:173], v[76:79], v139, v139 op_sel_hi:[0,0,0]
	v_mfma_scale_f32_16x16x128_f8f6f4 v[72:75], v[8:15], v[166:173], v[72:75], v139, v139 op_sel_hi:[0,0,0]
	v_mfma_scale_f32_16x16x128_f8f6f4 v[68:71], v[0:7], v[174:181], v[202:205], v139, v139 op_sel_hi:[0,0,0]
	v_mfma_scale_f32_16x16x128_f8f6f4 v[64:67], v[8:15], v[174:181], v[210:213], v139, v139 op_sel_hi:[0,0,0]
	v_mfma_scale_f32_16x16x128_f8f6f4 v[28:31], v[142:149], v[16:23], v[214:217], v139, v139 op_sel_hi:[0,0,0]
	v_mfma_scale_f32_16x16x128_f8f6f4 v[24:27], v[150:157], v[16:23], v[218:221], v139, v139 op_sel_hi:[0,0,0]
	v_mfma_scale_f32_16x16x128_f8f6f4 v[20:23], v[142:149], v[158:165], v[222:225], v139, v139 op_sel_hi:[0,0,0]
	v_mfma_scale_f32_16x16x128_f8f6f4 v[16:19], v[150:157], v[158:165], v[226:229], v139, v139 op_sel_hi:[0,0,0]
	v_mfma_scale_f32_16x16x128_f8f6f4 v[12:15], v[142:149], v[166:173], v[230:233], v139, v139 op_sel_hi:[0,0,0]
	v_mfma_scale_f32_16x16x128_f8f6f4 v[8:11], v[150:157], v[166:173], v[234:237], v139, v139 op_sel_hi:[0,0,0]
	v_mfma_scale_f32_16x16x128_f8f6f4 v[4:7], v[142:149], v[174:181], v[238:241], v139, v139 op_sel_hi:[0,0,0]
	v_mfma_scale_f32_16x16x128_f8f6f4 v[0:3], v[150:157], v[174:181], v[242:245], v139, v139 op_sel_hi:[0,0,0]
	s_setprio 0
	s_waitcnt vmcnt(8)
	s_barrier
	s_add_u32 s48, s48, 0x100
	s_addc_u32 s49, s49, 0
	s_cmp_ge_i32 s81, s0
	s_cbranch_scc1 .LBB0_1735
	s_mov_b32 s80, s81
	s_branch .LBB0_1724
